# GEMM loops: pre-barrier LDS-read wait split (last 4 of 16 fragment reads complete under the first 8 MFMAs) in all fp8 loops; bf16 loops keep Y reads in flight across the phase barrier
# speedup vs baseline: 1.0127x; 1.0127x over previous
.LBB0_219:
	s_waitcnt lgkmcnt(0)
	s_add_i32 s4, s92, 0x180
	s_add_i32 s5, s93, 0x180
	s_barrier
	s_setprio 1
	s_waitcnt lgkmcnt(7)
	v_mfma_f32_16x16x32_bf16 v[60:63], v[156:159], v[188:191], 0
	s_waitcnt lgkmcnt(6)
	v_mfma_f32_16x16x32_bf16 v[60:63], v[152:155], v[184:187], v[60:63]
	v_mfma_f32_16x16x32_bf16 v[56:59], v[148:151], v[188:191], 0
	s_nop 0
	v_mfma_f32_16x16x32_bf16 v[56:59], v[144:147], v[184:187], v[56:59]
	s_waitcnt lgkmcnt(5)
	v_mfma_f32_16x16x32_bf16 v[52:55], v[156:159], v[180:183], 0
	s_waitcnt lgkmcnt(4)
	v_mfma_f32_16x16x32_bf16 v[52:55], v[152:155], v[176:179], v[52:55]
	v_mfma_f32_16x16x32_bf16 v[48:51], v[148:151], v[180:183], 0
	s_nop 0
	v_mfma_f32_16x16x32_bf16 v[48:51], v[144:147], v[176:179], v[48:51]
	s_waitcnt lgkmcnt(3)
	v_mfma_f32_16x16x32_bf16 v[44:47], v[156:159], v[172:175], 0
	s_waitcnt lgkmcnt(2)
	v_mfma_f32_16x16x32_bf16 v[44:47], v[152:155], v[168:171], v[44:47]
	v_mfma_f32_16x16x32_bf16 v[40:43], v[148:151], v[172:175], 0
	s_nop 0
	v_mfma_f32_16x16x32_bf16 v[40:43], v[144:147], v[168:171], v[40:43]
	s_waitcnt lgkmcnt(1)
	v_mfma_f32_16x16x32_bf16 v[36:39], v[156:159], v[164:167], 0
	s_waitcnt lgkmcnt(0)
	v_mfma_f32_16x16x32_bf16 v[36:39], v[152:155], v[160:163], v[36:39]
	v_mfma_f32_16x16x32_bf16 v[32:35], v[148:151], v[164:167], 0
	s_nop 0
	v_mfma_f32_16x16x32_bf16 v[32:35], v[144:147], v[160:163], v[32:35]
	s_setprio 0
	s_setprio 1
	v_mfma_f32_16x16x32_bf16 v[28:31], v[140:143], v[188:191], 0
	s_nop 0
	v_mfma_f32_16x16x32_bf16 v[28:31], v[136:139], v[184:187], v[28:31]
	v_mfma_f32_16x16x32_bf16 v[24:27], v[132:135], v[188:191], 0
	s_nop 0
	v_mfma_f32_16x16x32_bf16 v[24:27], v[128:131], v[184:187], v[24:27]
	v_mfma_f32_16x16x32_bf16 v[20:23], v[140:143], v[180:183], 0
	s_nop 0
	v_mfma_f32_16x16x32_bf16 v[20:23], v[136:139], v[176:179], v[20:23]
	v_mfma_f32_16x16x32_bf16 v[16:19], v[132:135], v[180:183], 0
	s_nop 0
	v_mfma_f32_16x16x32_bf16 v[16:19], v[128:131], v[176:179], v[16:19]
	v_mfma_f32_16x16x32_bf16 v[12:15], v[140:143], v[172:175], 0
	s_nop 0
	v_mfma_f32_16x16x32_bf16 v[12:15], v[136:139], v[168:171], v[12:15]
	v_mfma_f32_16x16x32_bf16 v[8:11], v[132:135], v[172:175], 0
	s_nop 0
	v_mfma_f32_16x16x32_bf16 v[8:11], v[128:131], v[168:171], v[8:11]
	v_mfma_f32_16x16x32_bf16 v[4:7], v[140:143], v[164:167], 0
	s_nop 0
	v_mfma_f32_16x16x32_bf16 v[4:7], v[136:139], v[160:163], v[4:7]
	v_mfma_f32_16x16x32_bf16 v[0:3], v[132:135], v[164:167], 0
	s_nop 0
	v_mfma_f32_16x16x32_bf16 v[0:3], v[128:131], v[160:163], v[0:3]
	s_setprio 0
	s_barrier
	ds_read_b128 v[156:159], v211
	ds_read_b128 v[152:155], v212
	ds_read_b128 v[148:151], v213
	ds_read_b128 v[144:147], v214
	ds_read_b128 v[140:143], v215
	ds_read_b128 v[136:139], v216
	ds_read_b128 v[132:135], v217
	ds_read_b128 v[128:131], v218
	s_mov_b32 m0, s69
	s_add_i32 s14, s92, 0x20100
	buffer_load_dwordx4 v196, s[8:11], s14 offen lds
	s_add_i32 s14, s92, 0x30100
	s_mov_b32 m0, s70
	s_nop 0
	buffer_load_dwordx4 v196, s[8:11], s14 offen lds
	ds_read_b128 v[160:163], v219 offset:32768
	ds_read_b128 v[164:167], v219 offset:33792
	ds_read_b128 v[168:171], v219 offset:34816
	ds_read_b128 v[172:175], v219 offset:35840
	ds_read_b128 v[176:179], v219 offset:36864
	ds_read_b128 v[180:183], v219 offset:37888
	ds_read_b128 v[184:187], v219 offset:38912
	ds_read_b128 v[188:191], v219 offset:39936
	s_waitcnt vmcnt(8)
	s_waitcnt lgkmcnt(8)
	s_barrier
	s_setprio 1
	s_waitcnt lgkmcnt(7)
	v_mfma_f32_16x16x32_bf16 v[124:127], v[156:159], v[160:163], v[124:127]
	s_waitcnt lgkmcnt(6)
	v_mfma_f32_16x16x32_bf16 v[124:127], v[152:155], v[164:167], v[124:127]
	v_mfma_f32_16x16x32_bf16 v[120:123], v[148:151], v[160:163], v[120:123]
	s_nop 0
	v_mfma_f32_16x16x32_bf16 v[120:123], v[144:147], v[164:167], v[120:123]
	s_waitcnt lgkmcnt(5)
	v_mfma_f32_16x16x32_bf16 v[116:119], v[156:159], v[168:171], v[116:119]
	s_waitcnt lgkmcnt(4)
	v_mfma_f32_16x16x32_bf16 v[116:119], v[152:155], v[172:175], v[116:119]
	v_mfma_f32_16x16x32_bf16 v[112:115], v[148:151], v[168:171], v[112:115]
	s_nop 0
	v_mfma_f32_16x16x32_bf16 v[112:115], v[144:147], v[172:175], v[112:115]
	s_waitcnt lgkmcnt(3)
	v_mfma_f32_16x16x32_bf16 v[108:111], v[156:159], v[176:179], v[108:111]
	s_waitcnt lgkmcnt(2)
	v_mfma_f32_16x16x32_bf16 v[108:111], v[152:155], v[180:183], v[108:111]
	v_mfma_f32_16x16x32_bf16 v[104:107], v[148:151], v[176:179], v[104:107]
	s_nop 0
	v_mfma_f32_16x16x32_bf16 v[104:107], v[144:147], v[180:183], v[104:107]
	s_waitcnt lgkmcnt(1)
	v_mfma_f32_16x16x32_bf16 v[100:103], v[156:159], v[184:187], v[100:103]
	s_waitcnt lgkmcnt(0)
	v_mfma_f32_16x16x32_bf16 v[100:103], v[152:155], v[188:191], v[100:103]
	v_mfma_f32_16x16x32_bf16 v[96:99], v[148:151], v[184:187], v[96:99]
	s_nop 0
	v_mfma_f32_16x16x32_bf16 v[96:99], v[144:147], v[188:191], v[96:99]
	s_setprio 0
	s_setprio 1
	v_mfma_f32_16x16x32_bf16 v[92:95], v[140:143], v[160:163], v[92:95]
	s_nop 0
	v_mfma_f32_16x16x32_bf16 v[92:95], v[136:139], v[164:167], v[92:95]
	v_mfma_f32_16x16x32_bf16 v[88:91], v[132:135], v[160:163], v[88:91]
	s_nop 0
	v_mfma_f32_16x16x32_bf16 v[88:91], v[128:131], v[164:167], v[88:91]
	v_mfma_f32_16x16x32_bf16 v[84:87], v[140:143], v[168:171], v[84:87]
	s_nop 0
	v_mfma_f32_16x16x32_bf16 v[84:87], v[136:139], v[172:175], v[84:87]
	v_mfma_f32_16x16x32_bf16 v[80:83], v[132:135], v[168:171], v[80:83]
	s_nop 0
	v_mfma_f32_16x16x32_bf16 v[80:83], v[128:131], v[172:175], v[80:83]
	v_mfma_f32_16x16x32_bf16 v[76:79], v[140:143], v[176:179], v[76:79]
	s_nop 0
	v_mfma_f32_16x16x32_bf16 v[76:79], v[136:139], v[180:183], v[76:79]
	v_mfma_f32_16x16x32_bf16 v[72:75], v[132:135], v[176:179], v[72:75]
	s_nop 0
	v_mfma_f32_16x16x32_bf16 v[72:75], v[128:131], v[180:183], v[72:75]
	v_mfma_f32_16x16x32_bf16 v[68:71], v[140:143], v[184:187], v[68:71]
	s_nop 0
	v_mfma_f32_16x16x32_bf16 v[68:71], v[136:139], v[188:191], v[68:71]
	v_mfma_f32_16x16x32_bf16 v[64:67], v[132:135], v[184:187], v[64:67]
	s_nop 0
	v_mfma_f32_16x16x32_bf16 v[64:67], v[128:131], v[188:191], v[64:67]
	s_setprio 0
	s_barrier
	s_mov_b32 m0, s73
	s_mov_b32 s14, s10
	s_mov_b32 s15, s11
	buffer_load_dwordx4 v202, s[12:15], s5 offen lds
	s_add_i32 s5, s93, 0x80180
	s_mov_b32 m0, s74
	s_nop 0
	buffer_load_dwordx4 v202, s[12:15], s5 offen lds
	s_add_i32 s5, s93, 0x8180
	s_mov_b32 m0, s77
	s_nop 0
	buffer_load_dwordx4 v202, s[12:15], s5 offen lds
	s_add_i32 s5, s93, 0x88180
	s_mov_b32 m0, s78
	s_nop 0
	buffer_load_dwordx4 v202, s[12:15], s5 offen lds
	s_mov_b32 m0, s75
	s_nop 0
	buffer_load_dwordx4 v196, s[8:11], s4 offen lds
	s_add_i32 s4, s92, 0x10180
	s_mov_b32 m0, s76
	s_nop 0
	buffer_load_dwordx4 v196, s[8:11], s4 offen lds
	ds_read_b128 v[160:163], v219 offset:49152
	ds_read_b128 v[164:167], v219 offset:50176
	ds_read_b128 v[168:171], v219 offset:51200
	ds_read_b128 v[172:175], v219 offset:52224
	ds_read_b128 v[176:179], v219 offset:53248
	ds_read_b128 v[180:183], v219 offset:54272
	ds_read_b128 v[184:187], v219 offset:55296
	ds_read_b128 v[188:191], v219 offset:56320
	s_waitcnt vmcnt(8)
	s_waitcnt lgkmcnt(6)
	s_barrier
	s_setprio 1
	s_waitcnt lgkmcnt(7)
	v_mfma_f32_16x16x32_bf16 v[60:63], v[156:159], v[160:163], v[60:63]
	s_waitcnt lgkmcnt(6)
	v_mfma_f32_16x16x32_bf16 v[60:63], v[152:155], v[164:167], v[60:63]
	v_mfma_f32_16x16x32_bf16 v[56:59], v[148:151], v[160:163], v[56:59]
	s_nop 0
	v_mfma_f32_16x16x32_bf16 v[56:59], v[144:147], v[164:167], v[56:59]
	s_waitcnt lgkmcnt(5)
	v_mfma_f32_16x16x32_bf16 v[52:55], v[156:159], v[168:171], v[52:55]
	s_waitcnt lgkmcnt(4)
	v_mfma_f32_16x16x32_bf16 v[52:55], v[152:155], v[172:175], v[52:55]
	v_mfma_f32_16x16x32_bf16 v[48:51], v[148:151], v[168:171], v[48:51]
	s_nop 0
	v_mfma_f32_16x16x32_bf16 v[48:51], v[144:147], v[172:175], v[48:51]
	s_waitcnt lgkmcnt(3)
	v_mfma_f32_16x16x32_bf16 v[44:47], v[156:159], v[176:179], v[44:47]
	s_waitcnt lgkmcnt(2)
	v_mfma_f32_16x16x32_bf16 v[44:47], v[152:155], v[180:183], v[44:47]
	v_mfma_f32_16x16x32_bf16 v[40:43], v[148:151], v[176:179], v[40:43]
	s_nop 0
	v_mfma_f32_16x16x32_bf16 v[40:43], v[144:147], v[180:183], v[40:43]
	s_waitcnt lgkmcnt(1)
	v_mfma_f32_16x16x32_bf16 v[36:39], v[156:159], v[184:187], v[36:39]
	s_waitcnt lgkmcnt(0)
	v_mfma_f32_16x16x32_bf16 v[36:39], v[152:155], v[188:191], v[36:39]
	v_mfma_f32_16x16x32_bf16 v[32:35], v[148:151], v[184:187], v[32:35]
	s_nop 0
	v_mfma_f32_16x16x32_bf16 v[32:35], v[144:147], v[188:191], v[32:35]
	s_setprio 0
	s_setprio 1
	v_mfma_f32_16x16x32_bf16 v[28:31], v[140:143], v[160:163], v[28:31]
	s_nop 0
	v_mfma_f32_16x16x32_bf16 v[28:31], v[136:139], v[164:167], v[28:31]
	v_mfma_f32_16x16x32_bf16 v[24:27], v[132:135], v[160:163], v[24:27]
	s_nop 0
	v_mfma_f32_16x16x32_bf16 v[24:27], v[128:131], v[164:167], v[24:27]
	v_mfma_f32_16x16x32_bf16 v[20:23], v[140:143], v[168:171], v[20:23]
	s_nop 0
	v_mfma_f32_16x16x32_bf16 v[20:23], v[136:139], v[172:175], v[20:23]
	v_mfma_f32_16x16x32_bf16 v[16:19], v[132:135], v[168:171], v[16:19]
	s_nop 0
	v_mfma_f32_16x16x32_bf16 v[16:19], v[128:131], v[172:175], v[16:19]
	v_mfma_f32_16x16x32_bf16 v[12:15], v[140:143], v[176:179], v[12:15]
	s_nop 0
	v_mfma_f32_16x16x32_bf16 v[12:15], v[136:139], v[180:183], v[12:15]
	v_mfma_f32_16x16x32_bf16 v[8:11], v[132:135], v[176:179], v[8:11]
	s_nop 0
	v_mfma_f32_16x16x32_bf16 v[8:11], v[128:131], v[180:183], v[8:11]
	v_mfma_f32_16x16x32_bf16 v[4:7], v[140:143], v[184:187], v[4:7]
	s_nop 0
	v_mfma_f32_16x16x32_bf16 v[4:7], v[136:139], v[188:191], v[4:7]
	v_mfma_f32_16x16x32_bf16 v[0:3], v[132:135], v[184:187], v[0:3]
	s_nop 0
	v_mfma_f32_16x16x32_bf16 v[0:3], v[128:131], v[188:191], v[0:3]
	s_setprio 0
	s_barrier
	s_add_i32 s4, s92, 0x30180
	s_add_i32 s5, s93, 0x200
	s_mov_b32 s33, 0
.LBB0_220:
	ds_read_b128 v[128:131], v203
	ds_read_b128 v[132:135], v204
	ds_read_b128 v[136:139], v205
	ds_read_b128 v[140:143], v206
	ds_read_b128 v[144:147], v207
	ds_read_b128 v[148:151], v208
	ds_read_b128 v[152:155], v209
	ds_read_b128 v[156:159], v210
	s_add_i32 s66, s4, 0xfffd0080
	s_cmp_eq_u32 s33, 4
	s_cselect_b32 s66, s90, s66
	s_cselect_b32 s92, s91, s5
	s_add_i32 s67, s66, 0x80
	s_mov_b32 m0, s79
	s_add_i32 s93, s4, 0xffff0000
	buffer_load_dwordx4 v196, s[8:11], s93 offen lds
	s_mov_b32 m0, s81
	s_nop 0
	buffer_load_dwordx4 v196, s[8:11], s4 offen lds
	ds_read_b128 v[160:163], v219
	ds_read_b128 v[164:167], v219 offset:1024
	ds_read_b128 v[168:171], v219 offset:2048
	ds_read_b128 v[172:175], v219 offset:3072
	ds_read_b128 v[176:179], v219 offset:4096
	ds_read_b128 v[180:183], v219 offset:5120
	ds_read_b128 v[184:187], v219 offset:6144
	ds_read_b128 v[188:191], v219 offset:7168
	s_waitcnt vmcnt(8)
	s_waitcnt lgkmcnt(8)
	s_barrier
	s_setprio 1
	s_waitcnt lgkmcnt(7)
	v_mfma_f32_16x16x32_bf16 v[124:127], v[128:131], v[160:163], v[124:127]
	s_waitcnt lgkmcnt(6)
	v_mfma_f32_16x16x32_bf16 v[124:127], v[132:135], v[164:167], v[124:127]
	v_mfma_f32_16x16x32_bf16 v[120:123], v[136:139], v[160:163], v[120:123]
	s_nop 0
	v_mfma_f32_16x16x32_bf16 v[120:123], v[140:143], v[164:167], v[120:123]
	s_waitcnt lgkmcnt(5)
	v_mfma_f32_16x16x32_bf16 v[116:119], v[128:131], v[168:171], v[116:119]
	s_waitcnt lgkmcnt(4)
	v_mfma_f32_16x16x32_bf16 v[116:119], v[132:135], v[172:175], v[116:119]
	v_mfma_f32_16x16x32_bf16 v[112:115], v[136:139], v[168:171], v[112:115]
	s_nop 0
	v_mfma_f32_16x16x32_bf16 v[112:115], v[140:143], v[172:175], v[112:115]
	s_waitcnt lgkmcnt(3)
	v_mfma_f32_16x16x32_bf16 v[108:111], v[128:131], v[176:179], v[108:111]
	s_waitcnt lgkmcnt(2)
	v_mfma_f32_16x16x32_bf16 v[108:111], v[132:135], v[180:183], v[108:111]
	v_mfma_f32_16x16x32_bf16 v[104:107], v[136:139], v[176:179], v[104:107]
	s_nop 0
	v_mfma_f32_16x16x32_bf16 v[104:107], v[140:143], v[180:183], v[104:107]
	s_waitcnt lgkmcnt(1)
	v_mfma_f32_16x16x32_bf16 v[100:103], v[128:131], v[184:187], v[100:103]
	s_waitcnt lgkmcnt(0)
	v_mfma_f32_16x16x32_bf16 v[100:103], v[132:135], v[188:191], v[100:103]
	v_mfma_f32_16x16x32_bf16 v[96:99], v[136:139], v[184:187], v[96:99]
	s_nop 0
	v_mfma_f32_16x16x32_bf16 v[96:99], v[140:143], v[188:191], v[96:99]
	s_setprio 0
	s_setprio 1
	v_mfma_f32_16x16x32_bf16 v[92:95], v[144:147], v[160:163], v[92:95]
	s_nop 0
	v_mfma_f32_16x16x32_bf16 v[92:95], v[148:151], v[164:167], v[92:95]
	v_mfma_f32_16x16x32_bf16 v[88:91], v[152:155], v[160:163], v[88:91]
	s_nop 0
	v_mfma_f32_16x16x32_bf16 v[88:91], v[156:159], v[164:167], v[88:91]
	v_mfma_f32_16x16x32_bf16 v[84:87], v[144:147], v[168:171], v[84:87]
	s_nop 0
	v_mfma_f32_16x16x32_bf16 v[84:87], v[148:151], v[172:175], v[84:87]
	v_mfma_f32_16x16x32_bf16 v[80:83], v[152:155], v[168:171], v[80:83]
	s_nop 0
	v_mfma_f32_16x16x32_bf16 v[80:83], v[156:159], v[172:175], v[80:83]
	v_mfma_f32_16x16x32_bf16 v[76:79], v[144:147], v[176:179], v[76:79]
	s_nop 0
	v_mfma_f32_16x16x32_bf16 v[76:79], v[148:151], v[180:183], v[76:79]
	v_mfma_f32_16x16x32_bf16 v[72:75], v[152:155], v[176:179], v[72:75]
	s_nop 0
	v_mfma_f32_16x16x32_bf16 v[72:75], v[156:159], v[180:183], v[72:75]
	v_mfma_f32_16x16x32_bf16 v[68:71], v[144:147], v[184:187], v[68:71]
	s_nop 0
	v_mfma_f32_16x16x32_bf16 v[68:71], v[148:151], v[188:191], v[68:71]
	v_mfma_f32_16x16x32_bf16 v[64:67], v[152:155], v[184:187], v[64:67]
	s_nop 0
	v_mfma_f32_16x16x32_bf16 v[64:67], v[156:159], v[188:191], v[64:67]
	s_setprio 0
	s_barrier
	s_mov_b32 m0, s62
	s_add_i32 s93, s92, 0x80000
	buffer_load_dwordx4 v202, s[12:15], s92 offen lds
	s_mov_b32 m0, s63
	s_nop 0
	buffer_load_dwordx4 v202, s[12:15], s93 offen lds
	s_add_i32 s93, s92, 0x8000
	s_mov_b32 m0, s64
	s_nop 0
	buffer_load_dwordx4 v202, s[12:15], s93 offen lds
	s_add_i32 s93, s92, 0x88000
	s_mov_b32 m0, s65
	s_nop 0
	buffer_load_dwordx4 v202, s[12:15], s93 offen lds
	s_mov_b32 m0, s45
	s_add_i32 s93, s66, 0x10000
	buffer_load_dwordx4 v196, s[8:11], s66 offen lds
	s_mov_b32 m0, s68
	s_nop 0
	buffer_load_dwordx4 v196, s[8:11], s93 offen lds
	ds_read_b128 v[160:163], v219 offset:16384
	ds_read_b128 v[164:167], v219 offset:17408
	ds_read_b128 v[168:171], v219 offset:18432
	ds_read_b128 v[172:175], v219 offset:19456
	ds_read_b128 v[176:179], v219 offset:20480
	ds_read_b128 v[180:183], v219 offset:21504
	ds_read_b128 v[184:187], v219 offset:22528
	ds_read_b128 v[188:191], v219 offset:23552
	s_waitcnt vmcnt(8)
	s_waitcnt lgkmcnt(6)
	s_barrier
	s_setprio 1
	s_waitcnt lgkmcnt(7)
	v_mfma_f32_16x16x32_bf16 v[60:63], v[128:131], v[160:163], v[60:63]
	s_waitcnt lgkmcnt(6)
	v_mfma_f32_16x16x32_bf16 v[60:63], v[132:135], v[164:167], v[60:63]
	v_mfma_f32_16x16x32_bf16 v[56:59], v[136:139], v[160:163], v[56:59]
	s_nop 0
	v_mfma_f32_16x16x32_bf16 v[56:59], v[140:143], v[164:167], v[56:59]
	s_waitcnt lgkmcnt(5)
	v_mfma_f32_16x16x32_bf16 v[52:55], v[128:131], v[168:171], v[52:55]
	s_waitcnt lgkmcnt(4)
	v_mfma_f32_16x16x32_bf16 v[52:55], v[132:135], v[172:175], v[52:55]
	v_mfma_f32_16x16x32_bf16 v[48:51], v[136:139], v[168:171], v[48:51]
	s_nop 0
	v_mfma_f32_16x16x32_bf16 v[48:51], v[140:143], v[172:175], v[48:51]
	s_waitcnt lgkmcnt(3)
	v_mfma_f32_16x16x32_bf16 v[44:47], v[128:131], v[176:179], v[44:47]
	s_waitcnt lgkmcnt(2)
	v_mfma_f32_16x16x32_bf16 v[44:47], v[132:135], v[180:183], v[44:47]
	v_mfma_f32_16x16x32_bf16 v[40:43], v[136:139], v[176:179], v[40:43]
	s_nop 0
	v_mfma_f32_16x16x32_bf16 v[40:43], v[140:143], v[180:183], v[40:43]
	s_waitcnt lgkmcnt(1)
	v_mfma_f32_16x16x32_bf16 v[36:39], v[128:131], v[184:187], v[36:39]
	s_waitcnt lgkmcnt(0)
	v_mfma_f32_16x16x32_bf16 v[36:39], v[132:135], v[188:191], v[36:39]
	v_mfma_f32_16x16x32_bf16 v[32:35], v[136:139], v[184:187], v[32:35]
	s_nop 0
	v_mfma_f32_16x16x32_bf16 v[32:35], v[140:143], v[188:191], v[32:35]
	s_setprio 0
	s_setprio 1
	v_mfma_f32_16x16x32_bf16 v[28:31], v[144:147], v[160:163], v[28:31]
	s_nop 0
	v_mfma_f32_16x16x32_bf16 v[28:31], v[148:151], v[164:167], v[28:31]
	v_mfma_f32_16x16x32_bf16 v[24:27], v[152:155], v[160:163], v[24:27]
	s_nop 0
	v_mfma_f32_16x16x32_bf16 v[24:27], v[156:159], v[164:167], v[24:27]
	v_mfma_f32_16x16x32_bf16 v[20:23], v[144:147], v[168:171], v[20:23]
	s_nop 0
	v_mfma_f32_16x16x32_bf16 v[20:23], v[148:151], v[172:175], v[20:23]
	v_mfma_f32_16x16x32_bf16 v[16:19], v[152:155], v[168:171], v[16:19]
	s_nop 0
	v_mfma_f32_16x16x32_bf16 v[16:19], v[156:159], v[172:175], v[16:19]
	v_mfma_f32_16x16x32_bf16 v[12:15], v[144:147], v[176:179], v[12:15]
	s_nop 0
	v_mfma_f32_16x16x32_bf16 v[12:15], v[148:151], v[180:183], v[12:15]
	v_mfma_f32_16x16x32_bf16 v[8:11], v[152:155], v[176:179], v[8:11]
	s_nop 0
	v_mfma_f32_16x16x32_bf16 v[8:11], v[156:159], v[180:183], v[8:11]
	v_mfma_f32_16x16x32_bf16 v[4:7], v[144:147], v[184:187], v[4:7]
	s_nop 0
	v_mfma_f32_16x16x32_bf16 v[4:7], v[148:151], v[188:191], v[4:7]
	v_mfma_f32_16x16x32_bf16 v[0:3], v[152:155], v[184:187], v[0:3]
	s_nop 0
	v_mfma_f32_16x16x32_bf16 v[0:3], v[156:159], v[188:191], v[0:3]
	s_setprio 0
	s_barrier
	ds_read_b128 v[140:143], v211
	ds_read_b128 v[144:147], v212
	ds_read_b128 v[148:151], v213
	ds_read_b128 v[152:155], v214
	ds_read_b128 v[156:159], v215
	ds_read_b128 v[136:139], v216
	ds_read_b128 v[132:135], v217
	ds_read_b128 v[128:131], v218
	s_mov_b32 m0, s69
	s_add_i32 s93, s66, 0x20000
	buffer_load_dwordx4 v196, s[8:11], s93 offen lds
	s_add_i32 s93, s66, 0x30000
	s_mov_b32 m0, s70
	s_nop 0
	buffer_load_dwordx4 v196, s[8:11], s93 offen lds
	ds_read_b128 v[160:163], v219 offset:32768
	ds_read_b128 v[164:167], v219 offset:33792
	ds_read_b128 v[168:171], v219 offset:34816
	ds_read_b128 v[172:175], v219 offset:35840
	ds_read_b128 v[176:179], v219 offset:36864
	ds_read_b128 v[180:183], v219 offset:37888
	ds_read_b128 v[184:187], v219 offset:38912
	ds_read_b128 v[188:191], v219 offset:39936
	s_waitcnt vmcnt(8)
	s_waitcnt lgkmcnt(8)
	s_barrier
	s_setprio 1
	s_waitcnt lgkmcnt(7)
	v_mfma_f32_16x16x32_bf16 v[124:127], v[140:143], v[160:163], v[124:127]
	s_waitcnt lgkmcnt(6)
	v_mfma_f32_16x16x32_bf16 v[124:127], v[144:147], v[164:167], v[124:127]
	v_mfma_f32_16x16x32_bf16 v[120:123], v[148:151], v[160:163], v[120:123]
	s_nop 0
	v_mfma_f32_16x16x32_bf16 v[120:123], v[152:155], v[164:167], v[120:123]
	s_waitcnt lgkmcnt(5)
	v_mfma_f32_16x16x32_bf16 v[116:119], v[140:143], v[168:171], v[116:119]
	s_waitcnt lgkmcnt(4)
	v_mfma_f32_16x16x32_bf16 v[116:119], v[144:147], v[172:175], v[116:119]
	v_mfma_f32_16x16x32_bf16 v[112:115], v[148:151], v[168:171], v[112:115]
	s_nop 0
	v_mfma_f32_16x16x32_bf16 v[112:115], v[152:155], v[172:175], v[112:115]
	s_waitcnt lgkmcnt(3)
	v_mfma_f32_16x16x32_bf16 v[108:111], v[140:143], v[176:179], v[108:111]
	s_waitcnt lgkmcnt(2)
	v_mfma_f32_16x16x32_bf16 v[108:111], v[144:147], v[180:183], v[108:111]
	v_mfma_f32_16x16x32_bf16 v[104:107], v[148:151], v[176:179], v[104:107]
	s_nop 0
	v_mfma_f32_16x16x32_bf16 v[104:107], v[152:155], v[180:183], v[104:107]
	s_waitcnt lgkmcnt(1)
	v_mfma_f32_16x16x32_bf16 v[100:103], v[140:143], v[184:187], v[100:103]
	s_waitcnt lgkmcnt(0)
	v_mfma_f32_16x16x32_bf16 v[100:103], v[144:147], v[188:191], v[100:103]
	v_mfma_f32_16x16x32_bf16 v[96:99], v[148:151], v[184:187], v[96:99]
	s_nop 0
	v_mfma_f32_16x16x32_bf16 v[96:99], v[152:155], v[188:191], v[96:99]
	s_setprio 0
	s_setprio 1
	v_mfma_f32_16x16x32_bf16 v[92:95], v[156:159], v[160:163], v[92:95]
	s_nop 0
	v_mfma_f32_16x16x32_bf16 v[92:95], v[136:139], v[164:167], v[92:95]
	v_mfma_f32_16x16x32_bf16 v[88:91], v[132:135], v[160:163], v[88:91]
	s_nop 0
	v_mfma_f32_16x16x32_bf16 v[88:91], v[128:131], v[164:167], v[88:91]
	v_mfma_f32_16x16x32_bf16 v[84:87], v[156:159], v[168:171], v[84:87]
	s_nop 0
	v_mfma_f32_16x16x32_bf16 v[84:87], v[136:139], v[172:175], v[84:87]
	v_mfma_f32_16x16x32_bf16 v[80:83], v[132:135], v[168:171], v[80:83]
	s_nop 0
	v_mfma_f32_16x16x32_bf16 v[80:83], v[128:131], v[172:175], v[80:83]
	v_mfma_f32_16x16x32_bf16 v[76:79], v[156:159], v[176:179], v[76:79]
	s_nop 0
	v_mfma_f32_16x16x32_bf16 v[76:79], v[136:139], v[180:183], v[76:79]
	v_mfma_f32_16x16x32_bf16 v[72:75], v[132:135], v[176:179], v[72:75]
	s_nop 0
	v_mfma_f32_16x16x32_bf16 v[72:75], v[128:131], v[180:183], v[72:75]
	v_mfma_f32_16x16x32_bf16 v[68:71], v[156:159], v[184:187], v[68:71]
	s_nop 0
	v_mfma_f32_16x16x32_bf16 v[68:71], v[136:139], v[188:191], v[68:71]
	v_mfma_f32_16x16x32_bf16 v[64:67], v[132:135], v[184:187], v[64:67]
	s_nop 0
	v_mfma_f32_16x16x32_bf16 v[64:67], v[128:131], v[188:191], v[64:67]
	s_setprio 0
	s_barrier
	s_mov_b32 m0, s73
	s_add_i32 s93, s92, 0x80
	buffer_load_dwordx4 v202, s[12:15], s93 offen lds
	s_add_i32 s93, s92, 0x80080
	s_mov_b32 m0, s74
	s_add_i32 s66, s66, 0x10080
	buffer_load_dwordx4 v202, s[12:15], s93 offen lds
	s_add_i32 s93, s92, 0x8080
	s_mov_b32 m0, s77
	s_add_i32 s92, s92, 0x88080
	buffer_load_dwordx4 v202, s[12:15], s93 offen lds
	s_mov_b32 m0, s78
	s_nop 0
	buffer_load_dwordx4 v202, s[12:15], s92 offen lds
	s_mov_b32 m0, s75
	s_nop 0
	buffer_load_dwordx4 v196, s[8:11], s67 offen lds
	s_mov_b32 m0, s76
	s_nop 0
	buffer_load_dwordx4 v196, s[8:11], s66 offen lds
	ds_read_b128 v[160:163], v219 offset:49152
	ds_read_b128 v[164:167], v219 offset:50176
	ds_read_b128 v[168:171], v219 offset:51200
	ds_read_b128 v[172:175], v219 offset:52224
	ds_read_b128 v[176:179], v219 offset:53248
	ds_read_b128 v[180:183], v219 offset:54272
	ds_read_b128 v[184:187], v219 offset:55296
	ds_read_b128 v[188:191], v219 offset:56320
	s_waitcnt vmcnt(8)
	s_waitcnt lgkmcnt(6)
	s_barrier
	s_setprio 1
	s_waitcnt lgkmcnt(7)
	v_mfma_f32_16x16x32_bf16 v[60:63], v[140:143], v[160:163], v[60:63]
	s_waitcnt lgkmcnt(6)
	v_mfma_f32_16x16x32_bf16 v[60:63], v[144:147], v[164:167], v[60:63]
	v_mfma_f32_16x16x32_bf16 v[56:59], v[148:151], v[160:163], v[56:59]
	s_nop 0
	v_mfma_f32_16x16x32_bf16 v[56:59], v[152:155], v[164:167], v[56:59]
	s_waitcnt lgkmcnt(5)
	v_mfma_f32_16x16x32_bf16 v[52:55], v[140:143], v[168:171], v[52:55]
	s_waitcnt lgkmcnt(4)
	v_mfma_f32_16x16x32_bf16 v[52:55], v[144:147], v[172:175], v[52:55]
	v_mfma_f32_16x16x32_bf16 v[48:51], v[148:151], v[168:171], v[48:51]
	s_nop 0
	v_mfma_f32_16x16x32_bf16 v[48:51], v[152:155], v[172:175], v[48:51]
	s_waitcnt lgkmcnt(3)
	v_mfma_f32_16x16x32_bf16 v[44:47], v[140:143], v[176:179], v[44:47]
	s_waitcnt lgkmcnt(2)
	v_mfma_f32_16x16x32_bf16 v[44:47], v[144:147], v[180:183], v[44:47]
	v_mfma_f32_16x16x32_bf16 v[40:43], v[148:151], v[176:179], v[40:43]
	s_nop 0
	v_mfma_f32_16x16x32_bf16 v[40:43], v[152:155], v[180:183], v[40:43]
	s_waitcnt lgkmcnt(1)
	v_mfma_f32_16x16x32_bf16 v[36:39], v[140:143], v[184:187], v[36:39]
	s_waitcnt lgkmcnt(0)
	v_mfma_f32_16x16x32_bf16 v[36:39], v[144:147], v[188:191], v[36:39]
	v_mfma_f32_16x16x32_bf16 v[32:35], v[148:151], v[184:187], v[32:35]
	s_nop 0
	v_mfma_f32_16x16x32_bf16 v[32:35], v[152:155], v[188:191], v[32:35]
	s_setprio 0
	s_setprio 1
	v_mfma_f32_16x16x32_bf16 v[28:31], v[156:159], v[160:163], v[28:31]
	s_nop 0
	v_mfma_f32_16x16x32_bf16 v[28:31], v[136:139], v[164:167], v[28:31]
	v_mfma_f32_16x16x32_bf16 v[24:27], v[132:135], v[160:163], v[24:27]
	s_nop 0
	v_mfma_f32_16x16x32_bf16 v[24:27], v[128:131], v[164:167], v[24:27]
	v_mfma_f32_16x16x32_bf16 v[20:23], v[156:159], v[168:171], v[20:23]
	s_nop 0
	v_mfma_f32_16x16x32_bf16 v[20:23], v[136:139], v[172:175], v[20:23]
	v_mfma_f32_16x16x32_bf16 v[16:19], v[132:135], v[168:171], v[16:19]
	s_nop 0
	v_mfma_f32_16x16x32_bf16 v[16:19], v[128:131], v[172:175], v[16:19]
	v_mfma_f32_16x16x32_bf16 v[12:15], v[156:159], v[176:179], v[12:15]
	s_nop 0
	v_mfma_f32_16x16x32_bf16 v[12:15], v[136:139], v[180:183], v[12:15]
	v_mfma_f32_16x16x32_bf16 v[8:11], v[132:135], v[176:179], v[8:11]
	s_nop 0
	v_mfma_f32_16x16x32_bf16 v[8:11], v[128:131], v[180:183], v[8:11]
	v_mfma_f32_16x16x32_bf16 v[4:7], v[156:159], v[184:187], v[4:7]
	s_nop 0
	v_mfma_f32_16x16x32_bf16 v[4:7], v[136:139], v[188:191], v[4:7]
	v_mfma_f32_16x16x32_bf16 v[0:3], v[132:135], v[184:187], v[0:3]
	s_nop 0
	v_mfma_f32_16x16x32_bf16 v[0:3], v[128:131], v[188:191], v[0:3]
	s_setprio 0
	s_barrier
	s_add_i32 s33, s33, 2
	s_addk_i32 s4, 0x100
	s_addk_i32 s5, 0x100
	s_cmp_gt_u32 s33, 5
	s_cbranch_scc0 .LBB0_220
	s_and_b64 vcc, exec, s[16:17]
	s_cbranch_vccz .LBB0_223
	s_barrier

.LBB0_253:
	s_waitcnt lgkmcnt(0)
	s_add_i32 s33, s91, 0x180
	s_add_i32 s42, s90, 0x180
	s_barrier
	s_setprio 1
	s_waitcnt lgkmcnt(7)
	v_mfma_f32_16x16x32_bf16 v[60:63], v[156:159], v[188:191], 0
	s_waitcnt lgkmcnt(6)
	v_mfma_f32_16x16x32_bf16 v[60:63], v[152:155], v[184:187], v[60:63]
	v_mfma_f32_16x16x32_bf16 v[56:59], v[148:151], v[188:191], 0
	s_nop 0
	v_mfma_f32_16x16x32_bf16 v[56:59], v[144:147], v[184:187], v[56:59]
	s_waitcnt lgkmcnt(5)
	v_mfma_f32_16x16x32_bf16 v[52:55], v[156:159], v[180:183], 0
	s_waitcnt lgkmcnt(4)
	v_mfma_f32_16x16x32_bf16 v[52:55], v[152:155], v[176:179], v[52:55]
	v_mfma_f32_16x16x32_bf16 v[48:51], v[148:151], v[180:183], 0
	s_nop 0
	v_mfma_f32_16x16x32_bf16 v[48:51], v[144:147], v[176:179], v[48:51]
	s_waitcnt lgkmcnt(3)
	v_mfma_f32_16x16x32_bf16 v[44:47], v[156:159], v[172:175], 0
	s_waitcnt lgkmcnt(2)
	v_mfma_f32_16x16x32_bf16 v[44:47], v[152:155], v[168:171], v[44:47]
	v_mfma_f32_16x16x32_bf16 v[40:43], v[148:151], v[172:175], 0
	s_nop 0
	v_mfma_f32_16x16x32_bf16 v[40:43], v[144:147], v[168:171], v[40:43]
	s_waitcnt lgkmcnt(1)
	v_mfma_f32_16x16x32_bf16 v[36:39], v[156:159], v[164:167], 0
	s_waitcnt lgkmcnt(0)
	v_mfma_f32_16x16x32_bf16 v[36:39], v[152:155], v[160:163], v[36:39]
	v_mfma_f32_16x16x32_bf16 v[32:35], v[148:151], v[164:167], 0
	s_nop 0
	v_mfma_f32_16x16x32_bf16 v[32:35], v[144:147], v[160:163], v[32:35]
	s_setprio 0
	s_setprio 1
	v_mfma_f32_16x16x32_bf16 v[28:31], v[140:143], v[188:191], 0
	s_nop 0
	v_mfma_f32_16x16x32_bf16 v[28:31], v[136:139], v[184:187], v[28:31]
	v_mfma_f32_16x16x32_bf16 v[24:27], v[132:135], v[188:191], 0
	s_nop 0
	v_mfma_f32_16x16x32_bf16 v[24:27], v[128:131], v[184:187], v[24:27]
	v_mfma_f32_16x16x32_bf16 v[20:23], v[140:143], v[180:183], 0
	s_nop 0
	v_mfma_f32_16x16x32_bf16 v[20:23], v[136:139], v[176:179], v[20:23]
	v_mfma_f32_16x16x32_bf16 v[16:19], v[132:135], v[180:183], 0
	s_nop 0
	v_mfma_f32_16x16x32_bf16 v[16:19], v[128:131], v[176:179], v[16:19]
	v_mfma_f32_16x16x32_bf16 v[12:15], v[140:143], v[172:175], 0
	s_nop 0
	v_mfma_f32_16x16x32_bf16 v[12:15], v[136:139], v[168:171], v[12:15]
	v_mfma_f32_16x16x32_bf16 v[8:11], v[132:135], v[172:175], 0
	s_nop 0
	v_mfma_f32_16x16x32_bf16 v[8:11], v[128:131], v[168:171], v[8:11]
	v_mfma_f32_16x16x32_bf16 v[4:7], v[140:143], v[164:167], 0
	s_nop 0
	v_mfma_f32_16x16x32_bf16 v[4:7], v[136:139], v[160:163], v[4:7]
	v_mfma_f32_16x16x32_bf16 v[0:3], v[132:135], v[164:167], 0
	s_nop 0
	v_mfma_f32_16x16x32_bf16 v[0:3], v[128:131], v[160:163], v[0:3]
	s_setprio 0
	s_barrier
	ds_read_b128 v[156:159], v203
	ds_read_b128 v[152:155], v204
	ds_read_b128 v[148:151], v205
	ds_read_b128 v[144:147], v206
	ds_read_b128 v[140:143], v207
	ds_read_b128 v[136:139], v208
	ds_read_b128 v[132:135], v209
	ds_read_b128 v[128:131], v210
	s_mov_b32 m0, s69
	s_add_i32 s10, s91, 0x20100
	buffer_load_dwordx4 v196, s[4:7], s10 offen lds
	s_add_i32 s10, s91, 0x30100
	s_mov_b32 m0, s70
	s_nop 0
	buffer_load_dwordx4 v196, s[4:7], s10 offen lds
	ds_read_b128 v[160:163], v197 offset:32768
	ds_read_b128 v[164:167], v197 offset:33792
	ds_read_b128 v[168:171], v197 offset:34816
	ds_read_b128 v[172:175], v197 offset:35840
	ds_read_b128 v[176:179], v197 offset:36864
	ds_read_b128 v[180:183], v197 offset:37888
	ds_read_b128 v[184:187], v197 offset:38912
	ds_read_b128 v[188:191], v197 offset:39936
	s_waitcnt vmcnt(8)
	s_waitcnt lgkmcnt(8)
	s_barrier
	s_setprio 1
	s_waitcnt lgkmcnt(7)
	v_mfma_f32_16x16x32_bf16 v[124:127], v[156:159], v[160:163], v[124:127]
	s_waitcnt lgkmcnt(6)
	v_mfma_f32_16x16x32_bf16 v[124:127], v[152:155], v[164:167], v[124:127]
	v_mfma_f32_16x16x32_bf16 v[120:123], v[148:151], v[160:163], v[120:123]
	s_nop 0
	v_mfma_f32_16x16x32_bf16 v[120:123], v[144:147], v[164:167], v[120:123]
	s_waitcnt lgkmcnt(5)
	v_mfma_f32_16x16x32_bf16 v[116:119], v[156:159], v[168:171], v[116:119]
	s_waitcnt lgkmcnt(4)
	v_mfma_f32_16x16x32_bf16 v[116:119], v[152:155], v[172:175], v[116:119]
	v_mfma_f32_16x16x32_bf16 v[112:115], v[148:151], v[168:171], v[112:115]
	s_nop 0
	v_mfma_f32_16x16x32_bf16 v[112:115], v[144:147], v[172:175], v[112:115]
	s_waitcnt lgkmcnt(3)
	v_mfma_f32_16x16x32_bf16 v[108:111], v[156:159], v[176:179], v[108:111]
	s_waitcnt lgkmcnt(2)
	v_mfma_f32_16x16x32_bf16 v[108:111], v[152:155], v[180:183], v[108:111]
	v_mfma_f32_16x16x32_bf16 v[104:107], v[148:151], v[176:179], v[104:107]
	s_nop 0
	v_mfma_f32_16x16x32_bf16 v[104:107], v[144:147], v[180:183], v[104:107]
	s_waitcnt lgkmcnt(1)
	v_mfma_f32_16x16x32_bf16 v[100:103], v[156:159], v[184:187], v[100:103]
	s_waitcnt lgkmcnt(0)
	v_mfma_f32_16x16x32_bf16 v[100:103], v[152:155], v[188:191], v[100:103]
	v_mfma_f32_16x16x32_bf16 v[96:99], v[148:151], v[184:187], v[96:99]
	s_nop 0
	v_mfma_f32_16x16x32_bf16 v[96:99], v[144:147], v[188:191], v[96:99]
	s_setprio 0
	s_setprio 1
	v_mfma_f32_16x16x32_bf16 v[92:95], v[140:143], v[160:163], v[92:95]
	s_nop 0
	v_mfma_f32_16x16x32_bf16 v[92:95], v[136:139], v[164:167], v[92:95]
	v_mfma_f32_16x16x32_bf16 v[88:91], v[132:135], v[160:163], v[88:91]
	s_nop 0
	v_mfma_f32_16x16x32_bf16 v[88:91], v[128:131], v[164:167], v[88:91]
	v_mfma_f32_16x16x32_bf16 v[84:87], v[140:143], v[168:171], v[84:87]
	s_nop 0
	v_mfma_f32_16x16x32_bf16 v[84:87], v[136:139], v[172:175], v[84:87]
	v_mfma_f32_16x16x32_bf16 v[80:83], v[132:135], v[168:171], v[80:83]
	s_nop 0
	v_mfma_f32_16x16x32_bf16 v[80:83], v[128:131], v[172:175], v[80:83]
	v_mfma_f32_16x16x32_bf16 v[76:79], v[140:143], v[176:179], v[76:79]
	s_nop 0
	v_mfma_f32_16x16x32_bf16 v[76:79], v[136:139], v[180:183], v[76:79]
	v_mfma_f32_16x16x32_bf16 v[72:75], v[132:135], v[176:179], v[72:75]
	s_nop 0
	v_mfma_f32_16x16x32_bf16 v[72:75], v[128:131], v[180:183], v[72:75]
	v_mfma_f32_16x16x32_bf16 v[68:71], v[140:143], v[184:187], v[68:71]
	s_nop 0
	v_mfma_f32_16x16x32_bf16 v[68:71], v[136:139], v[188:191], v[68:71]
	v_mfma_f32_16x16x32_bf16 v[64:67], v[132:135], v[184:187], v[64:67]
	s_nop 0
	v_mfma_f32_16x16x32_bf16 v[64:67], v[128:131], v[188:191], v[64:67]
	s_setprio 0
	s_barrier
	s_mov_b32 m0, s72
	s_mov_b32 s10, s6
	s_mov_b32 s11, s7
	buffer_load_dwordx4 v192, s[8:11], s42 offen lds
	s_add_i32 s42, s90, 0x20180
	s_mov_b32 m0, s73
	s_nop 0
	buffer_load_dwordx4 v192, s[8:11], s42 offen lds
	s_add_i32 s42, s90, 0x2180
	s_mov_b32 m0, s76
	s_nop 0
	buffer_load_dwordx4 v192, s[8:11], s42 offen lds
	s_add_i32 s42, s90, 0x22180
	s_mov_b32 m0, s77
	s_nop 0
	buffer_load_dwordx4 v192, s[8:11], s42 offen lds
	s_mov_b32 m0, s74
	s_nop 0
	buffer_load_dwordx4 v196, s[4:7], s33 offen lds
	s_add_i32 s33, s91, 0x10180
	s_mov_b32 m0, s75
	s_nop 0
	buffer_load_dwordx4 v196, s[4:7], s33 offen lds
	ds_read_b128 v[160:163], v197 offset:49152
	ds_read_b128 v[164:167], v197 offset:50176
	ds_read_b128 v[168:171], v197 offset:51200
	ds_read_b128 v[172:175], v197 offset:52224
	ds_read_b128 v[176:179], v197 offset:53248
	ds_read_b128 v[180:183], v197 offset:54272
	ds_read_b128 v[184:187], v197 offset:55296
	ds_read_b128 v[188:191], v197 offset:56320
	s_waitcnt vmcnt(8)
	s_waitcnt lgkmcnt(6)
	s_barrier
	s_setprio 1
	s_waitcnt lgkmcnt(7)
	v_mfma_f32_16x16x32_bf16 v[60:63], v[156:159], v[160:163], v[60:63]
	s_waitcnt lgkmcnt(6)
	v_mfma_f32_16x16x32_bf16 v[60:63], v[152:155], v[164:167], v[60:63]
	v_mfma_f32_16x16x32_bf16 v[56:59], v[148:151], v[160:163], v[56:59]
	s_nop 0
	v_mfma_f32_16x16x32_bf16 v[56:59], v[144:147], v[164:167], v[56:59]
	s_waitcnt lgkmcnt(5)
	v_mfma_f32_16x16x32_bf16 v[52:55], v[156:159], v[168:171], v[52:55]
	s_waitcnt lgkmcnt(4)
	v_mfma_f32_16x16x32_bf16 v[52:55], v[152:155], v[172:175], v[52:55]
	v_mfma_f32_16x16x32_bf16 v[48:51], v[148:151], v[168:171], v[48:51]
	s_nop 0
	v_mfma_f32_16x16x32_bf16 v[48:51], v[144:147], v[172:175], v[48:51]
	s_waitcnt lgkmcnt(3)
	v_mfma_f32_16x16x32_bf16 v[44:47], v[156:159], v[176:179], v[44:47]
	s_waitcnt lgkmcnt(2)
	v_mfma_f32_16x16x32_bf16 v[44:47], v[152:155], v[180:183], v[44:47]
	v_mfma_f32_16x16x32_bf16 v[40:43], v[148:151], v[176:179], v[40:43]
	s_nop 0
	v_mfma_f32_16x16x32_bf16 v[40:43], v[144:147], v[180:183], v[40:43]
	s_waitcnt lgkmcnt(1)
	v_mfma_f32_16x16x32_bf16 v[36:39], v[156:159], v[184:187], v[36:39]
	s_waitcnt lgkmcnt(0)
	v_mfma_f32_16x16x32_bf16 v[36:39], v[152:155], v[188:191], v[36:39]
	v_mfma_f32_16x16x32_bf16 v[32:35], v[148:151], v[184:187], v[32:35]
	s_nop 0
	v_mfma_f32_16x16x32_bf16 v[32:35], v[144:147], v[188:191], v[32:35]
	s_setprio 0
	s_setprio 1
	v_mfma_f32_16x16x32_bf16 v[28:31], v[140:143], v[160:163], v[28:31]
	s_nop 0
	v_mfma_f32_16x16x32_bf16 v[28:31], v[136:139], v[164:167], v[28:31]
	v_mfma_f32_16x16x32_bf16 v[24:27], v[132:135], v[160:163], v[24:27]
	s_nop 0
	v_mfma_f32_16x16x32_bf16 v[24:27], v[128:131], v[164:167], v[24:27]
	v_mfma_f32_16x16x32_bf16 v[20:23], v[140:143], v[168:171], v[20:23]
	s_nop 0
	v_mfma_f32_16x16x32_bf16 v[20:23], v[136:139], v[172:175], v[20:23]
	v_mfma_f32_16x16x32_bf16 v[16:19], v[132:135], v[168:171], v[16:19]
	s_nop 0
	v_mfma_f32_16x16x32_bf16 v[16:19], v[128:131], v[172:175], v[16:19]
	v_mfma_f32_16x16x32_bf16 v[12:15], v[140:143], v[176:179], v[12:15]
	s_nop 0
	v_mfma_f32_16x16x32_bf16 v[12:15], v[136:139], v[180:183], v[12:15]
	v_mfma_f32_16x16x32_bf16 v[8:11], v[132:135], v[176:179], v[8:11]
	s_nop 0
	v_mfma_f32_16x16x32_bf16 v[8:11], v[128:131], v[180:183], v[8:11]
	v_mfma_f32_16x16x32_bf16 v[4:7], v[140:143], v[184:187], v[4:7]
	s_nop 0
	v_mfma_f32_16x16x32_bf16 v[4:7], v[136:139], v[188:191], v[4:7]
	v_mfma_f32_16x16x32_bf16 v[0:3], v[132:135], v[184:187], v[0:3]
	s_nop 0
	v_mfma_f32_16x16x32_bf16 v[0:3], v[128:131], v[188:191], v[0:3]
	s_setprio 0
	s_barrier
	s_add_i32 s33, s91, 0x30180
	s_add_i32 s42, s90, 0x200
	s_mov_b32 s43, 0
.LBB0_254:
	ds_read_b128 v[128:131], v193
	ds_read_b128 v[132:135], v194
	ds_read_b128 v[136:139], v195
	ds_read_b128 v[140:143], v198
	ds_read_b128 v[144:147], v199
	ds_read_b128 v[148:151], v200
	ds_read_b128 v[152:155], v201
	ds_read_b128 v[156:159], v202
	s_add_i32 s66, s33, 0xfffd0080
	s_cmp_eq_u32 s43, 4
	s_cselect_b32 s66, s88, s66
	s_cselect_b32 s90, s89, s42
	s_add_i32 s67, s66, 0x80
	s_mov_b32 m0, s78
	s_add_i32 s91, s33, 0xffff0000
	buffer_load_dwordx4 v196, s[4:7], s91 offen lds
	s_mov_b32 m0, s79
	s_nop 0
	buffer_load_dwordx4 v196, s[4:7], s33 offen lds
	ds_read_b128 v[160:163], v197
	ds_read_b128 v[164:167], v197 offset:1024
	ds_read_b128 v[168:171], v197 offset:2048
	ds_read_b128 v[172:175], v197 offset:3072
	ds_read_b128 v[176:179], v197 offset:4096
	ds_read_b128 v[180:183], v197 offset:5120
	ds_read_b128 v[184:187], v197 offset:6144
	ds_read_b128 v[188:191], v197 offset:7168
	s_waitcnt vmcnt(8)
	s_waitcnt lgkmcnt(8)
	s_barrier
	s_setprio 1
	s_waitcnt lgkmcnt(7)
	v_mfma_f32_16x16x32_bf16 v[124:127], v[128:131], v[160:163], v[124:127]
	s_waitcnt lgkmcnt(6)
	v_mfma_f32_16x16x32_bf16 v[124:127], v[132:135], v[164:167], v[124:127]
	v_mfma_f32_16x16x32_bf16 v[120:123], v[136:139], v[160:163], v[120:123]
	s_nop 0
	v_mfma_f32_16x16x32_bf16 v[120:123], v[140:143], v[164:167], v[120:123]
	s_waitcnt lgkmcnt(5)
	v_mfma_f32_16x16x32_bf16 v[116:119], v[128:131], v[168:171], v[116:119]
	s_waitcnt lgkmcnt(4)
	v_mfma_f32_16x16x32_bf16 v[116:119], v[132:135], v[172:175], v[116:119]
	v_mfma_f32_16x16x32_bf16 v[112:115], v[136:139], v[168:171], v[112:115]
	s_nop 0
	v_mfma_f32_16x16x32_bf16 v[112:115], v[140:143], v[172:175], v[112:115]
	s_waitcnt lgkmcnt(3)
	v_mfma_f32_16x16x32_bf16 v[108:111], v[128:131], v[176:179], v[108:111]
	s_waitcnt lgkmcnt(2)
	v_mfma_f32_16x16x32_bf16 v[108:111], v[132:135], v[180:183], v[108:111]
	v_mfma_f32_16x16x32_bf16 v[104:107], v[136:139], v[176:179], v[104:107]
	s_nop 0
	v_mfma_f32_16x16x32_bf16 v[104:107], v[140:143], v[180:183], v[104:107]
	s_waitcnt lgkmcnt(1)
	v_mfma_f32_16x16x32_bf16 v[100:103], v[128:131], v[184:187], v[100:103]
	s_waitcnt lgkmcnt(0)
	v_mfma_f32_16x16x32_bf16 v[100:103], v[132:135], v[188:191], v[100:103]
	v_mfma_f32_16x16x32_bf16 v[96:99], v[136:139], v[184:187], v[96:99]
	s_nop 0
	v_mfma_f32_16x16x32_bf16 v[96:99], v[140:143], v[188:191], v[96:99]
	s_setprio 0
	s_setprio 1
	v_mfma_f32_16x16x32_bf16 v[92:95], v[144:147], v[160:163], v[92:95]
	s_nop 0
	v_mfma_f32_16x16x32_bf16 v[92:95], v[148:151], v[164:167], v[92:95]
	v_mfma_f32_16x16x32_bf16 v[88:91], v[152:155], v[160:163], v[88:91]
	s_nop 0
	v_mfma_f32_16x16x32_bf16 v[88:91], v[156:159], v[164:167], v[88:91]
	v_mfma_f32_16x16x32_bf16 v[84:87], v[144:147], v[168:171], v[84:87]
	s_nop 0
	v_mfma_f32_16x16x32_bf16 v[84:87], v[148:151], v[172:175], v[84:87]
	v_mfma_f32_16x16x32_bf16 v[80:83], v[152:155], v[168:171], v[80:83]
	s_nop 0
	v_mfma_f32_16x16x32_bf16 v[80:83], v[156:159], v[172:175], v[80:83]
	v_mfma_f32_16x16x32_bf16 v[76:79], v[144:147], v[176:179], v[76:79]
	s_nop 0
	v_mfma_f32_16x16x32_bf16 v[76:79], v[148:151], v[180:183], v[76:79]
	v_mfma_f32_16x16x32_bf16 v[72:75], v[152:155], v[176:179], v[72:75]
	s_nop 0
	v_mfma_f32_16x16x32_bf16 v[72:75], v[156:159], v[180:183], v[72:75]
	v_mfma_f32_16x16x32_bf16 v[68:71], v[144:147], v[184:187], v[68:71]
	s_nop 0
	v_mfma_f32_16x16x32_bf16 v[68:71], v[148:151], v[188:191], v[68:71]
	v_mfma_f32_16x16x32_bf16 v[64:67], v[152:155], v[184:187], v[64:67]
	s_nop 0
	v_mfma_f32_16x16x32_bf16 v[64:67], v[156:159], v[188:191], v[64:67]
	s_setprio 0
	s_barrier
	s_mov_b32 m0, s62
	s_add_i32 s91, s90, 0x20000
	buffer_load_dwordx4 v192, s[8:11], s90 offen lds
	s_mov_b32 m0, s63
	s_nop 0
	buffer_load_dwordx4 v192, s[8:11], s91 offen lds
	s_add_i32 s91, s90, 0x2000
	s_mov_b32 m0, s64
	s_nop 0
	buffer_load_dwordx4 v192, s[8:11], s91 offen lds
	s_add_i32 s91, s90, 0x22000
	s_mov_b32 m0, s65
	s_nop 0
	buffer_load_dwordx4 v192, s[8:11], s91 offen lds
	s_mov_b32 m0, s47
	s_add_i32 s91, s66, 0x10000
	buffer_load_dwordx4 v196, s[4:7], s66 offen lds
	s_mov_b32 m0, s68
	s_nop 0
	buffer_load_dwordx4 v196, s[4:7], s91 offen lds
	ds_read_b128 v[160:163], v197 offset:16384
	ds_read_b128 v[164:167], v197 offset:17408
	ds_read_b128 v[168:171], v197 offset:18432
	ds_read_b128 v[172:175], v197 offset:19456
	ds_read_b128 v[176:179], v197 offset:20480
	ds_read_b128 v[180:183], v197 offset:21504
	ds_read_b128 v[184:187], v197 offset:22528
	ds_read_b128 v[188:191], v197 offset:23552
	s_waitcnt vmcnt(8)
	s_waitcnt lgkmcnt(6)
	s_barrier
	s_setprio 1
	s_waitcnt lgkmcnt(7)
	v_mfma_f32_16x16x32_bf16 v[60:63], v[128:131], v[160:163], v[60:63]
	s_waitcnt lgkmcnt(6)
	v_mfma_f32_16x16x32_bf16 v[60:63], v[132:135], v[164:167], v[60:63]
	v_mfma_f32_16x16x32_bf16 v[56:59], v[136:139], v[160:163], v[56:59]
	s_nop 0
	v_mfma_f32_16x16x32_bf16 v[56:59], v[140:143], v[164:167], v[56:59]
	s_waitcnt lgkmcnt(5)
	v_mfma_f32_16x16x32_bf16 v[52:55], v[128:131], v[168:171], v[52:55]
	s_waitcnt lgkmcnt(4)
	v_mfma_f32_16x16x32_bf16 v[52:55], v[132:135], v[172:175], v[52:55]
	v_mfma_f32_16x16x32_bf16 v[48:51], v[136:139], v[168:171], v[48:51]
	s_nop 0
	v_mfma_f32_16x16x32_bf16 v[48:51], v[140:143], v[172:175], v[48:51]
	s_waitcnt lgkmcnt(3)
	v_mfma_f32_16x16x32_bf16 v[44:47], v[128:131], v[176:179], v[44:47]
	s_waitcnt lgkmcnt(2)
	v_mfma_f32_16x16x32_bf16 v[44:47], v[132:135], v[180:183], v[44:47]
	v_mfma_f32_16x16x32_bf16 v[40:43], v[136:139], v[176:179], v[40:43]
	s_nop 0
	v_mfma_f32_16x16x32_bf16 v[40:43], v[140:143], v[180:183], v[40:43]
	s_waitcnt lgkmcnt(1)
	v_mfma_f32_16x16x32_bf16 v[36:39], v[128:131], v[184:187], v[36:39]
	s_waitcnt lgkmcnt(0)
	v_mfma_f32_16x16x32_bf16 v[36:39], v[132:135], v[188:191], v[36:39]
	v_mfma_f32_16x16x32_bf16 v[32:35], v[136:139], v[184:187], v[32:35]
	s_nop 0
	v_mfma_f32_16x16x32_bf16 v[32:35], v[140:143], v[188:191], v[32:35]
	s_setprio 0
	s_setprio 1
	v_mfma_f32_16x16x32_bf16 v[28:31], v[144:147], v[160:163], v[28:31]
	s_nop 0
	v_mfma_f32_16x16x32_bf16 v[28:31], v[148:151], v[164:167], v[28:31]
	v_mfma_f32_16x16x32_bf16 v[24:27], v[152:155], v[160:163], v[24:27]
	s_nop 0
	v_mfma_f32_16x16x32_bf16 v[24:27], v[156:159], v[164:167], v[24:27]
	v_mfma_f32_16x16x32_bf16 v[20:23], v[144:147], v[168:171], v[20:23]
	s_nop 0
	v_mfma_f32_16x16x32_bf16 v[20:23], v[148:151], v[172:175], v[20:23]
	v_mfma_f32_16x16x32_bf16 v[16:19], v[152:155], v[168:171], v[16:19]
	s_nop 0
	v_mfma_f32_16x16x32_bf16 v[16:19], v[156:159], v[172:175], v[16:19]
	v_mfma_f32_16x16x32_bf16 v[12:15], v[144:147], v[176:179], v[12:15]
	s_nop 0
	v_mfma_f32_16x16x32_bf16 v[12:15], v[148:151], v[180:183], v[12:15]
	v_mfma_f32_16x16x32_bf16 v[8:11], v[152:155], v[176:179], v[8:11]
	s_nop 0
	v_mfma_f32_16x16x32_bf16 v[8:11], v[156:159], v[180:183], v[8:11]
	v_mfma_f32_16x16x32_bf16 v[4:7], v[144:147], v[184:187], v[4:7]
	s_nop 0
	v_mfma_f32_16x16x32_bf16 v[4:7], v[148:151], v[188:191], v[4:7]
	v_mfma_f32_16x16x32_bf16 v[0:3], v[152:155], v[184:187], v[0:3]
	s_nop 0
	v_mfma_f32_16x16x32_bf16 v[0:3], v[156:159], v[188:191], v[0:3]
	s_setprio 0
	s_barrier
	ds_read_b128 v[140:143], v203
	ds_read_b128 v[144:147], v204
	ds_read_b128 v[148:151], v205
	ds_read_b128 v[152:155], v206
	ds_read_b128 v[156:159], v207
	ds_read_b128 v[136:139], v208
	ds_read_b128 v[132:135], v209
	ds_read_b128 v[128:131], v210
	s_mov_b32 m0, s69
	s_add_i32 s91, s66, 0x20000
	buffer_load_dwordx4 v196, s[4:7], s91 offen lds
	s_add_i32 s91, s66, 0x30000
	s_mov_b32 m0, s70
	s_nop 0
	buffer_load_dwordx4 v196, s[4:7], s91 offen lds
	ds_read_b128 v[160:163], v197 offset:32768
	ds_read_b128 v[164:167], v197 offset:33792
	ds_read_b128 v[168:171], v197 offset:34816
	ds_read_b128 v[172:175], v197 offset:35840
	ds_read_b128 v[176:179], v197 offset:36864
	ds_read_b128 v[180:183], v197 offset:37888
	ds_read_b128 v[184:187], v197 offset:38912
	ds_read_b128 v[188:191], v197 offset:39936
	s_waitcnt vmcnt(8)
	s_waitcnt lgkmcnt(8)
	s_barrier
	s_setprio 1
	s_waitcnt lgkmcnt(7)
	v_mfma_f32_16x16x32_bf16 v[124:127], v[140:143], v[160:163], v[124:127]
	s_waitcnt lgkmcnt(6)
	v_mfma_f32_16x16x32_bf16 v[124:127], v[144:147], v[164:167], v[124:127]
	v_mfma_f32_16x16x32_bf16 v[120:123], v[148:151], v[160:163], v[120:123]
	s_nop 0
	v_mfma_f32_16x16x32_bf16 v[120:123], v[152:155], v[164:167], v[120:123]
	s_waitcnt lgkmcnt(5)
	v_mfma_f32_16x16x32_bf16 v[116:119], v[140:143], v[168:171], v[116:119]
	s_waitcnt lgkmcnt(4)
	v_mfma_f32_16x16x32_bf16 v[116:119], v[144:147], v[172:175], v[116:119]
	v_mfma_f32_16x16x32_bf16 v[112:115], v[148:151], v[168:171], v[112:115]
	s_nop 0
	v_mfma_f32_16x16x32_bf16 v[112:115], v[152:155], v[172:175], v[112:115]
	s_waitcnt lgkmcnt(3)
	v_mfma_f32_16x16x32_bf16 v[108:111], v[140:143], v[176:179], v[108:111]
	s_waitcnt lgkmcnt(2)
	v_mfma_f32_16x16x32_bf16 v[108:111], v[144:147], v[180:183], v[108:111]
	v_mfma_f32_16x16x32_bf16 v[104:107], v[148:151], v[176:179], v[104:107]
	s_nop 0
	v_mfma_f32_16x16x32_bf16 v[104:107], v[152:155], v[180:183], v[104:107]
	s_waitcnt lgkmcnt(1)
	v_mfma_f32_16x16x32_bf16 v[100:103], v[140:143], v[184:187], v[100:103]
	s_waitcnt lgkmcnt(0)
	v_mfma_f32_16x16x32_bf16 v[100:103], v[144:147], v[188:191], v[100:103]
	v_mfma_f32_16x16x32_bf16 v[96:99], v[148:151], v[184:187], v[96:99]
	s_nop 0
	v_mfma_f32_16x16x32_bf16 v[96:99], v[152:155], v[188:191], v[96:99]
	s_setprio 0
	s_setprio 1
	v_mfma_f32_16x16x32_bf16 v[92:95], v[156:159], v[160:163], v[92:95]
	s_nop 0
	v_mfma_f32_16x16x32_bf16 v[92:95], v[136:139], v[164:167], v[92:95]
	v_mfma_f32_16x16x32_bf16 v[88:91], v[132:135], v[160:163], v[88:91]
	s_nop 0
	v_mfma_f32_16x16x32_bf16 v[88:91], v[128:131], v[164:167], v[88:91]
	v_mfma_f32_16x16x32_bf16 v[84:87], v[156:159], v[168:171], v[84:87]
	s_nop 0
	v_mfma_f32_16x16x32_bf16 v[84:87], v[136:139], v[172:175], v[84:87]
	v_mfma_f32_16x16x32_bf16 v[80:83], v[132:135], v[168:171], v[80:83]
	s_nop 0
	v_mfma_f32_16x16x32_bf16 v[80:83], v[128:131], v[172:175], v[80:83]
	v_mfma_f32_16x16x32_bf16 v[76:79], v[156:159], v[176:179], v[76:79]
	s_nop 0
	v_mfma_f32_16x16x32_bf16 v[76:79], v[136:139], v[180:183], v[76:79]
	v_mfma_f32_16x16x32_bf16 v[72:75], v[132:135], v[176:179], v[72:75]
	s_nop 0
	v_mfma_f32_16x16x32_bf16 v[72:75], v[128:131], v[180:183], v[72:75]
	v_mfma_f32_16x16x32_bf16 v[68:71], v[156:159], v[184:187], v[68:71]
	s_nop 0
	v_mfma_f32_16x16x32_bf16 v[68:71], v[136:139], v[188:191], v[68:71]
	v_mfma_f32_16x16x32_bf16 v[64:67], v[132:135], v[184:187], v[64:67]
	s_nop 0
	v_mfma_f32_16x16x32_bf16 v[64:67], v[128:131], v[188:191], v[64:67]
	s_setprio 0
	s_barrier
	s_mov_b32 m0, s72
	s_add_i32 s91, s90, 0x80
	buffer_load_dwordx4 v192, s[8:11], s91 offen lds
	s_add_i32 s91, s90, 0x20080
	s_mov_b32 m0, s73
	s_add_i32 s66, s66, 0x10080
	buffer_load_dwordx4 v192, s[8:11], s91 offen lds
	s_add_i32 s91, s90, 0x2080
	s_mov_b32 m0, s76
	s_add_i32 s90, s90, 0x22080
	buffer_load_dwordx4 v192, s[8:11], s91 offen lds
	s_mov_b32 m0, s77
	s_nop 0
	buffer_load_dwordx4 v192, s[8:11], s90 offen lds
	s_mov_b32 m0, s74
	s_nop 0
	buffer_load_dwordx4 v196, s[4:7], s67 offen lds
	s_mov_b32 m0, s75
	s_nop 0
	buffer_load_dwordx4 v196, s[4:7], s66 offen lds
	ds_read_b128 v[160:163], v197 offset:49152
	ds_read_b128 v[164:167], v197 offset:50176
	ds_read_b128 v[168:171], v197 offset:51200
	ds_read_b128 v[172:175], v197 offset:52224
	ds_read_b128 v[176:179], v197 offset:53248
	ds_read_b128 v[180:183], v197 offset:54272
	ds_read_b128 v[184:187], v197 offset:55296
	ds_read_b128 v[188:191], v197 offset:56320
	s_waitcnt vmcnt(8)
	s_waitcnt lgkmcnt(6)
	s_barrier
	s_setprio 1
	s_waitcnt lgkmcnt(7)
	v_mfma_f32_16x16x32_bf16 v[60:63], v[140:143], v[160:163], v[60:63]
	s_waitcnt lgkmcnt(6)
	v_mfma_f32_16x16x32_bf16 v[60:63], v[144:147], v[164:167], v[60:63]
	v_mfma_f32_16x16x32_bf16 v[56:59], v[148:151], v[160:163], v[56:59]
	s_nop 0
	v_mfma_f32_16x16x32_bf16 v[56:59], v[152:155], v[164:167], v[56:59]
	s_waitcnt lgkmcnt(5)
	v_mfma_f32_16x16x32_bf16 v[52:55], v[140:143], v[168:171], v[52:55]
	s_waitcnt lgkmcnt(4)
	v_mfma_f32_16x16x32_bf16 v[52:55], v[144:147], v[172:175], v[52:55]
	v_mfma_f32_16x16x32_bf16 v[48:51], v[148:151], v[168:171], v[48:51]
	s_nop 0
	v_mfma_f32_16x16x32_bf16 v[48:51], v[152:155], v[172:175], v[48:51]
	s_waitcnt lgkmcnt(3)
	v_mfma_f32_16x16x32_bf16 v[44:47], v[140:143], v[176:179], v[44:47]
	s_waitcnt lgkmcnt(2)
	v_mfma_f32_16x16x32_bf16 v[44:47], v[144:147], v[180:183], v[44:47]
	v_mfma_f32_16x16x32_bf16 v[40:43], v[148:151], v[176:179], v[40:43]
	s_nop 0
	v_mfma_f32_16x16x32_bf16 v[40:43], v[152:155], v[180:183], v[40:43]
	s_waitcnt lgkmcnt(1)
	v_mfma_f32_16x16x32_bf16 v[36:39], v[140:143], v[184:187], v[36:39]
	s_waitcnt lgkmcnt(0)
	v_mfma_f32_16x16x32_bf16 v[36:39], v[144:147], v[188:191], v[36:39]
	v_mfma_f32_16x16x32_bf16 v[32:35], v[148:151], v[184:187], v[32:35]
	s_nop 0
	v_mfma_f32_16x16x32_bf16 v[32:35], v[152:155], v[188:191], v[32:35]
	s_setprio 0
	s_setprio 1
	v_mfma_f32_16x16x32_bf16 v[28:31], v[156:159], v[160:163], v[28:31]
	s_nop 0
	v_mfma_f32_16x16x32_bf16 v[28:31], v[136:139], v[164:167], v[28:31]
	v_mfma_f32_16x16x32_bf16 v[24:27], v[132:135], v[160:163], v[24:27]
	s_nop 0
	v_mfma_f32_16x16x32_bf16 v[24:27], v[128:131], v[164:167], v[24:27]
	v_mfma_f32_16x16x32_bf16 v[20:23], v[156:159], v[168:171], v[20:23]
	s_nop 0
	v_mfma_f32_16x16x32_bf16 v[20:23], v[136:139], v[172:175], v[20:23]
	v_mfma_f32_16x16x32_bf16 v[16:19], v[132:135], v[168:171], v[16:19]
	s_nop 0
	v_mfma_f32_16x16x32_bf16 v[16:19], v[128:131], v[172:175], v[16:19]
	v_mfma_f32_16x16x32_bf16 v[12:15], v[156:159], v[176:179], v[12:15]
	s_nop 0
	v_mfma_f32_16x16x32_bf16 v[12:15], v[136:139], v[180:183], v[12:15]
	v_mfma_f32_16x16x32_bf16 v[8:11], v[132:135], v[176:179], v[8:11]
	s_nop 0
	v_mfma_f32_16x16x32_bf16 v[8:11], v[128:131], v[180:183], v[8:11]
	v_mfma_f32_16x16x32_bf16 v[4:7], v[156:159], v[184:187], v[4:7]
	s_nop 0
	v_mfma_f32_16x16x32_bf16 v[4:7], v[136:139], v[188:191], v[4:7]
	v_mfma_f32_16x16x32_bf16 v[0:3], v[132:135], v[184:187], v[0:3]
	s_nop 0
	v_mfma_f32_16x16x32_bf16 v[0:3], v[128:131], v[188:191], v[0:3]
	s_setprio 0
	s_barrier
	s_add_i32 s43, s43, 2
	s_addk_i32 s33, 0x100
	s_addk_i32 s42, 0x100
	s_cmp_gt_u32 s43, 5
	s_cbranch_scc0 .LBB0_254
	s_and_b64 vcc, exec, s[14:15]
	s_cbranch_vccz .LBB0_257
	s_barrier

.LBB0_344:
	s_waitcnt lgkmcnt(0)
	s_add_i32 s4, s60, 0x180
	s_add_i32 s5, s36, 0x180
	s_barrier
	s_setprio 1
	s_waitcnt lgkmcnt(7)
	v_mfma_f32_16x16x32_bf16 v[60:63], v[164:167], v[196:199], 0
	s_waitcnt lgkmcnt(6)
	v_mfma_f32_16x16x32_bf16 v[60:63], v[160:163], v[192:195], v[60:63]
	v_mfma_f32_16x16x32_bf16 v[56:59], v[156:159], v[196:199], 0
	s_nop 0
	v_mfma_f32_16x16x32_bf16 v[56:59], v[152:155], v[192:195], v[56:59]
	s_waitcnt lgkmcnt(5)
	v_mfma_f32_16x16x32_bf16 v[52:55], v[164:167], v[188:191], 0
	s_waitcnt lgkmcnt(4)
	v_mfma_f32_16x16x32_bf16 v[52:55], v[160:163], v[184:187], v[52:55]
	v_mfma_f32_16x16x32_bf16 v[48:51], v[156:159], v[188:191], 0
	s_nop 0
	v_mfma_f32_16x16x32_bf16 v[48:51], v[152:155], v[184:187], v[48:51]
	s_waitcnt lgkmcnt(3)
	v_mfma_f32_16x16x32_bf16 v[44:47], v[164:167], v[180:183], 0
	s_waitcnt lgkmcnt(2)
	v_mfma_f32_16x16x32_bf16 v[44:47], v[160:163], v[176:179], v[44:47]
	v_mfma_f32_16x16x32_bf16 v[40:43], v[156:159], v[180:183], 0
	s_nop 0
	v_mfma_f32_16x16x32_bf16 v[40:43], v[152:155], v[176:179], v[40:43]
	s_waitcnt lgkmcnt(1)
	v_mfma_f32_16x16x32_bf16 v[36:39], v[164:167], v[172:175], 0
	s_waitcnt lgkmcnt(0)
	v_mfma_f32_16x16x32_bf16 v[36:39], v[160:163], v[168:171], v[36:39]
	v_mfma_f32_16x16x32_bf16 v[32:35], v[156:159], v[172:175], 0
	s_nop 0
	v_mfma_f32_16x16x32_bf16 v[32:35], v[152:155], v[168:171], v[32:35]
	s_setprio 0
	s_setprio 1
	v_mfma_f32_16x16x32_bf16 v[28:31], v[148:151], v[196:199], 0
	s_nop 0
	v_mfma_f32_16x16x32_bf16 v[28:31], v[144:147], v[192:195], v[28:31]
	v_mfma_f32_16x16x32_bf16 v[24:27], v[140:143], v[196:199], 0
	s_nop 0
	v_mfma_f32_16x16x32_bf16 v[24:27], v[136:139], v[192:195], v[24:27]
	v_mfma_f32_16x16x32_bf16 v[20:23], v[148:151], v[188:191], 0
	s_nop 0
	v_mfma_f32_16x16x32_bf16 v[20:23], v[144:147], v[184:187], v[20:23]
	v_mfma_f32_16x16x32_bf16 v[16:19], v[140:143], v[188:191], 0
	s_nop 0
	v_mfma_f32_16x16x32_bf16 v[16:19], v[136:139], v[184:187], v[16:19]
	v_mfma_f32_16x16x32_bf16 v[12:15], v[148:151], v[180:183], 0
	s_nop 0
	v_mfma_f32_16x16x32_bf16 v[12:15], v[144:147], v[176:179], v[12:15]
	v_mfma_f32_16x16x32_bf16 v[8:11], v[140:143], v[180:183], 0
	s_nop 0
	v_mfma_f32_16x16x32_bf16 v[8:11], v[136:139], v[176:179], v[8:11]
	v_mfma_f32_16x16x32_bf16 v[4:7], v[148:151], v[172:175], 0
	s_nop 0
	v_mfma_f32_16x16x32_bf16 v[4:7], v[144:147], v[168:171], v[4:7]
	v_mfma_f32_16x16x32_bf16 v[0:3], v[140:143], v[172:175], 0
	s_nop 0
	v_mfma_f32_16x16x32_bf16 v[0:3], v[136:139], v[168:171], v[0:3]
	s_setprio 0
	s_barrier
	ds_read_b128 v[164:167], v225
	ds_read_b128 v[160:163], v226
	ds_read_b128 v[156:159], v227
	ds_read_b128 v[152:155], v228
	ds_read_b128 v[148:151], v229
	ds_read_b128 v[144:147], v230
	ds_read_b128 v[140:143], v231
	ds_read_b128 v[136:139], v232
	s_mov_b32 m0, s72
	s_add_i32 s14, s60, 0x100100
	buffer_load_dwordx4 v214, s[8:11], s14 offen lds
	s_add_i32 s14, s60, 0x180100
	s_mov_b32 m0, s73
	s_nop 0
	buffer_load_dwordx4 v214, s[8:11], s14 offen lds
	ds_read_b128 v[168:171], v233 offset:32768
	ds_read_b128 v[172:175], v233 offset:33792
	ds_read_b128 v[176:179], v233 offset:34816
	ds_read_b128 v[180:183], v233 offset:35840
	ds_read_b128 v[184:187], v233 offset:36864
	ds_read_b128 v[188:191], v233 offset:37888
	ds_read_b128 v[192:195], v233 offset:38912
	ds_read_b128 v[196:199], v233 offset:39936
	s_waitcnt vmcnt(10)
	s_waitcnt lgkmcnt(8)
	s_barrier
	s_setprio 1
	s_waitcnt lgkmcnt(7)
	v_mfma_f32_16x16x32_bf16 v[124:127], v[164:167], v[168:171], v[124:127]
	s_waitcnt lgkmcnt(6)
	v_mfma_f32_16x16x32_bf16 v[124:127], v[160:163], v[172:175], v[124:127]
	v_mfma_f32_16x16x32_bf16 v[120:123], v[156:159], v[168:171], v[120:123]
	s_nop 0
	v_mfma_f32_16x16x32_bf16 v[120:123], v[152:155], v[172:175], v[120:123]
	s_waitcnt lgkmcnt(5)
	v_mfma_f32_16x16x32_bf16 v[116:119], v[164:167], v[176:179], v[116:119]
	s_waitcnt lgkmcnt(4)
	v_mfma_f32_16x16x32_bf16 v[116:119], v[160:163], v[180:183], v[116:119]
	v_mfma_f32_16x16x32_bf16 v[112:115], v[156:159], v[176:179], v[112:115]
	s_nop 0
	v_mfma_f32_16x16x32_bf16 v[112:115], v[152:155], v[180:183], v[112:115]
	s_waitcnt lgkmcnt(3)
	v_mfma_f32_16x16x32_bf16 v[108:111], v[164:167], v[184:187], v[108:111]
	s_waitcnt lgkmcnt(2)
	v_mfma_f32_16x16x32_bf16 v[108:111], v[160:163], v[188:191], v[108:111]
	v_mfma_f32_16x16x32_bf16 v[104:107], v[156:159], v[184:187], v[104:107]
	s_nop 0
	v_mfma_f32_16x16x32_bf16 v[104:107], v[152:155], v[188:191], v[104:107]
	s_waitcnt lgkmcnt(1)
	v_mfma_f32_16x16x32_bf16 v[100:103], v[164:167], v[192:195], v[100:103]
	s_waitcnt lgkmcnt(0)
	v_mfma_f32_16x16x32_bf16 v[100:103], v[160:163], v[196:199], v[100:103]
	v_mfma_f32_16x16x32_bf16 v[96:99], v[156:159], v[192:195], v[96:99]
	s_nop 0
	v_mfma_f32_16x16x32_bf16 v[96:99], v[152:155], v[196:199], v[96:99]
	s_setprio 0
	s_setprio 1
	v_mfma_f32_16x16x32_bf16 v[92:95], v[148:151], v[168:171], v[92:95]
	s_nop 0
	v_mfma_f32_16x16x32_bf16 v[92:95], v[144:147], v[172:175], v[92:95]
	v_mfma_f32_16x16x32_bf16 v[88:91], v[140:143], v[168:171], v[88:91]
	s_nop 0
	v_mfma_f32_16x16x32_bf16 v[88:91], v[136:139], v[172:175], v[88:91]
	v_mfma_f32_16x16x32_bf16 v[84:87], v[148:151], v[176:179], v[84:87]
	s_nop 0
	v_mfma_f32_16x16x32_bf16 v[84:87], v[144:147], v[180:183], v[84:87]
	v_mfma_f32_16x16x32_bf16 v[80:83], v[140:143], v[176:179], v[80:83]
	s_nop 0
	v_mfma_f32_16x16x32_bf16 v[80:83], v[136:139], v[180:183], v[80:83]
	v_mfma_f32_16x16x32_bf16 v[76:79], v[148:151], v[184:187], v[76:79]
	s_nop 0
	v_mfma_f32_16x16x32_bf16 v[76:79], v[144:147], v[188:191], v[76:79]
	v_mfma_f32_16x16x32_bf16 v[72:75], v[140:143], v[184:187], v[72:75]
	s_nop 0
	v_mfma_f32_16x16x32_bf16 v[72:75], v[136:139], v[188:191], v[72:75]
	v_mfma_f32_16x16x32_bf16 v[68:71], v[148:151], v[192:195], v[68:71]
	s_nop 0
	v_mfma_f32_16x16x32_bf16 v[68:71], v[144:147], v[196:199], v[68:71]
	v_mfma_f32_16x16x32_bf16 v[64:67], v[140:143], v[192:195], v[64:67]
	s_nop 0
	v_mfma_f32_16x16x32_bf16 v[64:67], v[136:139], v[196:199], v[64:67]
	s_setprio 0
	s_barrier
	s_mov_b32 m0, s76
	s_mov_b32 s14, s10
	s_mov_b32 s15, s11
	buffer_load_dwordx4 v215, s[12:15], s5 offen lds
	s_add_i32 s5, s36, 0x100180
	s_mov_b32 m0, s77
	s_nop 0
	buffer_load_dwordx4 v215, s[12:15], s5 offen lds
	s_add_i32 s5, s36, 0x10180
	s_mov_b32 m0, s80
	s_nop 0
	buffer_load_dwordx4 v215, s[12:15], s5 offen lds
	s_add_i32 s5, s36, 0x110180
	s_mov_b32 m0, s81
	s_nop 0
	buffer_load_dwordx4 v215, s[12:15], s5 offen lds
	s_mov_b32 m0, s78
	s_nop 0
	buffer_load_dwordx4 v214, s[8:11], s4 offen lds
	s_add_i32 s4, s60, 0x80180
	s_mov_b32 m0, s79
	s_nop 0
	buffer_load_dwordx4 v214, s[8:11], s4 offen lds
	ds_read_b128 v[168:171], v233 offset:49152
	ds_read_b128 v[172:175], v233 offset:50176
	ds_read_b128 v[176:179], v233 offset:51200
	ds_read_b128 v[180:183], v233 offset:52224
	ds_read_b128 v[184:187], v233 offset:53248
	ds_read_b128 v[188:191], v233 offset:54272
	ds_read_b128 v[192:195], v233 offset:55296
	ds_read_b128 v[196:199], v233 offset:56320
	s_waitcnt vmcnt(8)
	s_waitcnt lgkmcnt(6)
	s_barrier
	s_setprio 1
	s_waitcnt lgkmcnt(7)
	v_mfma_f32_16x16x32_bf16 v[60:63], v[164:167], v[168:171], v[60:63]
	s_waitcnt lgkmcnt(6)
	v_mfma_f32_16x16x32_bf16 v[60:63], v[160:163], v[172:175], v[60:63]
	v_mfma_f32_16x16x32_bf16 v[56:59], v[156:159], v[168:171], v[56:59]
	s_nop 0
	v_mfma_f32_16x16x32_bf16 v[56:59], v[152:155], v[172:175], v[56:59]
	s_waitcnt lgkmcnt(5)
	v_mfma_f32_16x16x32_bf16 v[52:55], v[164:167], v[176:179], v[52:55]
	s_waitcnt lgkmcnt(4)
	v_mfma_f32_16x16x32_bf16 v[52:55], v[160:163], v[180:183], v[52:55]
	v_mfma_f32_16x16x32_bf16 v[48:51], v[156:159], v[176:179], v[48:51]
	s_nop 0
	v_mfma_f32_16x16x32_bf16 v[48:51], v[152:155], v[180:183], v[48:51]
	s_waitcnt lgkmcnt(3)
	v_mfma_f32_16x16x32_bf16 v[44:47], v[164:167], v[184:187], v[44:47]
	s_waitcnt lgkmcnt(2)
	v_mfma_f32_16x16x32_bf16 v[44:47], v[160:163], v[188:191], v[44:47]
	v_mfma_f32_16x16x32_bf16 v[40:43], v[156:159], v[184:187], v[40:43]
	s_nop 0
	v_mfma_f32_16x16x32_bf16 v[40:43], v[152:155], v[188:191], v[40:43]
	s_waitcnt lgkmcnt(1)
	v_mfma_f32_16x16x32_bf16 v[36:39], v[164:167], v[192:195], v[36:39]
	s_waitcnt lgkmcnt(0)
	v_mfma_f32_16x16x32_bf16 v[36:39], v[160:163], v[196:199], v[36:39]
	v_mfma_f32_16x16x32_bf16 v[32:35], v[156:159], v[192:195], v[32:35]
	s_nop 0
	v_mfma_f32_16x16x32_bf16 v[32:35], v[152:155], v[196:199], v[32:35]
	s_setprio 0
	s_setprio 1
	v_mfma_f32_16x16x32_bf16 v[28:31], v[148:151], v[168:171], v[28:31]
	s_nop 0
	v_mfma_f32_16x16x32_bf16 v[28:31], v[144:147], v[172:175], v[28:31]
	v_mfma_f32_16x16x32_bf16 v[24:27], v[140:143], v[168:171], v[24:27]
	s_nop 0
	v_mfma_f32_16x16x32_bf16 v[24:27], v[136:139], v[172:175], v[24:27]
	v_mfma_f32_16x16x32_bf16 v[20:23], v[148:151], v[176:179], v[20:23]
	s_nop 0
	v_mfma_f32_16x16x32_bf16 v[20:23], v[144:147], v[180:183], v[20:23]
	v_mfma_f32_16x16x32_bf16 v[16:19], v[140:143], v[176:179], v[16:19]
	s_nop 0
	v_mfma_f32_16x16x32_bf16 v[16:19], v[136:139], v[180:183], v[16:19]
	v_mfma_f32_16x16x32_bf16 v[12:15], v[148:151], v[184:187], v[12:15]
	s_nop 0
	v_mfma_f32_16x16x32_bf16 v[12:15], v[144:147], v[188:191], v[12:15]
	v_mfma_f32_16x16x32_bf16 v[8:11], v[140:143], v[184:187], v[8:11]
	s_nop 0
	v_mfma_f32_16x16x32_bf16 v[8:11], v[136:139], v[188:191], v[8:11]
	v_mfma_f32_16x16x32_bf16 v[4:7], v[148:151], v[192:195], v[4:7]
	s_nop 0
	v_mfma_f32_16x16x32_bf16 v[4:7], v[144:147], v[196:199], v[4:7]
	v_mfma_f32_16x16x32_bf16 v[0:3], v[140:143], v[192:195], v[0:3]
	s_nop 0
	v_mfma_f32_16x16x32_bf16 v[0:3], v[136:139], v[196:199], v[0:3]
	s_setprio 0
	s_barrier
	s_waitcnt vmcnt(14)
	v_mul_f32_e32 v132, 0x42800000, v132
	v_mul_f32_e32 v128, 0x42800000, v128
	v_mul_f32_e32 v133, 0x42800000, v133
	v_mul_f32_e32 v129, 0x42800000, v129
	v_mul_f32_e32 v134, 0x42800000, v134
	v_mul_f32_e32 v130, 0x42800000, v130
	v_mul_f32_e32 v135, 0x42800000, v135
	v_mul_f32_e32 v131, 0x42800000, v131
	v_cvt_pk_fp8_f32 v204, v128, v132
	v_cvt_pk_fp8_f32 v234, v129, v133
	v_cvt_pk_fp8_f32 v235, v130, v134
	v_cvt_pk_fp8_f32 v236, v131, v135
	s_add_i32 s33, s36, 0x200
	s_mov_b32 s61, 0
	s_mov_b32 s66, s75
	s_mov_b32 s94, s86
	s_branch .LBB0_347

.LBB0_347:
	v_mov_b32_e32 v152, v204
	v_mov_b32_e32 v153, v234
	v_mov_b32_e32 v154, v235
	v_mov_b32_e32 v155, v236
	ds_read_b128 v[158:161], v217
	ds_read_b128 v[162:165], v218
	ds_read_b128 v[166:169], v219
	ds_read_b128 v[170:173], v220
	ds_read_b128 v[148:151], v221
	ds_read_b128 v[144:147], v222
	ds_read_b128 v[140:143], v223
	ds_read_b128 v[136:139], v224
	s_add_i32 s4, s60, s61
	s_mov_b32 s46, s94
	s_add_i32 s94, s94, 1
	s_add_i32 s5, s4, 0x200
	s_add_i32 s16, s33, s61
	s_cmpk_eq_i32 s61, 0x1e00
	s_cselect_b32 s47, s90, s5
	s_cselect_b32 s97, s91, s16
	s_add_i32 s96, s47, 0x80
	s_mov_b32 m0, s82
	s_add_i32 s5, s4, 0x100180
	buffer_load_dwordx4 v214, s[8:11], s5 offen lds
	s_add_i32 s4, s4, 0x180180
	s_mov_b32 m0, s85
	s_add_i32 vcc_lo, s97, 0x80
	buffer_load_dwordx4 v214, s[8:11], s4 offen lds
	s_lshr_b32 s4, s94, 2
	s_mul_i32 s5, s4, s34
	s_add_i32 s16, s5, s2
	s_cmp_lt_i32 s4, s3
	s_cselect_b64 s[4:5], -1, 0
	s_and_b64 s[44:45], s[4:5], exec
	s_cselect_b32 s16, s16, 0
	s_bfe_u32 s17, s94, 0x10001
	s_or_b32 s17, s17, s83
	s_bfe_u32 s67, s16, 0x50007
	s_bfe_u32 s36, s16, 0x50002
	s_and_b32 s95, s16, 3
	s_cmpk_gt_i32 s16, 0xfff
	s_cselect_b64 s[44:45], -1, 0
	v_lshl_or_b32 v156, s17, 3, v216
	s_and_b64 s[16:17], s[44:45], exec
	s_cselect_b32 s16, s25, s21
	s_cselect_b32 s17, s24, s20
	s_lshl_b32 vcc_hi, s67, 23
	s_add_u32 s17, s17, vcc_hi
	s_addc_u32 s16, s16, 0
	s_lshl_b32 vcc_hi, s36, 18
	s_add_u32 s17, s17, vcc_hi
	s_addc_u32 vcc_hi, s16, 0
	s_lshl_b32 s16, s95, 9
	s_add_u32 s16, s17, s16
	v_and_or_b32 v204, s66, 2, v200
	s_addc_u32 s17, vcc_hi, 0
	v_lshlrev_b64 v[128:129], 11, v[204:205]
	v_lshl_add_u64 v[128:129], s[16:17], 0, v[128:129]
	v_lshlrev_b32_e32 v204, 4, v156
	v_lshl_add_u64 v[132:133], v[128:129], 0, v[204:205]
	global_load_dwordx4 v[128:131], v[132:133], off nt
	s_nop 0
	global_load_dwordx4 v[132:135], v[132:133], off offset:2048 nt
	ds_read_b128 v[174:177], v233
	ds_read_b128 v[178:181], v233 offset:1024
	ds_read_b128 v[182:185], v233 offset:2048
	ds_read_b128 v[186:189], v233 offset:3072
	ds_read_b128 v[190:193], v233 offset:4096
	ds_read_b128 v[194:197], v233 offset:5120
	ds_read_b128 v[234:237], v233 offset:6144
	ds_read_b128 v[238:241], v233 offset:7168
	s_waitcnt vmcnt(10)
	s_waitcnt lgkmcnt(8)
	s_barrier
	s_setprio 1
	s_waitcnt lgkmcnt(7)
	v_mfma_f32_16x16x32_bf16 v[124:127], v[158:161], v[174:177], v[124:127]
	s_waitcnt lgkmcnt(6)
	v_mfma_f32_16x16x32_bf16 v[124:127], v[162:165], v[178:181], v[124:127]
	v_mfma_f32_16x16x32_bf16 v[120:123], v[166:169], v[174:177], v[120:123]
	s_nop 0
	v_mfma_f32_16x16x32_bf16 v[120:123], v[170:173], v[178:181], v[120:123]
	s_waitcnt lgkmcnt(5)
	v_mfma_f32_16x16x32_bf16 v[116:119], v[158:161], v[182:185], v[116:119]
	s_waitcnt lgkmcnt(4)
	v_mfma_f32_16x16x32_bf16 v[116:119], v[162:165], v[186:189], v[116:119]
	v_mfma_f32_16x16x32_bf16 v[112:115], v[166:169], v[182:185], v[112:115]
	s_nop 0
	v_mfma_f32_16x16x32_bf16 v[112:115], v[170:173], v[186:189], v[112:115]
	s_waitcnt lgkmcnt(3)
	v_mfma_f32_16x16x32_bf16 v[108:111], v[158:161], v[190:193], v[108:111]
	s_waitcnt lgkmcnt(2)
	v_mfma_f32_16x16x32_bf16 v[108:111], v[162:165], v[194:197], v[108:111]
	v_mfma_f32_16x16x32_bf16 v[104:107], v[166:169], v[190:193], v[104:107]
	s_nop 0
	v_mfma_f32_16x16x32_bf16 v[104:107], v[170:173], v[194:197], v[104:107]
	s_waitcnt lgkmcnt(1)
	v_mfma_f32_16x16x32_bf16 v[100:103], v[158:161], v[234:237], v[100:103]
	s_waitcnt lgkmcnt(0)
	v_mfma_f32_16x16x32_bf16 v[100:103], v[162:165], v[238:241], v[100:103]
	v_mfma_f32_16x16x32_bf16 v[96:99], v[166:169], v[234:237], v[96:99]
	s_nop 0
	v_mfma_f32_16x16x32_bf16 v[96:99], v[170:173], v[238:241], v[96:99]
	s_setprio 0
	s_setprio 1
	v_mfma_f32_16x16x32_bf16 v[92:95], v[148:151], v[174:177], v[92:95]
	s_nop 0
	v_mfma_f32_16x16x32_bf16 v[92:95], v[144:147], v[178:181], v[92:95]
	v_mfma_f32_16x16x32_bf16 v[88:91], v[140:143], v[174:177], v[88:91]
	s_nop 0
	v_mfma_f32_16x16x32_bf16 v[88:91], v[136:139], v[178:181], v[88:91]
	v_mfma_f32_16x16x32_bf16 v[84:87], v[148:151], v[182:185], v[84:87]
	s_nop 0
	v_mfma_f32_16x16x32_bf16 v[84:87], v[144:147], v[186:189], v[84:87]
	v_mfma_f32_16x16x32_bf16 v[80:83], v[140:143], v[182:185], v[80:83]
	s_nop 0
	v_mfma_f32_16x16x32_bf16 v[80:83], v[136:139], v[186:189], v[80:83]
	v_mfma_f32_16x16x32_bf16 v[76:79], v[148:151], v[190:193], v[76:79]
	s_nop 0
	v_mfma_f32_16x16x32_bf16 v[76:79], v[144:147], v[194:197], v[76:79]
	v_mfma_f32_16x16x32_bf16 v[72:75], v[140:143], v[190:193], v[72:75]
	s_nop 0
	v_mfma_f32_16x16x32_bf16 v[72:75], v[136:139], v[194:197], v[72:75]
	v_mfma_f32_16x16x32_bf16 v[68:71], v[148:151], v[234:237], v[68:71]
	s_nop 0
	v_mfma_f32_16x16x32_bf16 v[68:71], v[144:147], v[238:241], v[68:71]
	v_mfma_f32_16x16x32_bf16 v[64:67], v[140:143], v[234:237], v[64:67]
	s_nop 0
	v_mfma_f32_16x16x32_bf16 v[64:67], v[136:139], v[238:241], v[64:67]
	s_setprio 0
	s_barrier
	s_mov_b32 m0, s65
	s_add_i32 s16, s97, 0x100000
	buffer_load_dwordx4 v215, s[12:15], s97 offen lds
	s_mov_b32 m0, s68
	s_nop 0
	buffer_load_dwordx4 v215, s[12:15], s16 offen lds
	s_add_i32 s16, s97, 0x10000
	s_mov_b32 m0, s69
	s_nop 0
	buffer_load_dwordx4 v215, s[12:15], s16 offen lds
	s_add_i32 s16, s97, 0x110000
	s_mov_b32 m0, s70
	s_nop 0
	buffer_load_dwordx4 v215, s[12:15], s16 offen lds
	s_mov_b32 m0, s64
	s_add_i32 s16, s47, 0x80000
	buffer_load_dwordx4 v214, s[8:11], s47 offen lds
	s_mov_b32 m0, s71
	s_nop 0
	buffer_load_dwordx4 v214, s[8:11], s16 offen lds
	ds_read_b128 v[174:177], v233 offset:16384
	ds_read_b128 v[178:181], v233 offset:17408
	ds_read_b128 v[182:185], v233 offset:18432
	ds_read_b128 v[186:189], v233 offset:19456
	ds_read_b128 v[190:193], v233 offset:20480
	ds_read_b128 v[194:197], v233 offset:21504
	ds_read_b128 v[234:237], v233 offset:22528
	ds_read_b128 v[238:241], v233 offset:23552
	s_waitcnt vmcnt(10)
	s_waitcnt lgkmcnt(6)
	s_barrier
	s_setprio 1
	s_waitcnt lgkmcnt(7)
	v_mfma_f32_16x16x32_bf16 v[60:63], v[158:161], v[174:177], v[60:63]
	s_waitcnt lgkmcnt(6)
	v_mfma_f32_16x16x32_bf16 v[60:63], v[162:165], v[178:181], v[60:63]
	v_mfma_f32_16x16x32_bf16 v[56:59], v[166:169], v[174:177], v[56:59]
	s_nop 0
	v_mfma_f32_16x16x32_bf16 v[56:59], v[170:173], v[178:181], v[56:59]
	s_waitcnt lgkmcnt(5)
	v_mfma_f32_16x16x32_bf16 v[52:55], v[158:161], v[182:185], v[52:55]
	s_waitcnt lgkmcnt(4)
	v_mfma_f32_16x16x32_bf16 v[52:55], v[162:165], v[186:189], v[52:55]
	v_mfma_f32_16x16x32_bf16 v[48:51], v[166:169], v[182:185], v[48:51]
	s_nop 0
	v_mfma_f32_16x16x32_bf16 v[48:51], v[170:173], v[186:189], v[48:51]
	s_waitcnt lgkmcnt(3)
	v_mfma_f32_16x16x32_bf16 v[44:47], v[158:161], v[190:193], v[44:47]
	s_waitcnt lgkmcnt(2)
	v_mfma_f32_16x16x32_bf16 v[44:47], v[162:165], v[194:197], v[44:47]
	v_mfma_f32_16x16x32_bf16 v[40:43], v[166:169], v[190:193], v[40:43]
	s_nop 0
	v_mfma_f32_16x16x32_bf16 v[40:43], v[170:173], v[194:197], v[40:43]
	s_waitcnt lgkmcnt(1)
	v_mfma_f32_16x16x32_bf16 v[36:39], v[158:161], v[234:237], v[36:39]
	s_waitcnt lgkmcnt(0)
	v_mfma_f32_16x16x32_bf16 v[36:39], v[162:165], v[238:241], v[36:39]
	v_mfma_f32_16x16x32_bf16 v[32:35], v[166:169], v[234:237], v[32:35]
	s_nop 0
	v_mfma_f32_16x16x32_bf16 v[32:35], v[170:173], v[238:241], v[32:35]
	s_setprio 0
	s_setprio 1
	v_mfma_f32_16x16x32_bf16 v[28:31], v[148:151], v[174:177], v[28:31]
	s_nop 0
	v_mfma_f32_16x16x32_bf16 v[28:31], v[144:147], v[178:181], v[28:31]
	v_mfma_f32_16x16x32_bf16 v[24:27], v[140:143], v[174:177], v[24:27]
	s_nop 0
	v_mfma_f32_16x16x32_bf16 v[24:27], v[136:139], v[178:181], v[24:27]
	v_mfma_f32_16x16x32_bf16 v[20:23], v[148:151], v[182:185], v[20:23]
	s_nop 0
	v_mfma_f32_16x16x32_bf16 v[20:23], v[144:147], v[186:189], v[20:23]
	v_mfma_f32_16x16x32_bf16 v[16:19], v[140:143], v[182:185], v[16:19]
	s_nop 0
	v_mfma_f32_16x16x32_bf16 v[16:19], v[136:139], v[186:189], v[16:19]
	v_mfma_f32_16x16x32_bf16 v[12:15], v[148:151], v[190:193], v[12:15]
	s_nop 0
	v_mfma_f32_16x16x32_bf16 v[12:15], v[144:147], v[194:197], v[12:15]
	v_mfma_f32_16x16x32_bf16 v[8:11], v[140:143], v[190:193], v[8:11]
	s_nop 0
	v_mfma_f32_16x16x32_bf16 v[8:11], v[136:139], v[194:197], v[8:11]
	v_mfma_f32_16x16x32_bf16 v[4:7], v[148:151], v[234:237], v[4:7]
	s_nop 0
	v_mfma_f32_16x16x32_bf16 v[4:7], v[144:147], v[238:241], v[4:7]
	v_mfma_f32_16x16x32_bf16 v[0:3], v[140:143], v[234:237], v[0:3]
	s_nop 0
	v_mfma_f32_16x16x32_bf16 v[0:3], v[136:139], v[238:241], v[0:3]
	s_setprio 0
	s_barrier
	ds_read_b128 v[136:139], v225
	ds_read_b128 v[140:143], v226
	ds_read_b128 v[144:147], v227
	ds_read_b128 v[148:151], v228
	ds_read_b128 v[158:161], v229
	ds_read_b128 v[162:165], v230
	ds_read_b128 v[166:169], v231
	ds_read_b128 v[170:173], v232
	s_mov_b32 m0, s72
	s_add_i32 s16, s47, 0x100000
	buffer_load_dwordx4 v214, s[8:11], s16 offen lds
	s_add_i32 s16, s47, 0x180000
	s_mov_b32 m0, s73
	s_nop 0
	buffer_load_dwordx4 v214, s[8:11], s16 offen lds
	ds_read_b128 v[174:177], v233 offset:32768
	ds_read_b128 v[178:181], v233 offset:33792
	ds_read_b128 v[182:185], v233 offset:34816
	ds_read_b128 v[186:189], v233 offset:35840
	ds_read_b128 v[190:193], v233 offset:36864
	ds_read_b128 v[194:197], v233 offset:37888
	ds_read_b128 v[234:237], v233 offset:38912
	ds_read_b128 v[238:241], v233 offset:39936
	s_waitcnt vmcnt(10)
	s_waitcnt lgkmcnt(8)
	s_barrier
	s_setprio 1
	s_waitcnt lgkmcnt(7)
	v_mfma_f32_16x16x32_bf16 v[124:127], v[136:139], v[174:177], v[124:127]
	s_waitcnt lgkmcnt(6)
	v_mfma_f32_16x16x32_bf16 v[124:127], v[140:143], v[178:181], v[124:127]
	v_mfma_f32_16x16x32_bf16 v[120:123], v[144:147], v[174:177], v[120:123]
	s_nop 0
	v_mfma_f32_16x16x32_bf16 v[120:123], v[148:151], v[178:181], v[120:123]
	s_waitcnt lgkmcnt(5)
	v_mfma_f32_16x16x32_bf16 v[116:119], v[136:139], v[182:185], v[116:119]
	s_waitcnt lgkmcnt(4)
	v_mfma_f32_16x16x32_bf16 v[116:119], v[140:143], v[186:189], v[116:119]
	v_mfma_f32_16x16x32_bf16 v[112:115], v[144:147], v[182:185], v[112:115]
	s_nop 0
	v_mfma_f32_16x16x32_bf16 v[112:115], v[148:151], v[186:189], v[112:115]
	s_waitcnt lgkmcnt(3)
	v_mfma_f32_16x16x32_bf16 v[108:111], v[136:139], v[190:193], v[108:111]
	s_waitcnt lgkmcnt(2)
	v_mfma_f32_16x16x32_bf16 v[108:111], v[140:143], v[194:197], v[108:111]
	v_mfma_f32_16x16x32_bf16 v[104:107], v[144:147], v[190:193], v[104:107]
	s_nop 0
	v_mfma_f32_16x16x32_bf16 v[104:107], v[148:151], v[194:197], v[104:107]
	s_waitcnt lgkmcnt(1)
	v_mfma_f32_16x16x32_bf16 v[100:103], v[136:139], v[234:237], v[100:103]
	s_waitcnt lgkmcnt(0)
	v_mfma_f32_16x16x32_bf16 v[100:103], v[140:143], v[238:241], v[100:103]
	v_mfma_f32_16x16x32_bf16 v[96:99], v[144:147], v[234:237], v[96:99]
	s_nop 0
	v_mfma_f32_16x16x32_bf16 v[96:99], v[148:151], v[238:241], v[96:99]
	s_setprio 0
	s_setprio 1
	v_mfma_f32_16x16x32_bf16 v[92:95], v[158:161], v[174:177], v[92:95]
	s_nop 0
	v_mfma_f32_16x16x32_bf16 v[92:95], v[162:165], v[178:181], v[92:95]
	v_mfma_f32_16x16x32_bf16 v[88:91], v[166:169], v[174:177], v[88:91]
	s_nop 0
	v_mfma_f32_16x16x32_bf16 v[88:91], v[170:173], v[178:181], v[88:91]
	v_mfma_f32_16x16x32_bf16 v[84:87], v[158:161], v[182:185], v[84:87]
	s_nop 0
	v_mfma_f32_16x16x32_bf16 v[84:87], v[162:165], v[186:189], v[84:87]
	v_mfma_f32_16x16x32_bf16 v[80:83], v[166:169], v[182:185], v[80:83]
	s_nop 0
	v_mfma_f32_16x16x32_bf16 v[80:83], v[170:173], v[186:189], v[80:83]
	v_mfma_f32_16x16x32_bf16 v[76:79], v[158:161], v[190:193], v[76:79]
	s_nop 0
	v_mfma_f32_16x16x32_bf16 v[76:79], v[162:165], v[194:197], v[76:79]
	v_mfma_f32_16x16x32_bf16 v[72:75], v[166:169], v[190:193], v[72:75]
	s_nop 0
	v_mfma_f32_16x16x32_bf16 v[72:75], v[170:173], v[194:197], v[72:75]
	v_mfma_f32_16x16x32_bf16 v[68:71], v[158:161], v[234:237], v[68:71]
	s_nop 0
	v_mfma_f32_16x16x32_bf16 v[68:71], v[162:165], v[238:241], v[68:71]
	v_mfma_f32_16x16x32_bf16 v[64:67], v[166:169], v[234:237], v[64:67]
	s_nop 0
	v_mfma_f32_16x16x32_bf16 v[64:67], v[170:173], v[238:241], v[64:67]
	s_setprio 0
	s_barrier
	s_mov_b32 m0, s76
	s_add_i32 s16, s97, 0x100080
	buffer_load_dwordx4 v215, s[12:15], vcc_lo offen lds
	s_mov_b32 m0, s77
	s_add_i32 s47, s47, 0x80080
	buffer_load_dwordx4 v215, s[12:15], s16 offen lds
	s_add_i32 s16, s97, 0x10080
	s_mov_b32 m0, s80
	s_add_i32 s97, s97, 0x110080
	buffer_load_dwordx4 v215, s[12:15], s16 offen lds
	s_mov_b32 m0, s81
	s_nop 0
	buffer_load_dwordx4 v215, s[12:15], s97 offen lds
	s_mov_b32 m0, s78
	s_nop 0
	buffer_load_dwordx4 v214, s[8:11], s96 offen lds
	s_mov_b32 m0, s79
	s_nop 0
	buffer_load_dwordx4 v214, s[8:11], s47 offen lds
	ds_read_b128 v[174:177], v233 offset:49152
	ds_read_b128 v[178:181], v233 offset:50176
	ds_read_b128 v[182:185], v233 offset:51200
	ds_read_b128 v[186:189], v233 offset:52224
	ds_read_b128 v[190:193], v233 offset:53248
	ds_read_b128 v[194:197], v233 offset:54272
	ds_read_b128 v[234:237], v233 offset:55296
	ds_read_b128 v[238:241], v233 offset:56320
	s_waitcnt vmcnt(8)
	s_waitcnt lgkmcnt(6)
	s_barrier
	s_setprio 1
	s_waitcnt lgkmcnt(7)
	v_mfma_f32_16x16x32_bf16 v[60:63], v[136:139], v[174:177], v[60:63]
	s_waitcnt lgkmcnt(6)
	v_mfma_f32_16x16x32_bf16 v[60:63], v[140:143], v[178:181], v[60:63]
	v_mfma_f32_16x16x32_bf16 v[56:59], v[144:147], v[174:177], v[56:59]
	s_nop 0
	v_mfma_f32_16x16x32_bf16 v[56:59], v[148:151], v[178:181], v[56:59]
	s_waitcnt lgkmcnt(5)
	v_mfma_f32_16x16x32_bf16 v[52:55], v[136:139], v[182:185], v[52:55]
	s_waitcnt lgkmcnt(4)
	v_mfma_f32_16x16x32_bf16 v[52:55], v[140:143], v[186:189], v[52:55]
	v_mfma_f32_16x16x32_bf16 v[48:51], v[144:147], v[182:185], v[48:51]
	s_nop 0
	v_mfma_f32_16x16x32_bf16 v[48:51], v[148:151], v[186:189], v[48:51]
	s_waitcnt lgkmcnt(3)
	v_mfma_f32_16x16x32_bf16 v[44:47], v[136:139], v[190:193], v[44:47]
	s_waitcnt lgkmcnt(2)
	v_mfma_f32_16x16x32_bf16 v[44:47], v[140:143], v[194:197], v[44:47]
	v_mfma_f32_16x16x32_bf16 v[40:43], v[144:147], v[190:193], v[40:43]
	s_nop 0
	v_mfma_f32_16x16x32_bf16 v[40:43], v[148:151], v[194:197], v[40:43]
	s_waitcnt lgkmcnt(1)
	v_mfma_f32_16x16x32_bf16 v[36:39], v[136:139], v[234:237], v[36:39]
	s_waitcnt lgkmcnt(0)
	v_mfma_f32_16x16x32_bf16 v[36:39], v[140:143], v[238:241], v[36:39]
	v_mfma_f32_16x16x32_bf16 v[32:35], v[144:147], v[234:237], v[32:35]
	s_nop 0
	v_mfma_f32_16x16x32_bf16 v[32:35], v[148:151], v[238:241], v[32:35]
	s_setprio 0
	s_setprio 1
	v_mfma_f32_16x16x32_bf16 v[28:31], v[158:161], v[174:177], v[28:31]
	s_nop 0
	v_mfma_f32_16x16x32_bf16 v[28:31], v[162:165], v[178:181], v[28:31]
	v_mfma_f32_16x16x32_bf16 v[24:27], v[166:169], v[174:177], v[24:27]
	s_nop 0
	v_mfma_f32_16x16x32_bf16 v[24:27], v[170:173], v[178:181], v[24:27]
	v_mfma_f32_16x16x32_bf16 v[20:23], v[158:161], v[182:185], v[20:23]
	s_nop 0
	v_mfma_f32_16x16x32_bf16 v[20:23], v[162:165], v[186:189], v[20:23]
	v_mfma_f32_16x16x32_bf16 v[16:19], v[166:169], v[182:185], v[16:19]
	s_nop 0
	v_mfma_f32_16x16x32_bf16 v[16:19], v[170:173], v[186:189], v[16:19]
	v_mfma_f32_16x16x32_bf16 v[12:15], v[158:161], v[190:193], v[12:15]
	s_nop 0
	v_mfma_f32_16x16x32_bf16 v[12:15], v[162:165], v[194:197], v[12:15]
	v_mfma_f32_16x16x32_bf16 v[8:11], v[166:169], v[190:193], v[8:11]
	s_nop 0
	v_mfma_f32_16x16x32_bf16 v[8:11], v[170:173], v[194:197], v[8:11]
	v_mfma_f32_16x16x32_bf16 v[4:7], v[158:161], v[234:237], v[4:7]
	s_nop 0
	v_mfma_f32_16x16x32_bf16 v[4:7], v[162:165], v[238:241], v[4:7]
	v_mfma_f32_16x16x32_bf16 v[0:3], v[166:169], v[234:237], v[0:3]
	s_nop 0
	v_mfma_f32_16x16x32_bf16 v[0:3], v[170:173], v[238:241], v[0:3]
	s_setprio 0
	s_barrier
	s_bitcmp0_b32 s46, 0
	s_waitcnt vmcnt(15)
	v_mul_f32_e32 v128, 0x42800000, v128
	s_waitcnt vmcnt(14)
	v_mul_f32_e32 v132, 0x42800000, v132
	v_mul_f32_e32 v129, 0x42800000, v129
	v_mul_f32_e32 v133, 0x42800000, v133
	v_mul_f32_e32 v130, 0x42800000, v130
	v_mul_f32_e32 v134, 0x42800000, v134
	v_mul_f32_e32 v131, 0x42800000, v131
	v_mul_f32_e32 v135, 0x42800000, v135
	s_mov_b64 s[46:47], -1
	s_cbranch_scc0 .LBB0_350
	s_andn2_b64 vcc, exec, s[46:47]
	s_cbranch_vccnz .LBB0_346
	s_branch .LBB0_351

.LBB0_592:
	s_waitcnt lgkmcnt(0)
	s_add_i32 s4, s60, 0x180
	s_add_i32 s5, s42, 0x180
	s_barrier
	s_setprio 1
	s_waitcnt lgkmcnt(7)
	v_mfma_f32_16x16x32_bf16 v[60:63], v[164:167], v[196:199], 0
	s_waitcnt lgkmcnt(6)
	v_mfma_f32_16x16x32_bf16 v[60:63], v[160:163], v[192:195], v[60:63]
	v_mfma_f32_16x16x32_bf16 v[56:59], v[156:159], v[196:199], 0
	s_nop 0
	v_mfma_f32_16x16x32_bf16 v[56:59], v[152:155], v[192:195], v[56:59]
	s_waitcnt lgkmcnt(5)
	v_mfma_f32_16x16x32_bf16 v[52:55], v[164:167], v[188:191], 0
	s_waitcnt lgkmcnt(4)
	v_mfma_f32_16x16x32_bf16 v[52:55], v[160:163], v[184:187], v[52:55]
	v_mfma_f32_16x16x32_bf16 v[48:51], v[156:159], v[188:191], 0
	s_nop 0
	v_mfma_f32_16x16x32_bf16 v[48:51], v[152:155], v[184:187], v[48:51]
	s_waitcnt lgkmcnt(3)
	v_mfma_f32_16x16x32_bf16 v[44:47], v[164:167], v[180:183], 0
	s_waitcnt lgkmcnt(2)
	v_mfma_f32_16x16x32_bf16 v[44:47], v[160:163], v[176:179], v[44:47]
	v_mfma_f32_16x16x32_bf16 v[40:43], v[156:159], v[180:183], 0
	s_nop 0
	v_mfma_f32_16x16x32_bf16 v[40:43], v[152:155], v[176:179], v[40:43]
	s_waitcnt lgkmcnt(1)
	v_mfma_f32_16x16x32_bf16 v[36:39], v[164:167], v[172:175], 0
	s_waitcnt lgkmcnt(0)
	v_mfma_f32_16x16x32_bf16 v[36:39], v[160:163], v[168:171], v[36:39]
	v_mfma_f32_16x16x32_bf16 v[32:35], v[156:159], v[172:175], 0
	s_nop 0
	v_mfma_f32_16x16x32_bf16 v[32:35], v[152:155], v[168:171], v[32:35]
	s_setprio 0
	s_setprio 1
	v_mfma_f32_16x16x32_bf16 v[28:31], v[148:151], v[196:199], 0
	s_nop 0
	v_mfma_f32_16x16x32_bf16 v[28:31], v[144:147], v[192:195], v[28:31]
	v_mfma_f32_16x16x32_bf16 v[24:27], v[140:143], v[196:199], 0
	s_nop 0
	v_mfma_f32_16x16x32_bf16 v[24:27], v[136:139], v[192:195], v[24:27]
	v_mfma_f32_16x16x32_bf16 v[20:23], v[148:151], v[188:191], 0
	s_nop 0
	v_mfma_f32_16x16x32_bf16 v[20:23], v[144:147], v[184:187], v[20:23]
	v_mfma_f32_16x16x32_bf16 v[16:19], v[140:143], v[188:191], 0
	s_nop 0
	v_mfma_f32_16x16x32_bf16 v[16:19], v[136:139], v[184:187], v[16:19]
	v_mfma_f32_16x16x32_bf16 v[12:15], v[148:151], v[180:183], 0
	s_nop 0
	v_mfma_f32_16x16x32_bf16 v[12:15], v[144:147], v[176:179], v[12:15]
	v_mfma_f32_16x16x32_bf16 v[8:11], v[140:143], v[180:183], 0
	s_nop 0
	v_mfma_f32_16x16x32_bf16 v[8:11], v[136:139], v[176:179], v[8:11]
	v_mfma_f32_16x16x32_bf16 v[4:7], v[148:151], v[172:175], 0
	s_nop 0
	v_mfma_f32_16x16x32_bf16 v[4:7], v[144:147], v[168:171], v[4:7]
	v_mfma_f32_16x16x32_bf16 v[0:3], v[140:143], v[172:175], 0
	s_nop 0
	v_mfma_f32_16x16x32_bf16 v[0:3], v[136:139], v[168:171], v[0:3]
	s_setprio 0
	s_barrier
	ds_read_b128 v[164:167], v224
	ds_read_b128 v[160:163], v225
	ds_read_b128 v[156:159], v226
	ds_read_b128 v[152:155], v227
	ds_read_b128 v[148:151], v228
	ds_read_b128 v[144:147], v229
	ds_read_b128 v[140:143], v230
	ds_read_b128 v[136:139], v231
	s_mov_b32 m0, s68
	s_add_i32 s10, s60, 0x100100
	buffer_load_dwordx4 v213, s[12:15], s10 offen lds
	s_add_i32 s10, s60, 0x180100
	s_mov_b32 m0, s69
	s_nop 0
	buffer_load_dwordx4 v213, s[12:15], s10 offen lds
	ds_read_b128 v[168:171], v232 offset:32768
	ds_read_b128 v[172:175], v232 offset:33792
	ds_read_b128 v[176:179], v232 offset:34816
	ds_read_b128 v[180:183], v232 offset:35840
	ds_read_b128 v[184:187], v232 offset:36864
	ds_read_b128 v[188:191], v232 offset:37888
	ds_read_b128 v[192:195], v232 offset:38912
	ds_read_b128 v[196:199], v232 offset:39936
	s_waitcnt vmcnt(10)
	s_waitcnt lgkmcnt(8)
	s_barrier
	s_setprio 1
	s_waitcnt lgkmcnt(7)
	v_mfma_f32_16x16x32_bf16 v[124:127], v[164:167], v[168:171], v[124:127]
	s_waitcnt lgkmcnt(6)
	v_mfma_f32_16x16x32_bf16 v[124:127], v[160:163], v[172:175], v[124:127]
	v_mfma_f32_16x16x32_bf16 v[120:123], v[156:159], v[168:171], v[120:123]
	s_nop 0
	v_mfma_f32_16x16x32_bf16 v[120:123], v[152:155], v[172:175], v[120:123]
	s_waitcnt lgkmcnt(5)
	v_mfma_f32_16x16x32_bf16 v[116:119], v[164:167], v[176:179], v[116:119]
	s_waitcnt lgkmcnt(4)
	v_mfma_f32_16x16x32_bf16 v[116:119], v[160:163], v[180:183], v[116:119]
	v_mfma_f32_16x16x32_bf16 v[112:115], v[156:159], v[176:179], v[112:115]
	s_nop 0
	v_mfma_f32_16x16x32_bf16 v[112:115], v[152:155], v[180:183], v[112:115]
	s_waitcnt lgkmcnt(3)
	v_mfma_f32_16x16x32_bf16 v[108:111], v[164:167], v[184:187], v[108:111]
	s_waitcnt lgkmcnt(2)
	v_mfma_f32_16x16x32_bf16 v[108:111], v[160:163], v[188:191], v[108:111]
	v_mfma_f32_16x16x32_bf16 v[104:107], v[156:159], v[184:187], v[104:107]
	s_nop 0
	v_mfma_f32_16x16x32_bf16 v[104:107], v[152:155], v[188:191], v[104:107]
	s_waitcnt lgkmcnt(1)
	v_mfma_f32_16x16x32_bf16 v[100:103], v[164:167], v[192:195], v[100:103]
	s_waitcnt lgkmcnt(0)
	v_mfma_f32_16x16x32_bf16 v[100:103], v[160:163], v[196:199], v[100:103]
	v_mfma_f32_16x16x32_bf16 v[96:99], v[156:159], v[192:195], v[96:99]
	s_nop 0
	v_mfma_f32_16x16x32_bf16 v[96:99], v[152:155], v[196:199], v[96:99]
	s_setprio 0
	s_setprio 1
	v_mfma_f32_16x16x32_bf16 v[92:95], v[148:151], v[168:171], v[92:95]
	s_nop 0
	v_mfma_f32_16x16x32_bf16 v[92:95], v[144:147], v[172:175], v[92:95]
	v_mfma_f32_16x16x32_bf16 v[88:91], v[140:143], v[168:171], v[88:91]
	s_nop 0
	v_mfma_f32_16x16x32_bf16 v[88:91], v[136:139], v[172:175], v[88:91]
	v_mfma_f32_16x16x32_bf16 v[84:87], v[148:151], v[176:179], v[84:87]
	s_nop 0
	v_mfma_f32_16x16x32_bf16 v[84:87], v[144:147], v[180:183], v[84:87]
	v_mfma_f32_16x16x32_bf16 v[80:83], v[140:143], v[176:179], v[80:83]
	s_nop 0
	v_mfma_f32_16x16x32_bf16 v[80:83], v[136:139], v[180:183], v[80:83]
	v_mfma_f32_16x16x32_bf16 v[76:79], v[148:151], v[184:187], v[76:79]
	s_nop 0
	v_mfma_f32_16x16x32_bf16 v[76:79], v[144:147], v[188:191], v[76:79]
	v_mfma_f32_16x16x32_bf16 v[72:75], v[140:143], v[184:187], v[72:75]
	s_nop 0
	v_mfma_f32_16x16x32_bf16 v[72:75], v[136:139], v[188:191], v[72:75]
	v_mfma_f32_16x16x32_bf16 v[68:71], v[148:151], v[192:195], v[68:71]
	s_nop 0
	v_mfma_f32_16x16x32_bf16 v[68:71], v[144:147], v[196:199], v[68:71]
	v_mfma_f32_16x16x32_bf16 v[64:67], v[140:143], v[192:195], v[64:67]
	s_nop 0
	v_mfma_f32_16x16x32_bf16 v[64:67], v[136:139], v[196:199], v[64:67]
	s_setprio 0
	s_barrier
	s_mov_b32 m0, s72
	s_mov_b32 s10, s14
	s_mov_b32 s11, s15
	buffer_load_dwordx4 v214, s[8:11], s5 offen lds
	s_add_i32 s5, s42, 0x40180
	s_mov_b32 m0, s73
	s_nop 0
	buffer_load_dwordx4 v214, s[8:11], s5 offen lds
	s_add_i32 s5, s42, 0x4180
	s_mov_b32 m0, s76
	s_nop 0
	buffer_load_dwordx4 v214, s[8:11], s5 offen lds
	s_add_i32 s5, s42, 0x44180
	s_mov_b32 m0, s77
	s_nop 0
	buffer_load_dwordx4 v214, s[8:11], s5 offen lds
	s_mov_b32 m0, s74
	s_nop 0
	buffer_load_dwordx4 v213, s[12:15], s4 offen lds
	s_add_i32 s4, s60, 0x80180
	s_mov_b32 m0, s75
	s_nop 0
	buffer_load_dwordx4 v213, s[12:15], s4 offen lds
	ds_read_b128 v[168:171], v232 offset:49152
	ds_read_b128 v[172:175], v232 offset:50176
	ds_read_b128 v[176:179], v232 offset:51200
	ds_read_b128 v[180:183], v232 offset:52224
	ds_read_b128 v[184:187], v232 offset:53248
	ds_read_b128 v[188:191], v232 offset:54272
	ds_read_b128 v[192:195], v232 offset:55296
	ds_read_b128 v[196:199], v232 offset:56320
	s_waitcnt vmcnt(8)
	s_waitcnt lgkmcnt(6)
	s_barrier
	s_setprio 1
	s_waitcnt lgkmcnt(7)
	v_mfma_f32_16x16x32_bf16 v[60:63], v[164:167], v[168:171], v[60:63]
	s_waitcnt lgkmcnt(6)
	v_mfma_f32_16x16x32_bf16 v[60:63], v[160:163], v[172:175], v[60:63]
	v_mfma_f32_16x16x32_bf16 v[56:59], v[156:159], v[168:171], v[56:59]
	s_nop 0
	v_mfma_f32_16x16x32_bf16 v[56:59], v[152:155], v[172:175], v[56:59]
	s_waitcnt lgkmcnt(5)
	v_mfma_f32_16x16x32_bf16 v[52:55], v[164:167], v[176:179], v[52:55]
	s_waitcnt lgkmcnt(4)
	v_mfma_f32_16x16x32_bf16 v[52:55], v[160:163], v[180:183], v[52:55]
	v_mfma_f32_16x16x32_bf16 v[48:51], v[156:159], v[176:179], v[48:51]
	s_nop 0
	v_mfma_f32_16x16x32_bf16 v[48:51], v[152:155], v[180:183], v[48:51]
	s_waitcnt lgkmcnt(3)
	v_mfma_f32_16x16x32_bf16 v[44:47], v[164:167], v[184:187], v[44:47]
	s_waitcnt lgkmcnt(2)
	v_mfma_f32_16x16x32_bf16 v[44:47], v[160:163], v[188:191], v[44:47]
	v_mfma_f32_16x16x32_bf16 v[40:43], v[156:159], v[184:187], v[40:43]
	s_nop 0
	v_mfma_f32_16x16x32_bf16 v[40:43], v[152:155], v[188:191], v[40:43]
	s_waitcnt lgkmcnt(1)
	v_mfma_f32_16x16x32_bf16 v[36:39], v[164:167], v[192:195], v[36:39]
	s_waitcnt lgkmcnt(0)
	v_mfma_f32_16x16x32_bf16 v[36:39], v[160:163], v[196:199], v[36:39]
	v_mfma_f32_16x16x32_bf16 v[32:35], v[156:159], v[192:195], v[32:35]
	s_nop 0
	v_mfma_f32_16x16x32_bf16 v[32:35], v[152:155], v[196:199], v[32:35]
	s_setprio 0
	s_setprio 1
	v_mfma_f32_16x16x32_bf16 v[28:31], v[148:151], v[168:171], v[28:31]
	s_nop 0
	v_mfma_f32_16x16x32_bf16 v[28:31], v[144:147], v[172:175], v[28:31]
	v_mfma_f32_16x16x32_bf16 v[24:27], v[140:143], v[168:171], v[24:27]
	s_nop 0
	v_mfma_f32_16x16x32_bf16 v[24:27], v[136:139], v[172:175], v[24:27]
	v_mfma_f32_16x16x32_bf16 v[20:23], v[148:151], v[176:179], v[20:23]
	s_nop 0
	v_mfma_f32_16x16x32_bf16 v[20:23], v[144:147], v[180:183], v[20:23]
	v_mfma_f32_16x16x32_bf16 v[16:19], v[140:143], v[176:179], v[16:19]
	s_nop 0
	v_mfma_f32_16x16x32_bf16 v[16:19], v[136:139], v[180:183], v[16:19]
	v_mfma_f32_16x16x32_bf16 v[12:15], v[148:151], v[184:187], v[12:15]
	s_nop 0
	v_mfma_f32_16x16x32_bf16 v[12:15], v[144:147], v[188:191], v[12:15]
	v_mfma_f32_16x16x32_bf16 v[8:11], v[140:143], v[184:187], v[8:11]
	s_nop 0
	v_mfma_f32_16x16x32_bf16 v[8:11], v[136:139], v[188:191], v[8:11]
	v_mfma_f32_16x16x32_bf16 v[4:7], v[148:151], v[192:195], v[4:7]
	s_nop 0
	v_mfma_f32_16x16x32_bf16 v[4:7], v[144:147], v[196:199], v[4:7]
	v_mfma_f32_16x16x32_bf16 v[0:3], v[140:143], v[192:195], v[0:3]
	s_nop 0
	v_mfma_f32_16x16x32_bf16 v[0:3], v[136:139], v[196:199], v[0:3]
	s_setprio 0
	s_barrier
	s_waitcnt vmcnt(14)
	v_mul_f32_e32 v132, 0x42800000, v132
	v_mul_f32_e32 v128, 0x42800000, v128
	v_mul_f32_e32 v133, 0x42800000, v133
	v_mul_f32_e32 v129, 0x42800000, v129
	v_mul_f32_e32 v134, 0x42800000, v134
	v_mul_f32_e32 v130, 0x42800000, v130
	v_mul_f32_e32 v135, 0x42800000, v135
	v_mul_f32_e32 v131, 0x42800000, v131
	v_cvt_pk_fp8_f32 v202, v128, v132
	v_cvt_pk_fp8_f32 v233, v129, v133
	v_cvt_pk_fp8_f32 v234, v130, v134
	v_cvt_pk_fp8_f32 v235, v131, v135
	s_add_i32 s33, s42, 0x200
	s_mov_b32 s66, 0
	s_mov_b32 s89, s70
	s_mov_b32 s90, s71
	s_branch .LBB0_595

.LBB0_595:
	v_mov_b32_e32 v152, v202
	v_mov_b32_e32 v153, v233
	v_mov_b32_e32 v154, v234
	v_mov_b32_e32 v155, v235
	ds_read_b128 v[158:161], v216
	ds_read_b128 v[162:165], v217
	ds_read_b128 v[166:169], v218
	ds_read_b128 v[170:173], v219
	ds_read_b128 v[148:151], v220
	ds_read_b128 v[144:147], v221
	ds_read_b128 v[140:143], v222
	ds_read_b128 v[136:139], v223
	s_add_i32 s4, s60, s66
	s_mov_b32 s42, s90
	s_add_i32 s90, s90, 1
	s_add_i32 s5, s4, 0x200
	s_add_i32 s67, s33, s66
	s_cmpk_eq_i32 s66, 0x200
	s_cselect_b32 s43, s87, s5
	s_cselect_b32 s93, s88, s67
	s_add_i32 s92, s43, 0x80
	s_mov_b32 m0, s78
	s_add_i32 s5, s4, 0x100180
	buffer_load_dwordx4 v213, s[12:15], s5 offen lds
	s_add_i32 s4, s4, 0x180180
	s_mov_b32 m0, s81
	s_add_i32 s94, s93, 0x80
	buffer_load_dwordx4 v213, s[12:15], s4 offen lds
	s_lshr_b32 s4, s90, 2
	s_mul_i32 s67, s4, s34
	s_add_i32 s67, s67, s2
	s_cmp_lt_i32 s4, s3
	s_cselect_b64 s[4:5], -1, 0
	s_and_b64 s[96:97], s[4:5], exec
	s_cselect_b32 s91, s67, 0
	s_ashr_i32 s96, s91, 7
	s_bfe_u32 s95, s90, 0x10001
	s_ashr_i32 s97, s96, 31
	s_or_b32 s95, s95, s79
	s_lshl_b64 s[96:97], s[96:97], 23
	s_add_u32 s96, s48, s96
	s_addc_u32 s97, s49, s97
	s_lshl_b32 vcc_lo, s91, 16
	s_and_b32 vcc_lo, vcc_lo, 0x600000
	s_add_u32 s96, s96, vcc_lo
	s_addc_u32 s97, s97, 0
	s_lshl_b32 s91, s91, 7
	s_and_b32 s91, s91, 0xf80
	s_lshl_b32 vcc_lo, s91, 2
	s_add_u32 s96, s96, vcc_lo
	v_and_or_b32 v202, s89, 2, v200
	s_addc_u32 s97, s97, 0
	v_lshl_or_b32 v156, s95, 5, v215
	v_lshlrev_b64 v[128:129], 14, v[202:203]
	v_lshl_add_u64 v[128:129], s[96:97], 0, v[128:129]
	v_lshlrev_b32_e32 v202, 2, v156
	v_lshl_add_u64 v[128:129], v[128:129], 0, v[202:203]
	s_movk_i32 s95, 0x4000
	v_add_co_u32_e32 v132, vcc, s95, v128
	s_nop 1
	v_addc_co_u32_e32 v133, vcc, 0, v129, vcc
	global_load_dwordx4 v[128:131], v[128:129], off nt
	s_nop 0
	global_load_dwordx4 v[132:135], v[132:133], off nt
	ds_read_b128 v[174:177], v232
	ds_read_b128 v[178:181], v232 offset:1024
	ds_read_b128 v[182:185], v232 offset:2048
	ds_read_b128 v[186:189], v232 offset:3072
	ds_read_b128 v[190:193], v232 offset:4096
	ds_read_b128 v[194:197], v232 offset:5120
	ds_read_b128 v[234:237], v232 offset:6144
	ds_read_b128 v[238:241], v232 offset:7168
	s_waitcnt vmcnt(10)
	s_waitcnt lgkmcnt(8)
	s_barrier
	s_setprio 1
	s_waitcnt lgkmcnt(7)
	v_mfma_f32_16x16x32_bf16 v[124:127], v[158:161], v[174:177], v[124:127]
	s_waitcnt lgkmcnt(6)
	v_mfma_f32_16x16x32_bf16 v[124:127], v[162:165], v[178:181], v[124:127]
	v_mfma_f32_16x16x32_bf16 v[120:123], v[166:169], v[174:177], v[120:123]
	s_nop 0
	v_mfma_f32_16x16x32_bf16 v[120:123], v[170:173], v[178:181], v[120:123]
	s_waitcnt lgkmcnt(5)
	v_mfma_f32_16x16x32_bf16 v[116:119], v[158:161], v[182:185], v[116:119]
	s_waitcnt lgkmcnt(4)
	v_mfma_f32_16x16x32_bf16 v[116:119], v[162:165], v[186:189], v[116:119]
	v_mfma_f32_16x16x32_bf16 v[112:115], v[166:169], v[182:185], v[112:115]
	s_nop 0
	v_mfma_f32_16x16x32_bf16 v[112:115], v[170:173], v[186:189], v[112:115]
	s_waitcnt lgkmcnt(3)
	v_mfma_f32_16x16x32_bf16 v[108:111], v[158:161], v[190:193], v[108:111]
	s_waitcnt lgkmcnt(2)
	v_mfma_f32_16x16x32_bf16 v[108:111], v[162:165], v[194:197], v[108:111]
	v_mfma_f32_16x16x32_bf16 v[104:107], v[166:169], v[190:193], v[104:107]
	s_nop 0
	v_mfma_f32_16x16x32_bf16 v[104:107], v[170:173], v[194:197], v[104:107]
	s_waitcnt lgkmcnt(1)
	v_mfma_f32_16x16x32_bf16 v[100:103], v[158:161], v[234:237], v[100:103]
	s_waitcnt lgkmcnt(0)
	v_mfma_f32_16x16x32_bf16 v[100:103], v[162:165], v[238:241], v[100:103]
	v_mfma_f32_16x16x32_bf16 v[96:99], v[166:169], v[234:237], v[96:99]
	s_nop 0
	v_mfma_f32_16x16x32_bf16 v[96:99], v[170:173], v[238:241], v[96:99]
	s_setprio 0
	s_setprio 1
	v_mfma_f32_16x16x32_bf16 v[92:95], v[148:151], v[174:177], v[92:95]
	s_nop 0
	v_mfma_f32_16x16x32_bf16 v[92:95], v[144:147], v[178:181], v[92:95]
	v_mfma_f32_16x16x32_bf16 v[88:91], v[140:143], v[174:177], v[88:91]
	s_nop 0
	v_mfma_f32_16x16x32_bf16 v[88:91], v[136:139], v[178:181], v[88:91]
	v_mfma_f32_16x16x32_bf16 v[84:87], v[148:151], v[182:185], v[84:87]
	s_nop 0
	v_mfma_f32_16x16x32_bf16 v[84:87], v[144:147], v[186:189], v[84:87]
	v_mfma_f32_16x16x32_bf16 v[80:83], v[140:143], v[182:185], v[80:83]
	s_nop 0
	v_mfma_f32_16x16x32_bf16 v[80:83], v[136:139], v[186:189], v[80:83]
	v_mfma_f32_16x16x32_bf16 v[76:79], v[148:151], v[190:193], v[76:79]
	s_nop 0
	v_mfma_f32_16x16x32_bf16 v[76:79], v[144:147], v[194:197], v[76:79]
	v_mfma_f32_16x16x32_bf16 v[72:75], v[140:143], v[190:193], v[72:75]
	s_nop 0
	v_mfma_f32_16x16x32_bf16 v[72:75], v[136:139], v[194:197], v[72:75]
	v_mfma_f32_16x16x32_bf16 v[68:71], v[148:151], v[234:237], v[68:71]
	s_nop 0
	v_mfma_f32_16x16x32_bf16 v[68:71], v[144:147], v[238:241], v[68:71]
	v_mfma_f32_16x16x32_bf16 v[64:67], v[140:143], v[234:237], v[64:67]
	s_nop 0
	v_mfma_f32_16x16x32_bf16 v[64:67], v[136:139], v[238:241], v[64:67]
	s_setprio 0
	s_barrier
	s_mov_b32 m0, s47
	s_add_i32 s95, s93, 0x40000
	buffer_load_dwordx4 v214, s[8:11], s93 offen lds
	s_mov_b32 m0, s62
	s_nop 0
	buffer_load_dwordx4 v214, s[8:11], s95 offen lds
	s_add_i32 s95, s93, 0x4000
	s_mov_b32 m0, s63
	s_nop 0
	buffer_load_dwordx4 v214, s[8:11], s95 offen lds
	s_add_i32 s95, s93, 0x44000
	s_mov_b32 m0, s64
	s_nop 0
	buffer_load_dwordx4 v214, s[8:11], s95 offen lds
	s_mov_b32 m0, s46
	s_add_i32 s95, s43, 0x80000
	buffer_load_dwordx4 v213, s[12:15], s43 offen lds
	s_mov_b32 m0, s65
	s_nop 0
	buffer_load_dwordx4 v213, s[12:15], s95 offen lds
	ds_read_b128 v[174:177], v232 offset:16384
	ds_read_b128 v[178:181], v232 offset:17408
	ds_read_b128 v[182:185], v232 offset:18432
	ds_read_b128 v[186:189], v232 offset:19456
	ds_read_b128 v[190:193], v232 offset:20480
	ds_read_b128 v[194:197], v232 offset:21504
	ds_read_b128 v[234:237], v232 offset:22528
	ds_read_b128 v[238:241], v232 offset:23552
	s_waitcnt vmcnt(10)
	s_waitcnt lgkmcnt(6)
	s_barrier
	s_setprio 1
	s_waitcnt lgkmcnt(7)
	v_mfma_f32_16x16x32_bf16 v[60:63], v[158:161], v[174:177], v[60:63]
	s_waitcnt lgkmcnt(6)
	v_mfma_f32_16x16x32_bf16 v[60:63], v[162:165], v[178:181], v[60:63]
	v_mfma_f32_16x16x32_bf16 v[56:59], v[166:169], v[174:177], v[56:59]
	s_nop 0
	v_mfma_f32_16x16x32_bf16 v[56:59], v[170:173], v[178:181], v[56:59]
	s_waitcnt lgkmcnt(5)
	v_mfma_f32_16x16x32_bf16 v[52:55], v[158:161], v[182:185], v[52:55]
	s_waitcnt lgkmcnt(4)
	v_mfma_f32_16x16x32_bf16 v[52:55], v[162:165], v[186:189], v[52:55]
	v_mfma_f32_16x16x32_bf16 v[48:51], v[166:169], v[182:185], v[48:51]
	s_nop 0
	v_mfma_f32_16x16x32_bf16 v[48:51], v[170:173], v[186:189], v[48:51]
	s_waitcnt lgkmcnt(3)
	v_mfma_f32_16x16x32_bf16 v[44:47], v[158:161], v[190:193], v[44:47]
	s_waitcnt lgkmcnt(2)
	v_mfma_f32_16x16x32_bf16 v[44:47], v[162:165], v[194:197], v[44:47]
	v_mfma_f32_16x16x32_bf16 v[40:43], v[166:169], v[190:193], v[40:43]
	s_nop 0
	v_mfma_f32_16x16x32_bf16 v[40:43], v[170:173], v[194:197], v[40:43]
	s_waitcnt lgkmcnt(1)
	v_mfma_f32_16x16x32_bf16 v[36:39], v[158:161], v[234:237], v[36:39]
	s_waitcnt lgkmcnt(0)
	v_mfma_f32_16x16x32_bf16 v[36:39], v[162:165], v[238:241], v[36:39]
	v_mfma_f32_16x16x32_bf16 v[32:35], v[166:169], v[234:237], v[32:35]
	s_nop 0
	v_mfma_f32_16x16x32_bf16 v[32:35], v[170:173], v[238:241], v[32:35]
	s_setprio 0
	s_setprio 1
	v_mfma_f32_16x16x32_bf16 v[28:31], v[148:151], v[174:177], v[28:31]
	s_nop 0
	v_mfma_f32_16x16x32_bf16 v[28:31], v[144:147], v[178:181], v[28:31]
	v_mfma_f32_16x16x32_bf16 v[24:27], v[140:143], v[174:177], v[24:27]
	s_nop 0
	v_mfma_f32_16x16x32_bf16 v[24:27], v[136:139], v[178:181], v[24:27]
	v_mfma_f32_16x16x32_bf16 v[20:23], v[148:151], v[182:185], v[20:23]
	s_nop 0
	v_mfma_f32_16x16x32_bf16 v[20:23], v[144:147], v[186:189], v[20:23]
	v_mfma_f32_16x16x32_bf16 v[16:19], v[140:143], v[182:185], v[16:19]
	s_nop 0
	v_mfma_f32_16x16x32_bf16 v[16:19], v[136:139], v[186:189], v[16:19]
	v_mfma_f32_16x16x32_bf16 v[12:15], v[148:151], v[190:193], v[12:15]
	s_nop 0
	v_mfma_f32_16x16x32_bf16 v[12:15], v[144:147], v[194:197], v[12:15]
	v_mfma_f32_16x16x32_bf16 v[8:11], v[140:143], v[190:193], v[8:11]
	s_nop 0
	v_mfma_f32_16x16x32_bf16 v[8:11], v[136:139], v[194:197], v[8:11]
	v_mfma_f32_16x16x32_bf16 v[4:7], v[148:151], v[234:237], v[4:7]
	s_nop 0
	v_mfma_f32_16x16x32_bf16 v[4:7], v[144:147], v[238:241], v[4:7]
	v_mfma_f32_16x16x32_bf16 v[0:3], v[140:143], v[234:237], v[0:3]
	s_nop 0
	v_mfma_f32_16x16x32_bf16 v[0:3], v[136:139], v[238:241], v[0:3]
	s_setprio 0
	s_barrier
	ds_read_b128 v[136:139], v224
	ds_read_b128 v[140:143], v225
	ds_read_b128 v[144:147], v226
	ds_read_b128 v[148:151], v227
	ds_read_b128 v[158:161], v228
	ds_read_b128 v[162:165], v229
	ds_read_b128 v[166:169], v230
	ds_read_b128 v[170:173], v231
	s_mov_b32 m0, s68
	s_add_i32 s95, s43, 0x100000
	buffer_load_dwordx4 v213, s[12:15], s95 offen lds
	s_add_i32 s95, s43, 0x180000
	s_mov_b32 m0, s69
	s_nop 0
	buffer_load_dwordx4 v213, s[12:15], s95 offen lds
	ds_read_b128 v[174:177], v232 offset:32768
	ds_read_b128 v[178:181], v232 offset:33792
	ds_read_b128 v[182:185], v232 offset:34816
	ds_read_b128 v[186:189], v232 offset:35840
	ds_read_b128 v[190:193], v232 offset:36864
	ds_read_b128 v[194:197], v232 offset:37888
	ds_read_b128 v[234:237], v232 offset:38912
	ds_read_b128 v[238:241], v232 offset:39936
	s_waitcnt vmcnt(10)
	s_waitcnt lgkmcnt(8)
	s_barrier
	s_setprio 1
	s_waitcnt lgkmcnt(7)
	v_mfma_f32_16x16x32_bf16 v[124:127], v[136:139], v[174:177], v[124:127]
	s_waitcnt lgkmcnt(6)
	v_mfma_f32_16x16x32_bf16 v[124:127], v[140:143], v[178:181], v[124:127]
	v_mfma_f32_16x16x32_bf16 v[120:123], v[144:147], v[174:177], v[120:123]
	s_nop 0
	v_mfma_f32_16x16x32_bf16 v[120:123], v[148:151], v[178:181], v[120:123]
	s_waitcnt lgkmcnt(5)
	v_mfma_f32_16x16x32_bf16 v[116:119], v[136:139], v[182:185], v[116:119]
	s_waitcnt lgkmcnt(4)
	v_mfma_f32_16x16x32_bf16 v[116:119], v[140:143], v[186:189], v[116:119]
	v_mfma_f32_16x16x32_bf16 v[112:115], v[144:147], v[182:185], v[112:115]
	s_nop 0
	v_mfma_f32_16x16x32_bf16 v[112:115], v[148:151], v[186:189], v[112:115]
	s_waitcnt lgkmcnt(3)
	v_mfma_f32_16x16x32_bf16 v[108:111], v[136:139], v[190:193], v[108:111]
	s_waitcnt lgkmcnt(2)
	v_mfma_f32_16x16x32_bf16 v[108:111], v[140:143], v[194:197], v[108:111]
	v_mfma_f32_16x16x32_bf16 v[104:107], v[144:147], v[190:193], v[104:107]
	s_nop 0
	v_mfma_f32_16x16x32_bf16 v[104:107], v[148:151], v[194:197], v[104:107]
	s_waitcnt lgkmcnt(1)
	v_mfma_f32_16x16x32_bf16 v[100:103], v[136:139], v[234:237], v[100:103]
	s_waitcnt lgkmcnt(0)
	v_mfma_f32_16x16x32_bf16 v[100:103], v[140:143], v[238:241], v[100:103]
	v_mfma_f32_16x16x32_bf16 v[96:99], v[144:147], v[234:237], v[96:99]
	s_nop 0
	v_mfma_f32_16x16x32_bf16 v[96:99], v[148:151], v[238:241], v[96:99]
	s_setprio 0
	s_setprio 1
	v_mfma_f32_16x16x32_bf16 v[92:95], v[158:161], v[174:177], v[92:95]
	s_nop 0
	v_mfma_f32_16x16x32_bf16 v[92:95], v[162:165], v[178:181], v[92:95]
	v_mfma_f32_16x16x32_bf16 v[88:91], v[166:169], v[174:177], v[88:91]
	s_nop 0
	v_mfma_f32_16x16x32_bf16 v[88:91], v[170:173], v[178:181], v[88:91]
	v_mfma_f32_16x16x32_bf16 v[84:87], v[158:161], v[182:185], v[84:87]
	s_nop 0
	v_mfma_f32_16x16x32_bf16 v[84:87], v[162:165], v[186:189], v[84:87]
	v_mfma_f32_16x16x32_bf16 v[80:83], v[166:169], v[182:185], v[80:83]
	s_nop 0
	v_mfma_f32_16x16x32_bf16 v[80:83], v[170:173], v[186:189], v[80:83]
	v_mfma_f32_16x16x32_bf16 v[76:79], v[158:161], v[190:193], v[76:79]
	s_nop 0
	v_mfma_f32_16x16x32_bf16 v[76:79], v[162:165], v[194:197], v[76:79]
	v_mfma_f32_16x16x32_bf16 v[72:75], v[166:169], v[190:193], v[72:75]
	s_nop 0
	v_mfma_f32_16x16x32_bf16 v[72:75], v[170:173], v[194:197], v[72:75]
	v_mfma_f32_16x16x32_bf16 v[68:71], v[158:161], v[234:237], v[68:71]
	s_nop 0
	v_mfma_f32_16x16x32_bf16 v[68:71], v[162:165], v[238:241], v[68:71]
	v_mfma_f32_16x16x32_bf16 v[64:67], v[166:169], v[234:237], v[64:67]
	s_nop 0
	v_mfma_f32_16x16x32_bf16 v[64:67], v[170:173], v[238:241], v[64:67]
	s_setprio 0
	s_barrier
	s_mov_b32 m0, s72
	s_add_i32 s43, s43, 0x80080
	buffer_load_dwordx4 v214, s[8:11], s94 offen lds
	s_add_i32 s94, s93, 0x40080
	s_mov_b32 m0, s73
	s_nop 0
	buffer_load_dwordx4 v214, s[8:11], s94 offen lds
	s_add_i32 s94, s93, 0x4080
	s_mov_b32 m0, s76
	s_add_i32 s93, s93, 0x44080
	buffer_load_dwordx4 v214, s[8:11], s94 offen lds
	s_mov_b32 m0, s77
	s_nop 0
	buffer_load_dwordx4 v214, s[8:11], s93 offen lds
	s_mov_b32 m0, s74
	s_nop 0
	buffer_load_dwordx4 v213, s[12:15], s92 offen lds
	s_mov_b32 m0, s75
	s_nop 0
	buffer_load_dwordx4 v213, s[12:15], s43 offen lds
	ds_read_b128 v[174:177], v232 offset:49152
	ds_read_b128 v[178:181], v232 offset:50176
	ds_read_b128 v[182:185], v232 offset:51200
	ds_read_b128 v[186:189], v232 offset:52224
	ds_read_b128 v[190:193], v232 offset:53248
	ds_read_b128 v[194:197], v232 offset:54272
	ds_read_b128 v[234:237], v232 offset:55296
	ds_read_b128 v[238:241], v232 offset:56320
	s_waitcnt vmcnt(8)
	s_waitcnt lgkmcnt(6)
	s_barrier
	s_setprio 1
	s_waitcnt lgkmcnt(7)
	v_mfma_f32_16x16x32_bf16 v[60:63], v[136:139], v[174:177], v[60:63]
	s_waitcnt lgkmcnt(6)
	v_mfma_f32_16x16x32_bf16 v[60:63], v[140:143], v[178:181], v[60:63]
	v_mfma_f32_16x16x32_bf16 v[56:59], v[144:147], v[174:177], v[56:59]
	s_nop 0
	v_mfma_f32_16x16x32_bf16 v[56:59], v[148:151], v[178:181], v[56:59]
	s_waitcnt lgkmcnt(5)
	v_mfma_f32_16x16x32_bf16 v[52:55], v[136:139], v[182:185], v[52:55]
	s_waitcnt lgkmcnt(4)
	v_mfma_f32_16x16x32_bf16 v[52:55], v[140:143], v[186:189], v[52:55]
	v_mfma_f32_16x16x32_bf16 v[48:51], v[144:147], v[182:185], v[48:51]
	s_nop 0
	v_mfma_f32_16x16x32_bf16 v[48:51], v[148:151], v[186:189], v[48:51]
	s_waitcnt lgkmcnt(3)
	v_mfma_f32_16x16x32_bf16 v[44:47], v[136:139], v[190:193], v[44:47]
	s_waitcnt lgkmcnt(2)
	v_mfma_f32_16x16x32_bf16 v[44:47], v[140:143], v[194:197], v[44:47]
	v_mfma_f32_16x16x32_bf16 v[40:43], v[144:147], v[190:193], v[40:43]
	s_nop 0
	v_mfma_f32_16x16x32_bf16 v[40:43], v[148:151], v[194:197], v[40:43]
	s_waitcnt lgkmcnt(1)
	v_mfma_f32_16x16x32_bf16 v[36:39], v[136:139], v[234:237], v[36:39]
	s_waitcnt lgkmcnt(0)
	v_mfma_f32_16x16x32_bf16 v[36:39], v[140:143], v[238:241], v[36:39]
	v_mfma_f32_16x16x32_bf16 v[32:35], v[144:147], v[234:237], v[32:35]
	s_nop 0
	v_mfma_f32_16x16x32_bf16 v[32:35], v[148:151], v[238:241], v[32:35]
	s_setprio 0
	s_setprio 1
	v_mfma_f32_16x16x32_bf16 v[28:31], v[158:161], v[174:177], v[28:31]
	s_nop 0
	v_mfma_f32_16x16x32_bf16 v[28:31], v[162:165], v[178:181], v[28:31]
	v_mfma_f32_16x16x32_bf16 v[24:27], v[166:169], v[174:177], v[24:27]
	s_nop 0
	v_mfma_f32_16x16x32_bf16 v[24:27], v[170:173], v[178:181], v[24:27]
	v_mfma_f32_16x16x32_bf16 v[20:23], v[158:161], v[182:185], v[20:23]
	s_nop 0
	v_mfma_f32_16x16x32_bf16 v[20:23], v[162:165], v[186:189], v[20:23]
	v_mfma_f32_16x16x32_bf16 v[16:19], v[166:169], v[182:185], v[16:19]
	s_nop 0
	v_mfma_f32_16x16x32_bf16 v[16:19], v[170:173], v[186:189], v[16:19]
	v_mfma_f32_16x16x32_bf16 v[12:15], v[158:161], v[190:193], v[12:15]
	s_nop 0
	v_mfma_f32_16x16x32_bf16 v[12:15], v[162:165], v[194:197], v[12:15]
	v_mfma_f32_16x16x32_bf16 v[8:11], v[166:169], v[190:193], v[8:11]
	s_nop 0
	v_mfma_f32_16x16x32_bf16 v[8:11], v[170:173], v[194:197], v[8:11]
	v_mfma_f32_16x16x32_bf16 v[4:7], v[158:161], v[234:237], v[4:7]
	s_nop 0
	v_mfma_f32_16x16x32_bf16 v[4:7], v[162:165], v[238:241], v[4:7]
	v_mfma_f32_16x16x32_bf16 v[0:3], v[166:169], v[234:237], v[0:3]
	s_nop 0
	v_mfma_f32_16x16x32_bf16 v[0:3], v[170:173], v[238:241], v[0:3]
	s_setprio 0
	s_barrier
	s_bitcmp0_b32 s42, 0
	s_waitcnt vmcnt(15)
	v_mul_f32_e32 v128, 0x42800000, v128
	s_waitcnt vmcnt(14)
	v_mul_f32_e32 v132, 0x42800000, v132
	v_mul_f32_e32 v129, 0x42800000, v129
	v_mul_f32_e32 v133, 0x42800000, v133
	v_mul_f32_e32 v130, 0x42800000, v130
	v_mul_f32_e32 v134, 0x42800000, v134
	v_mul_f32_e32 v131, 0x42800000, v131
	v_mul_f32_e32 v135, 0x42800000, v135
	s_mov_b64 s[42:43], -1
	s_cbranch_scc0 .LBB0_598
	s_andn2_b64 vcc, exec, s[42:43]
	s_cbranch_vccnz .LBB0_594
	s_branch .LBB0_599

.LBB0_917:
	s_lshl_b32 s3, s91, 20
	ds_read_b128 v[24:27], v217 offset:0
	ds_read_b128 v[28:31], v217 offset:0x400
	ds_read_b128 v[16:19], v217 offset:0x800
	ds_read_b128 v[20:23], v217 offset:0xc00
	s_and_b64 s[4:5], s[4:5], exec
	s_cselect_b32 s95, s3, s36
	s_mov_b32 m0, s86
	s_add_i32 s3, s94, 0x80080
	ds_read_b128 v[56:59], v216 offset:0
	ds_read_b128 v[60:63], v216 offset:0x400
	ds_read_b128 v[48:51], v216 offset:0x800
	ds_read_b128 v[52:55], v216 offset:0xc00
	ds_read_b128 v[40:43], v216 offset:0x1000
	ds_read_b128 v[44:47], v216 offset:0x1400
	ds_read_b128 v[32:35], v216 offset:0x1800
	ds_read_b128 v[36:39], v216 offset:0x1c00
	ds_read_b128 v[8:11], v217 offset:0x4000
	ds_read_b128 v[12:15], v217 offset:0x4400
	ds_read_b128 v[0:3], v217 offset:0x4800
	ds_read_b128 v[4:7], v217 offset:0x4c00
	buffer_load_dwordx4 v214, s[12:15], s3 offen lds
	s_add_i32 s3, s94, 0xc0080
	s_mov_b32 m0, s89
	v_mov_b32_e32 v211, v203
	buffer_load_dwordx4 v214, s[12:15], s3 offen lds
	s_lshr_b32 s3, s68, 2
	s_mul_i32 s4, s3, s34
	s_add_i32 s4, s4, s2
	s_cmp_lt_i32 s3, s47
	s_cselect_b32 s3, s4, 0
	s_ashr_i32 s4, s3, 7
	s_ashr_i32 s5, s4, 31
	s_lshl_b64 s[4:5], s[4:5], 23
	s_add_u32 s4, s28, s4
	s_addc_u32 s5, s29, s5
	s_lshl_b32 s11, s3, 16
	s_and_b32 s11, s11, 0x600000
	s_add_u32 s4, s4, s11
	s_addc_u32 s5, s5, 0
	s_lshl_b32 s3, s3, 9
	s_and_b32 s3, s3, 0x3e00
	s_add_u32 s4, s4, s3
	s_addc_u32 s5, s5, 0
	v_lshl_add_u64 v[192:193], s[4:5], 0, v[204:205]
	v_lshl_add_u64 v[192:193], v[192:193], 0, v[210:211]
	v_add_co_u32_e32 v196, vcc, 0x4000, v192
	s_cmp_lg_u32 s10, 0
	s_nop 0
	v_addc_co_u32_e32 v197, vcc, 0, v193, vcc
	global_load_dwordx4 v[192:195], v[192:193], off nt
	s_nop 0
	global_load_dwordx4 v[196:199], v[196:197], off nt
	s_cselect_b64 s[4:5], -1, 0
	s_and_b64 vcc, exec, s[4:5]
	s_cbranch_vccz .LBB0_937
	s_waitcnt vmcnt(54)
	s_cbranch_execnz .LBB0_920

.LBB0_920:
	s_add_i32 s3, s94, 0x100
	s_add_i32 s16, s36, 0x100
	s_waitcnt lgkmcnt(4)
	s_barrier
	s_setprio 1
	v_mfma_scale_f32_16x16x128_f8f6f4 v[188:191], v[24:31], v[56:63], 0, v213, v213 op_sel_hi:[0,0,0]
	v_mfma_scale_f32_16x16x128_f8f6f4 v[184:187], v[16:23], v[56:63], 0, v213, v213 op_sel_hi:[0,0,0]
	v_mfma_scale_f32_16x16x128_f8f6f4 v[180:183], v[24:31], v[48:55], 0, v213, v213 op_sel_hi:[0,0,0]
	v_mfma_scale_f32_16x16x128_f8f6f4 v[176:179], v[16:23], v[48:55], 0, v213, v213 op_sel_hi:[0,0,0]
	v_mfma_scale_f32_16x16x128_f8f6f4 v[172:175], v[24:31], v[40:47], 0, v213, v213 op_sel_hi:[0,0,0]
	v_mfma_scale_f32_16x16x128_f8f6f4 v[168:171], v[16:23], v[40:47], 0, v213, v213 op_sel_hi:[0,0,0]
	v_mfma_scale_f32_16x16x128_f8f6f4 v[164:167], v[24:31], v[32:39], 0, v213, v213 op_sel_hi:[0,0,0]
	v_mfma_scale_f32_16x16x128_f8f6f4 v[160:163], v[16:23], v[32:39], 0, v213, v213 op_sel_hi:[0,0,0]
	s_waitcnt lgkmcnt(0)
	s_setprio 0
	s_setprio 1
	v_mfma_scale_f32_16x16x128_f8f6f4 v[156:159], v[8:15], v[56:63], 0, v213, v213 op_sel_hi:[0,0,0]
	v_mfma_scale_f32_16x16x128_f8f6f4 v[152:155], v[0:7], v[56:63], 0, v213, v213 op_sel_hi:[0,0,0]
	v_mfma_scale_f32_16x16x128_f8f6f4 v[148:151], v[8:15], v[48:55], 0, v213, v213 op_sel_hi:[0,0,0]
	v_mfma_scale_f32_16x16x128_f8f6f4 v[144:147], v[0:7], v[48:55], 0, v213, v213 op_sel_hi:[0,0,0]
	v_mfma_scale_f32_16x16x128_f8f6f4 v[140:143], v[8:15], v[40:47], 0, v213, v213 op_sel_hi:[0,0,0]
	v_mfma_scale_f32_16x16x128_f8f6f4 v[136:139], v[0:7], v[40:47], 0, v213, v213 op_sel_hi:[0,0,0]
	v_mfma_scale_f32_16x16x128_f8f6f4 v[132:135], v[8:15], v[32:39], 0, v213, v213 op_sel_hi:[0,0,0]
	v_mfma_scale_f32_16x16x128_f8f6f4 v[128:131], v[0:7], v[32:39], 0, v213, v213 op_sel_hi:[0,0,0]
	s_setprio 0
	s_barrier
	s_mov_b32 m0, s71
	s_mov_b32 s10, s14
	s_mov_b32 s11, s15
	ds_read_b128 v[56:59], v216 offset:0x4000
	ds_read_b128 v[60:63], v216 offset:0x4400
	ds_read_b128 v[48:51], v216 offset:0x4800
	ds_read_b128 v[52:55], v216 offset:0x4c00
	ds_read_b128 v[40:43], v216 offset:0x5000
	ds_read_b128 v[44:47], v216 offset:0x5400
	ds_read_b128 v[32:35], v216 offset:0x5800
	ds_read_b128 v[36:39], v216 offset:0x5c00
	buffer_load_dwordx4 v215, s[8:11], s16 offen lds
	s_add_i32 s16, s36, 0x80100
	s_mov_b32 m0, s72
	s_and_b64 vcc, exec, s[4:5]
	buffer_load_dwordx4 v215, s[8:11], s16 offen lds
	s_add_i32 s16, s36, 0x8100
	s_mov_b32 m0, s73
	s_nop 0
	buffer_load_dwordx4 v215, s[8:11], s16 offen lds
	s_add_i32 s16, s36, 0x88100
	s_mov_b32 m0, s74
	s_nop 0
	buffer_load_dwordx4 v215, s[8:11], s16 offen lds
	s_mov_b32 m0, s70
	s_nop 0
	buffer_load_dwordx4 v214, s[12:15], s3 offen lds
	s_add_i32 s3, s94, 0x40100
	s_mov_b32 m0, s75
	s_nop 0
	buffer_load_dwordx4 v214, s[12:15], s3 offen lds
	s_cbranch_vccz .LBB0_938
	s_waitcnt vmcnt(54)
	s_cbranch_execnz .LBB0_923

.LBB0_923:
	s_add_i32 s3, s94, 0x180
	s_add_i32 s4, s36, 0x180
	s_waitcnt lgkmcnt(0)
	s_barrier
	s_setprio 1
	v_mfma_scale_f32_16x16x128_f8f6f4 v[124:127], v[24:31], v[56:63], 0, v213, v213 op_sel_hi:[0,0,0]
	v_mfma_scale_f32_16x16x128_f8f6f4 v[120:123], v[16:23], v[56:63], 0, v213, v213 op_sel_hi:[0,0,0]
	v_mfma_scale_f32_16x16x128_f8f6f4 v[116:119], v[24:31], v[48:55], 0, v213, v213 op_sel_hi:[0,0,0]
	v_mfma_scale_f32_16x16x128_f8f6f4 v[112:115], v[16:23], v[48:55], 0, v213, v213 op_sel_hi:[0,0,0]
	v_mfma_scale_f32_16x16x128_f8f6f4 v[108:111], v[24:31], v[40:47], 0, v213, v213 op_sel_hi:[0,0,0]
	v_mfma_scale_f32_16x16x128_f8f6f4 v[104:107], v[16:23], v[40:47], 0, v213, v213 op_sel_hi:[0,0,0]
	v_mfma_scale_f32_16x16x128_f8f6f4 v[100:103], v[24:31], v[32:39], 0, v213, v213 op_sel_hi:[0,0,0]
	v_mfma_scale_f32_16x16x128_f8f6f4 v[96:99], v[16:23], v[32:39], 0, v213, v213 op_sel_hi:[0,0,0]
	s_setprio 0
	s_setprio 1
	v_mfma_scale_f32_16x16x128_f8f6f4 v[92:95], v[8:15], v[56:63], 0, v213, v213 op_sel_hi:[0,0,0]
	v_mfma_scale_f32_16x16x128_f8f6f4 v[88:91], v[0:7], v[56:63], 0, v213, v213 op_sel_hi:[0,0,0]
	v_mfma_scale_f32_16x16x128_f8f6f4 v[84:87], v[8:15], v[48:55], 0, v213, v213 op_sel_hi:[0,0,0]
	v_mfma_scale_f32_16x16x128_f8f6f4 v[80:83], v[0:7], v[48:55], 0, v213, v213 op_sel_hi:[0,0,0]
	v_mfma_scale_f32_16x16x128_f8f6f4 v[76:79], v[8:15], v[40:47], 0, v213, v213 op_sel_hi:[0,0,0]
	v_mfma_scale_f32_16x16x128_f8f6f4 v[72:75], v[0:7], v[40:47], 0, v213, v213 op_sel_hi:[0,0,0]
	v_mfma_scale_f32_16x16x128_f8f6f4 v[68:71], v[8:15], v[32:39], 0, v213, v213 op_sel_hi:[0,0,0]
	v_mfma_scale_f32_16x16x128_f8f6f4 v[64:67], v[0:7], v[32:39], 0, v213, v213 op_sel_hi:[0,0,0]
	s_setprio 0
	s_barrier
	ds_read_b128 v[24:27], v217 offset:0x8000
	ds_read_b128 v[28:31], v217 offset:0x8400
	ds_read_b128 v[16:19], v217 offset:0x8800
	ds_read_b128 v[20:23], v217 offset:0x8c00
	s_mov_b32 m0, s76
	s_add_i32 s5, s94, 0x80100
	ds_read_b128 v[32:35], v216 offset:0x8000
	ds_read_b128 v[36:39], v216 offset:0x8400
	ds_read_b128 v[40:43], v216 offset:0x8800
	ds_read_b128 v[44:47], v216 offset:0x8c00
	ds_read_b128 v[48:51], v216 offset:0x9000
	ds_read_b128 v[52:55], v216 offset:0x9400
	ds_read_b128 v[56:59], v216 offset:0x9800
	ds_read_b128 v[60:63], v216 offset:0x9c00
	ds_read_b128 v[8:11], v217 offset:0xc000
	ds_read_b128 v[12:15], v217 offset:0xc400
	ds_read_b128 v[0:3], v217 offset:0xc800
	ds_read_b128 v[4:7], v217 offset:0xcc00
	buffer_load_dwordx4 v214, s[12:15], s5 offen lds
	s_add_i32 s5, s94, 0xc0100
	s_mov_b32 m0, s77
	s_nop 0
	buffer_load_dwordx4 v214, s[12:15], s5 offen lds
	s_waitcnt vmcnt(10)
	s_waitcnt lgkmcnt(4)
	s_barrier
	s_setprio 1
	v_mfma_scale_f32_16x16x128_f8f6f4 v[188:191], v[24:31], v[32:39], v[188:191], v213, v213 op_sel_hi:[0,0,0]
	v_mfma_scale_f32_16x16x128_f8f6f4 v[184:187], v[16:23], v[32:39], v[184:187], v213, v213 op_sel_hi:[0,0,0]
	v_mfma_scale_f32_16x16x128_f8f6f4 v[180:183], v[24:31], v[40:47], v[180:183], v213, v213 op_sel_hi:[0,0,0]
	v_mfma_scale_f32_16x16x128_f8f6f4 v[176:179], v[16:23], v[40:47], v[176:179], v213, v213 op_sel_hi:[0,0,0]
	v_mfma_scale_f32_16x16x128_f8f6f4 v[172:175], v[24:31], v[48:55], v[172:175], v213, v213 op_sel_hi:[0,0,0]
	v_mfma_scale_f32_16x16x128_f8f6f4 v[168:171], v[16:23], v[48:55], v[168:171], v213, v213 op_sel_hi:[0,0,0]
	v_mfma_scale_f32_16x16x128_f8f6f4 v[164:167], v[24:31], v[56:63], v[164:167], v213, v213 op_sel_hi:[0,0,0]
	v_mfma_scale_f32_16x16x128_f8f6f4 v[160:163], v[16:23], v[56:63], v[160:163], v213, v213 op_sel_hi:[0,0,0]
	s_waitcnt lgkmcnt(0)
	s_setprio 0
	s_setprio 1
	v_mfma_scale_f32_16x16x128_f8f6f4 v[156:159], v[8:15], v[32:39], v[156:159], v213, v213 op_sel_hi:[0,0,0]
	v_mfma_scale_f32_16x16x128_f8f6f4 v[152:155], v[0:7], v[32:39], v[152:155], v213, v213 op_sel_hi:[0,0,0]
	v_mfma_scale_f32_16x16x128_f8f6f4 v[148:151], v[8:15], v[40:47], v[148:151], v213, v213 op_sel_hi:[0,0,0]
	v_mfma_scale_f32_16x16x128_f8f6f4 v[144:147], v[0:7], v[40:47], v[144:147], v213, v213 op_sel_hi:[0,0,0]
	v_mfma_scale_f32_16x16x128_f8f6f4 v[140:143], v[8:15], v[48:55], v[140:143], v213, v213 op_sel_hi:[0,0,0]
	v_mfma_scale_f32_16x16x128_f8f6f4 v[136:139], v[0:7], v[48:55], v[136:139], v213, v213 op_sel_hi:[0,0,0]
	v_mfma_scale_f32_16x16x128_f8f6f4 v[132:135], v[8:15], v[56:63], v[132:135], v213, v213 op_sel_hi:[0,0,0]
	v_mfma_scale_f32_16x16x128_f8f6f4 v[128:131], v[0:7], v[56:63], v[128:131], v213, v213 op_sel_hi:[0,0,0]
	s_setprio 0
	s_barrier
	s_mov_b32 m0, s80
	s_mov_b32 s10, s14
	s_mov_b32 s11, s15
	ds_read_b128 v[32:35], v216 offset:0xc000
	ds_read_b128 v[36:39], v216 offset:0xc400
	ds_read_b128 v[40:43], v216 offset:0xc800
	ds_read_b128 v[44:47], v216 offset:0xcc00
	ds_read_b128 v[48:51], v216 offset:0xd000
	ds_read_b128 v[52:55], v216 offset:0xd400
	ds_read_b128 v[56:59], v216 offset:0xd800
	ds_read_b128 v[60:63], v216 offset:0xdc00
	buffer_load_dwordx4 v215, s[8:11], s4 offen lds
	s_add_i32 s4, s36, 0x80180
	s_mov_b32 m0, s81
	s_nop 0
	buffer_load_dwordx4 v215, s[8:11], s4 offen lds
	s_add_i32 s4, s36, 0x8180
	s_mov_b32 m0, s84
	s_nop 0
	buffer_load_dwordx4 v215, s[8:11], s4 offen lds
	s_add_i32 s4, s36, 0x88180
	s_mov_b32 m0, s85
	s_nop 0
	buffer_load_dwordx4 v215, s[8:11], s4 offen lds
	s_mov_b32 m0, s82
	s_nop 0
	buffer_load_dwordx4 v214, s[12:15], s3 offen lds
	s_add_i32 s3, s94, 0x40180
	s_mov_b32 m0, s83
	s_nop 0
	buffer_load_dwordx4 v214, s[12:15], s3 offen lds
	s_waitcnt vmcnt(8)
	s_waitcnt lgkmcnt(0)
	s_barrier
	s_setprio 1
	v_mfma_scale_f32_16x16x128_f8f6f4 v[124:127], v[24:31], v[32:39], v[124:127], v213, v213 op_sel_hi:[0,0,0]
	v_mfma_scale_f32_16x16x128_f8f6f4 v[120:123], v[16:23], v[32:39], v[120:123], v213, v213 op_sel_hi:[0,0,0]
	v_mfma_scale_f32_16x16x128_f8f6f4 v[116:119], v[24:31], v[40:47], v[116:119], v213, v213 op_sel_hi:[0,0,0]
	v_mfma_scale_f32_16x16x128_f8f6f4 v[112:115], v[16:23], v[40:47], v[112:115], v213, v213 op_sel_hi:[0,0,0]
	v_mfma_scale_f32_16x16x128_f8f6f4 v[108:111], v[24:31], v[48:55], v[108:111], v213, v213 op_sel_hi:[0,0,0]
	v_mfma_scale_f32_16x16x128_f8f6f4 v[104:107], v[16:23], v[48:55], v[104:107], v213, v213 op_sel_hi:[0,0,0]
	v_mfma_scale_f32_16x16x128_f8f6f4 v[100:103], v[24:31], v[56:63], v[100:103], v213, v213 op_sel_hi:[0,0,0]
	v_mfma_scale_f32_16x16x128_f8f6f4 v[96:99], v[16:23], v[56:63], v[96:99], v213, v213 op_sel_hi:[0,0,0]
	s_setprio 0
	s_setprio 1
	v_mfma_scale_f32_16x16x128_f8f6f4 v[92:95], v[8:15], v[32:39], v[92:95], v213, v213 op_sel_hi:[0,0,0]
	v_mfma_scale_f32_16x16x128_f8f6f4 v[88:91], v[0:7], v[32:39], v[88:91], v213, v213 op_sel_hi:[0,0,0]
	v_mfma_scale_f32_16x16x128_f8f6f4 v[84:87], v[8:15], v[40:47], v[84:87], v213, v213 op_sel_hi:[0,0,0]
	v_mfma_scale_f32_16x16x128_f8f6f4 v[80:83], v[0:7], v[40:47], v[80:83], v213, v213 op_sel_hi:[0,0,0]
	v_mfma_scale_f32_16x16x128_f8f6f4 v[76:79], v[8:15], v[48:55], v[76:79], v213, v213 op_sel_hi:[0,0,0]
	v_mfma_scale_f32_16x16x128_f8f6f4 v[72:75], v[0:7], v[48:55], v[72:75], v213, v213 op_sel_hi:[0,0,0]
	v_mfma_scale_f32_16x16x128_f8f6f4 v[68:71], v[8:15], v[56:63], v[68:71], v213, v213 op_sel_hi:[0,0,0]
	v_mfma_scale_f32_16x16x128_f8f6f4 v[64:67], v[0:7], v[56:63], v[64:67], v213, v213 op_sel_hi:[0,0,0]
	s_setprio 0
	s_barrier
	s_waitcnt vmcnt(14)
	v_mul_f32_e32 v0, 0x42800000, v196
	v_mul_f32_e32 v1, 0x42800000, v192
	v_mul_f32_e32 v2, 0x42800000, v197
	v_mul_f32_e32 v3, 0x42800000, v193
	v_mul_f32_e32 v4, 0x42800000, v198
	v_mul_f32_e32 v5, 0x42800000, v194
	v_mul_f32_e32 v6, 0x42800000, v199
	v_mul_f32_e32 v7, 0x42800000, v195
	v_cvt_pk_fp8_f32 v202, v1, v0
	v_cvt_pk_fp8_f32 v219, v3, v2
	v_cvt_pk_fp8_f32 v220, v5, v4
	v_cvt_pk_fp8_f32 v221, v7, v6
	s_add_i32 s61, s36, 0x200
	s_mov_b32 s33, 0
	s_mov_b32 s79, s66
	s_mov_b32 s90, s68
	s_branch .LBB0_926

.LBB0_926:
	v_mov_b32_e32 v40, v202
	v_mov_b32_e32 v41, v219
	v_mov_b32_e32 v42, v220
	v_mov_b32_e32 v43, v221
	s_add_i32 s4, s94, s33
	s_mov_b32 s64, s90
	s_add_i32 s90, s90, 1
	s_add_i32 s3, s4, 0x200
	s_add_i32 s5, s61, s33
	ds_read_b128 v[24:27], v217 offset:0
	ds_read_b128 v[28:31], v217 offset:0x400
	ds_read_b128 v[16:19], v217 offset:0x800
	ds_read_b128 v[20:23], v217 offset:0xc00
	s_cmpk_eq_i32 s33, 0xe00
	s_cselect_b32 s65, s60, s3
	s_cselect_b32 s16, s95, s5
	s_add_i32 s3, s65, 0x80
	s_mov_b32 m0, s86
	s_add_i32 s5, s4, 0x80180
	ds_read_b128 v[46:49], v216 offset:0
	ds_read_b128 v[50:53], v216 offset:0x400
	ds_read_b128 v[54:57], v216 offset:0x800
	ds_read_b128 v[58:61], v216 offset:0xc00
	ds_read_b128 v[192:195], v216 offset:0x1000
	ds_read_b128 v[196:199], v216 offset:0x1400
	ds_read_b128 v[220:223], v216 offset:0x1800
	ds_read_b128 v[224:227], v216 offset:0x1c00
	ds_read_b128 v[8:11], v217 offset:0x4000
	ds_read_b128 v[12:15], v217 offset:0x4400
	ds_read_b128 v[0:3], v217 offset:0x4800
	ds_read_b128 v[4:7], v217 offset:0x4c00
	buffer_load_dwordx4 v214, s[12:15], s5 offen lds
	s_add_i32 s4, s4, 0xc0180
	s_mov_b32 m0, s89
	s_add_i32 s17, s16, 0x80
	buffer_load_dwordx4 v214, s[12:15], s4 offen lds
	s_lshr_b32 s4, s90, 2
	s_mul_i32 s5, s4, s34
	s_add_i32 s36, s5, s2
	s_cmp_lt_i32 s4, s47
	s_cselect_b64 s[4:5], -1, 0
	s_and_b64 s[62:63], s[4:5], exec
	s_cselect_b32 s67, s36, 0
	s_ashr_i32 s62, s67, 7
	s_bfe_u32 s36, s90, 0x10001
	s_ashr_i32 s63, s62, 31
	s_or_b32 s78, s36, s87
	s_bfe_u32 s36, s67, 0x20005
	s_lshl_b64 vcc, s[62:63], 23
	s_add_u32 vcc_lo, s28, vcc_lo
	s_addc_u32 vcc_hi, s29, vcc_hi
	s_lshl_b32 s38, s36, 21
	s_add_u32 s38, vcc_lo, s38
	s_addc_u32 s39, vcc_hi, 0
	s_lshl_b32 s67, s67, 7
	s_and_b32 s67, s67, 0xf80
	s_lshl_b32 vcc_lo, s67, 2
	s_add_u32 vcc_lo, s38, vcc_lo
	v_and_or_b32 v202, s79, 2, v200
	s_addc_u32 vcc_hi, s39, 0
	v_lshl_or_b32 v44, s78, 5, v218
	v_lshlrev_b64 v[32:33], 14, v[202:203]
	v_lshl_add_u64 v[32:33], vcc, 0, v[32:33]
	v_lshlrev_b32_e32 v202, 2, v44
	v_lshl_add_u64 v[32:33], v[32:33], 0, v[202:203]
	s_movk_i32 s38, 0x4000
	v_add_co_u32_e32 v36, vcc, s38, v32
	s_nop 1
	v_addc_co_u32_e32 v37, vcc, 0, v33, vcc
	global_load_dwordx4 v[32:35], v[32:33], off nt
	s_nop 0
	global_load_dwordx4 v[36:39], v[36:37], off nt
	s_waitcnt vmcnt(10)
	s_waitcnt lgkmcnt(4)
	s_barrier
	s_setprio 1
	v_mfma_scale_f32_16x16x128_f8f6f4 v[188:191], v[24:31], v[46:53], v[188:191], v213, v213 op_sel_hi:[0,0,0]
	v_mfma_scale_f32_16x16x128_f8f6f4 v[184:187], v[16:23], v[46:53], v[184:187], v213, v213 op_sel_hi:[0,0,0]
	v_mfma_scale_f32_16x16x128_f8f6f4 v[180:183], v[24:31], v[54:61], v[180:183], v213, v213 op_sel_hi:[0,0,0]
	v_mfma_scale_f32_16x16x128_f8f6f4 v[176:179], v[16:23], v[54:61], v[176:179], v213, v213 op_sel_hi:[0,0,0]
	v_mfma_scale_f32_16x16x128_f8f6f4 v[172:175], v[24:31], v[192:199], v[172:175], v213, v213 op_sel_hi:[0,0,0]
	v_mfma_scale_f32_16x16x128_f8f6f4 v[168:171], v[16:23], v[192:199], v[168:171], v213, v213 op_sel_hi:[0,0,0]
	v_mfma_scale_f32_16x16x128_f8f6f4 v[164:167], v[24:31], v[220:227], v[164:167], v213, v213 op_sel_hi:[0,0,0]
	v_mfma_scale_f32_16x16x128_f8f6f4 v[160:163], v[16:23], v[220:227], v[160:163], v213, v213 op_sel_hi:[0,0,0]
	s_waitcnt lgkmcnt(0)
	s_setprio 0
	s_setprio 1
	v_mfma_scale_f32_16x16x128_f8f6f4 v[156:159], v[8:15], v[46:53], v[156:159], v213, v213 op_sel_hi:[0,0,0]
	v_mfma_scale_f32_16x16x128_f8f6f4 v[152:155], v[0:7], v[46:53], v[152:155], v213, v213 op_sel_hi:[0,0,0]
	v_mfma_scale_f32_16x16x128_f8f6f4 v[148:151], v[8:15], v[54:61], v[148:151], v213, v213 op_sel_hi:[0,0,0]
	v_mfma_scale_f32_16x16x128_f8f6f4 v[144:147], v[0:7], v[54:61], v[144:147], v213, v213 op_sel_hi:[0,0,0]
	v_mfma_scale_f32_16x16x128_f8f6f4 v[140:143], v[8:15], v[192:199], v[140:143], v213, v213 op_sel_hi:[0,0,0]
	v_mfma_scale_f32_16x16x128_f8f6f4 v[136:139], v[0:7], v[192:199], v[136:139], v213, v213 op_sel_hi:[0,0,0]
	v_mfma_scale_f32_16x16x128_f8f6f4 v[132:135], v[8:15], v[220:227], v[132:135], v213, v213 op_sel_hi:[0,0,0]
	v_mfma_scale_f32_16x16x128_f8f6f4 v[128:131], v[0:7], v[220:227], v[128:131], v213, v213 op_sel_hi:[0,0,0]
	s_setprio 0
	s_barrier
	s_mov_b32 m0, s71
	ds_read_b128 v[46:49], v216 offset:0x4000
	ds_read_b128 v[50:53], v216 offset:0x4400
	ds_read_b128 v[54:57], v216 offset:0x4800
	ds_read_b128 v[58:61], v216 offset:0x4c00
	ds_read_b128 v[192:195], v216 offset:0x5000
	ds_read_b128 v[196:199], v216 offset:0x5400
	ds_read_b128 v[220:223], v216 offset:0x5800
	ds_read_b128 v[224:227], v216 offset:0x5c00
	s_nop 0
	buffer_load_dwordx4 v215, s[8:11], s16 offen lds
	s_add_i32 s38, s16, 0x80000
	s_mov_b32 m0, s72
	s_nop 0
	buffer_load_dwordx4 v215, s[8:11], s38 offen lds
	s_add_i32 s38, s16, 0x8000
	s_mov_b32 m0, s73
	s_nop 0
	buffer_load_dwordx4 v215, s[8:11], s38 offen lds
	s_add_i32 s38, s16, 0x88000
	s_mov_b32 m0, s74
	s_nop 0
	buffer_load_dwordx4 v215, s[8:11], s38 offen lds
	s_mov_b32 m0, s70
	s_add_i32 s38, s65, 0x40000
	buffer_load_dwordx4 v214, s[12:15], s65 offen lds
	s_mov_b32 m0, s75
	s_nop 0
	buffer_load_dwordx4 v214, s[12:15], s38 offen lds
	s_waitcnt vmcnt(10)
	s_waitcnt lgkmcnt(0)
	s_barrier
	s_setprio 1
	v_mfma_scale_f32_16x16x128_f8f6f4 v[124:127], v[24:31], v[46:53], v[124:127], v213, v213 op_sel_hi:[0,0,0]
	v_mfma_scale_f32_16x16x128_f8f6f4 v[120:123], v[16:23], v[46:53], v[120:123], v213, v213 op_sel_hi:[0,0,0]
	v_mfma_scale_f32_16x16x128_f8f6f4 v[116:119], v[24:31], v[54:61], v[116:119], v213, v213 op_sel_hi:[0,0,0]
	v_mfma_scale_f32_16x16x128_f8f6f4 v[112:115], v[16:23], v[54:61], v[112:115], v213, v213 op_sel_hi:[0,0,0]
	v_mfma_scale_f32_16x16x128_f8f6f4 v[108:111], v[24:31], v[192:199], v[108:111], v213, v213 op_sel_hi:[0,0,0]
	v_mfma_scale_f32_16x16x128_f8f6f4 v[104:107], v[16:23], v[192:199], v[104:107], v213, v213 op_sel_hi:[0,0,0]
	v_mfma_scale_f32_16x16x128_f8f6f4 v[100:103], v[24:31], v[220:227], v[100:103], v213, v213 op_sel_hi:[0,0,0]
	v_mfma_scale_f32_16x16x128_f8f6f4 v[96:99], v[16:23], v[220:227], v[96:99], v213, v213 op_sel_hi:[0,0,0]
	s_setprio 0
	s_setprio 1
	v_mfma_scale_f32_16x16x128_f8f6f4 v[92:95], v[8:15], v[46:53], v[92:95], v213, v213 op_sel_hi:[0,0,0]
	v_mfma_scale_f32_16x16x128_f8f6f4 v[88:91], v[0:7], v[46:53], v[88:91], v213, v213 op_sel_hi:[0,0,0]
	v_mfma_scale_f32_16x16x128_f8f6f4 v[84:87], v[8:15], v[54:61], v[84:87], v213, v213 op_sel_hi:[0,0,0]
	v_mfma_scale_f32_16x16x128_f8f6f4 v[80:83], v[0:7], v[54:61], v[80:83], v213, v213 op_sel_hi:[0,0,0]
	v_mfma_scale_f32_16x16x128_f8f6f4 v[76:79], v[8:15], v[192:199], v[76:79], v213, v213 op_sel_hi:[0,0,0]
	v_mfma_scale_f32_16x16x128_f8f6f4 v[72:75], v[0:7], v[192:199], v[72:75], v213, v213 op_sel_hi:[0,0,0]
	v_mfma_scale_f32_16x16x128_f8f6f4 v[68:71], v[8:15], v[220:227], v[68:71], v213, v213 op_sel_hi:[0,0,0]
	v_mfma_scale_f32_16x16x128_f8f6f4 v[64:67], v[0:7], v[220:227], v[64:67], v213, v213 op_sel_hi:[0,0,0]
	s_setprio 0
	s_barrier
	ds_read_b128 v[16:19], v217 offset:0x8000
	ds_read_b128 v[20:23], v217 offset:0x8400
	ds_read_b128 v[24:27], v217 offset:0x8800
	ds_read_b128 v[28:31], v217 offset:0x8c00
	s_mov_b32 m0, s76
	s_add_i32 s38, s65, 0x80000
	ds_read_b128 v[46:49], v216 offset:0x8000
	ds_read_b128 v[50:53], v216 offset:0x8400
	ds_read_b128 v[54:57], v216 offset:0x8800
	ds_read_b128 v[58:61], v216 offset:0x8c00
	ds_read_b128 v[192:195], v216 offset:0x9000
	ds_read_b128 v[196:199], v216 offset:0x9400
	ds_read_b128 v[220:223], v216 offset:0x9800
	ds_read_b128 v[224:227], v216 offset:0x9c00
	ds_read_b128 v[8:11], v217 offset:0xc000
	ds_read_b128 v[12:15], v217 offset:0xc400
	ds_read_b128 v[0:3], v217 offset:0xc800
	ds_read_b128 v[4:7], v217 offset:0xcc00
	buffer_load_dwordx4 v214, s[12:15], s38 offen lds
	s_add_i32 s38, s65, 0xc0000
	s_mov_b32 m0, s77
	s_nop 0
	buffer_load_dwordx4 v214, s[12:15], s38 offen lds
	s_waitcnt vmcnt(10)
	s_waitcnt lgkmcnt(4)
	s_barrier
	s_setprio 1
	v_mfma_scale_f32_16x16x128_f8f6f4 v[188:191], v[16:23], v[46:53], v[188:191], v213, v213 op_sel_hi:[0,0,0]
	v_mfma_scale_f32_16x16x128_f8f6f4 v[184:187], v[24:31], v[46:53], v[184:187], v213, v213 op_sel_hi:[0,0,0]
	v_mfma_scale_f32_16x16x128_f8f6f4 v[180:183], v[16:23], v[54:61], v[180:183], v213, v213 op_sel_hi:[0,0,0]
	v_mfma_scale_f32_16x16x128_f8f6f4 v[176:179], v[24:31], v[54:61], v[176:179], v213, v213 op_sel_hi:[0,0,0]
	v_mfma_scale_f32_16x16x128_f8f6f4 v[172:175], v[16:23], v[192:199], v[172:175], v213, v213 op_sel_hi:[0,0,0]
	v_mfma_scale_f32_16x16x128_f8f6f4 v[168:171], v[24:31], v[192:199], v[168:171], v213, v213 op_sel_hi:[0,0,0]
	v_mfma_scale_f32_16x16x128_f8f6f4 v[164:167], v[16:23], v[220:227], v[164:167], v213, v213 op_sel_hi:[0,0,0]
	v_mfma_scale_f32_16x16x128_f8f6f4 v[160:163], v[24:31], v[220:227], v[160:163], v213, v213 op_sel_hi:[0,0,0]
	s_waitcnt lgkmcnt(0)
	s_setprio 0
	s_setprio 1
	v_mfma_scale_f32_16x16x128_f8f6f4 v[156:159], v[8:15], v[46:53], v[156:159], v213, v213 op_sel_hi:[0,0,0]
	v_mfma_scale_f32_16x16x128_f8f6f4 v[152:155], v[0:7], v[46:53], v[152:155], v213, v213 op_sel_hi:[0,0,0]
	v_mfma_scale_f32_16x16x128_f8f6f4 v[148:151], v[8:15], v[54:61], v[148:151], v213, v213 op_sel_hi:[0,0,0]
	v_mfma_scale_f32_16x16x128_f8f6f4 v[144:147], v[0:7], v[54:61], v[144:147], v213, v213 op_sel_hi:[0,0,0]
	v_mfma_scale_f32_16x16x128_f8f6f4 v[140:143], v[8:15], v[192:199], v[140:143], v213, v213 op_sel_hi:[0,0,0]
	v_mfma_scale_f32_16x16x128_f8f6f4 v[136:139], v[0:7], v[192:199], v[136:139], v213, v213 op_sel_hi:[0,0,0]
	v_mfma_scale_f32_16x16x128_f8f6f4 v[132:135], v[8:15], v[220:227], v[132:135], v213, v213 op_sel_hi:[0,0,0]
	v_mfma_scale_f32_16x16x128_f8f6f4 v[128:131], v[0:7], v[220:227], v[128:131], v213, v213 op_sel_hi:[0,0,0]
	s_setprio 0
	s_barrier
	s_mov_b32 m0, s80
	ds_read_b128 v[46:49], v216 offset:0xc000
	ds_read_b128 v[50:53], v216 offset:0xc400
	ds_read_b128 v[54:57], v216 offset:0xc800
	ds_read_b128 v[58:61], v216 offset:0xcc00
	ds_read_b128 v[192:195], v216 offset:0xd000
	ds_read_b128 v[196:199], v216 offset:0xd400
	ds_read_b128 v[220:223], v216 offset:0xd800
	ds_read_b128 v[224:227], v216 offset:0xdc00
	s_nop 0
	buffer_load_dwordx4 v215, s[8:11], s17 offen lds
	s_add_i32 s17, s16, 0x80080
	s_mov_b32 m0, s81
	s_add_i32 s65, s65, 0x40080
	buffer_load_dwordx4 v215, s[8:11], s17 offen lds
	s_add_i32 s17, s16, 0x8080
	s_mov_b32 m0, s84
	s_add_i32 s16, s16, 0x88080
	buffer_load_dwordx4 v215, s[8:11], s17 offen lds
	s_mov_b32 m0, s85
	s_nop 0
	buffer_load_dwordx4 v215, s[8:11], s16 offen lds
	s_mov_b32 m0, s82
	s_nop 0
	buffer_load_dwordx4 v214, s[12:15], s3 offen lds
	s_mov_b32 m0, s83
	s_nop 0
	buffer_load_dwordx4 v214, s[12:15], s65 offen lds
	s_waitcnt vmcnt(8)
	s_waitcnt lgkmcnt(0)
	s_barrier
	s_setprio 1
	v_mfma_scale_f32_16x16x128_f8f6f4 v[124:127], v[16:23], v[46:53], v[124:127], v213, v213 op_sel_hi:[0,0,0]
	v_mfma_scale_f32_16x16x128_f8f6f4 v[120:123], v[24:31], v[46:53], v[120:123], v213, v213 op_sel_hi:[0,0,0]
	v_mfma_scale_f32_16x16x128_f8f6f4 v[116:119], v[16:23], v[54:61], v[116:119], v213, v213 op_sel_hi:[0,0,0]
	v_mfma_scale_f32_16x16x128_f8f6f4 v[112:115], v[24:31], v[54:61], v[112:115], v213, v213 op_sel_hi:[0,0,0]
	v_mfma_scale_f32_16x16x128_f8f6f4 v[108:111], v[16:23], v[192:199], v[108:111], v213, v213 op_sel_hi:[0,0,0]
	v_mfma_scale_f32_16x16x128_f8f6f4 v[104:107], v[24:31], v[192:199], v[104:107], v213, v213 op_sel_hi:[0,0,0]
	v_mfma_scale_f32_16x16x128_f8f6f4 v[100:103], v[16:23], v[220:227], v[100:103], v213, v213 op_sel_hi:[0,0,0]
	v_mfma_scale_f32_16x16x128_f8f6f4 v[96:99], v[24:31], v[220:227], v[96:99], v213, v213 op_sel_hi:[0,0,0]
	s_setprio 0
	s_setprio 1
	v_mfma_scale_f32_16x16x128_f8f6f4 v[92:95], v[8:15], v[46:53], v[92:95], v213, v213 op_sel_hi:[0,0,0]
	v_mfma_scale_f32_16x16x128_f8f6f4 v[88:91], v[0:7], v[46:53], v[88:91], v213, v213 op_sel_hi:[0,0,0]
	v_mfma_scale_f32_16x16x128_f8f6f4 v[84:87], v[8:15], v[54:61], v[84:87], v213, v213 op_sel_hi:[0,0,0]
	v_mfma_scale_f32_16x16x128_f8f6f4 v[80:83], v[0:7], v[54:61], v[80:83], v213, v213 op_sel_hi:[0,0,0]
	v_mfma_scale_f32_16x16x128_f8f6f4 v[76:79], v[8:15], v[192:199], v[76:79], v213, v213 op_sel_hi:[0,0,0]
	v_mfma_scale_f32_16x16x128_f8f6f4 v[72:75], v[0:7], v[192:199], v[72:75], v213, v213 op_sel_hi:[0,0,0]
	v_mfma_scale_f32_16x16x128_f8f6f4 v[68:71], v[8:15], v[220:227], v[68:71], v213, v213 op_sel_hi:[0,0,0]
	v_mfma_scale_f32_16x16x128_f8f6f4 v[64:67], v[0:7], v[220:227], v[64:67], v213, v213 op_sel_hi:[0,0,0]
	s_setprio 0
	s_barrier
	s_bitcmp0_b32 s64, 0
	s_waitcnt vmcnt(15)
	v_mul_f32_e32 v0, 0x42800000, v32
	s_waitcnt vmcnt(14)
	v_mul_f32_e32 v4, 0x42800000, v36
	v_mul_f32_e32 v1, 0x42800000, v33
	v_mul_f32_e32 v5, 0x42800000, v37
	v_mul_f32_e32 v2, 0x42800000, v34
	v_mul_f32_e32 v6, 0x42800000, v38
	v_mul_f32_e32 v3, 0x42800000, v35
	v_mul_f32_e32 v7, 0x42800000, v39
	s_mov_b64 s[64:65], -1
	s_cbranch_scc0 .LBB0_929
	s_andn2_b64 vcc, exec, s[64:65]
	s_cbranch_vccnz .LBB0_925
	s_branch .LBB0_930

.LBB0_1228:
	s_add_i32 s28, s61, 0x180
	s_add_i32 s29, s60, 0x180
	s_waitcnt lgkmcnt(0)
	s_barrier
	s_setprio 1
	v_mfma_scale_f32_16x16x128_f8f6f4 v[128:131], v[24:31], v[56:63], 0, v201, v201 op_sel_hi:[0,0,0]
	v_mfma_scale_f32_16x16x128_f8f6f4 v[124:127], v[16:23], v[56:63], 0, v201, v201 op_sel_hi:[0,0,0]
	v_mfma_scale_f32_16x16x128_f8f6f4 v[120:123], v[24:31], v[48:55], 0, v201, v201 op_sel_hi:[0,0,0]
	v_mfma_scale_f32_16x16x128_f8f6f4 v[116:119], v[16:23], v[48:55], 0, v201, v201 op_sel_hi:[0,0,0]
	v_mfma_scale_f32_16x16x128_f8f6f4 v[112:115], v[24:31], v[40:47], 0, v201, v201 op_sel_hi:[0,0,0]
	v_mfma_scale_f32_16x16x128_f8f6f4 v[108:111], v[16:23], v[40:47], 0, v201, v201 op_sel_hi:[0,0,0]
	v_mfma_scale_f32_16x16x128_f8f6f4 v[104:107], v[24:31], v[32:39], 0, v201, v201 op_sel_hi:[0,0,0]
	v_mfma_scale_f32_16x16x128_f8f6f4 v[100:103], v[16:23], v[32:39], 0, v201, v201 op_sel_hi:[0,0,0]
	s_setprio 0
	s_setprio 1
	v_mfma_scale_f32_16x16x128_f8f6f4 v[96:99], v[8:15], v[56:63], 0, v201, v201 op_sel_hi:[0,0,0]
	v_mfma_scale_f32_16x16x128_f8f6f4 v[92:95], v[0:7], v[56:63], 0, v201, v201 op_sel_hi:[0,0,0]
	v_mfma_scale_f32_16x16x128_f8f6f4 v[88:91], v[8:15], v[48:55], 0, v201, v201 op_sel_hi:[0,0,0]
	v_mfma_scale_f32_16x16x128_f8f6f4 v[84:87], v[0:7], v[48:55], 0, v201, v201 op_sel_hi:[0,0,0]
	v_mfma_scale_f32_16x16x128_f8f6f4 v[80:83], v[8:15], v[40:47], 0, v201, v201 op_sel_hi:[0,0,0]
	v_mfma_scale_f32_16x16x128_f8f6f4 v[76:79], v[0:7], v[40:47], 0, v201, v201 op_sel_hi:[0,0,0]
	v_mfma_scale_f32_16x16x128_f8f6f4 v[72:75], v[8:15], v[32:39], 0, v201, v201 op_sel_hi:[0,0,0]
	v_mfma_scale_f32_16x16x128_f8f6f4 v[68:71], v[0:7], v[32:39], 0, v201, v201 op_sel_hi:[0,0,0]
	s_setprio 0
	s_barrier
	ds_read_b128 v[24:27], v205 offset:0x8000
	ds_read_b128 v[28:31], v205 offset:0x8400
	ds_read_b128 v[16:19], v205 offset:0x8800
	ds_read_b128 v[20:23], v205 offset:0x8c00
	s_mov_b32 m0, s44
	ds_read_b128 v[32:35], v204 offset:0x8000
	ds_read_b128 v[36:39], v204 offset:0x8400
	ds_read_b128 v[40:43], v204 offset:0x8800
	ds_read_b128 v[44:47], v204 offset:0x8c00
	ds_read_b128 v[48:51], v204 offset:0x9000
	ds_read_b128 v[52:55], v204 offset:0x9400
	ds_read_b128 v[56:59], v204 offset:0x9800
	ds_read_b128 v[60:63], v204 offset:0x9c00
	ds_read_b128 v[8:11], v205 offset:0xc000
	ds_read_b128 v[12:15], v205 offset:0xc400
	ds_read_b128 v[0:3], v205 offset:0xc800
	ds_read_b128 v[4:7], v205 offset:0xcc00
	s_nop 0
	buffer_load_dwordx4 v216, s[4:7], s33 offen lds
	s_mov_b32 m0, s45
	s_nop 0
	buffer_load_dwordx4 v215, s[4:7], s33 offen lds
	s_waitcnt vmcnt(8)
	s_waitcnt lgkmcnt(4)
	s_barrier
	s_setprio 1
	v_mfma_scale_f32_16x16x128_f8f6f4 v[192:195], v[24:31], v[32:39], v[192:195], v201, v201 op_sel_hi:[0,0,0]
	v_mfma_scale_f32_16x16x128_f8f6f4 v[188:191], v[16:23], v[32:39], v[188:191], v201, v201 op_sel_hi:[0,0,0]
	v_mfma_scale_f32_16x16x128_f8f6f4 v[184:187], v[24:31], v[40:47], v[184:187], v201, v201 op_sel_hi:[0,0,0]
	v_mfma_scale_f32_16x16x128_f8f6f4 v[180:183], v[16:23], v[40:47], v[180:183], v201, v201 op_sel_hi:[0,0,0]
	v_mfma_scale_f32_16x16x128_f8f6f4 v[176:179], v[24:31], v[48:55], v[176:179], v201, v201 op_sel_hi:[0,0,0]
	v_mfma_scale_f32_16x16x128_f8f6f4 v[172:175], v[16:23], v[48:55], v[172:175], v201, v201 op_sel_hi:[0,0,0]
	v_mfma_scale_f32_16x16x128_f8f6f4 v[168:171], v[24:31], v[56:63], v[168:171], v201, v201 op_sel_hi:[0,0,0]
	v_mfma_scale_f32_16x16x128_f8f6f4 v[164:167], v[16:23], v[56:63], v[164:167], v201, v201 op_sel_hi:[0,0,0]
	s_waitcnt lgkmcnt(0)
	s_setprio 0
	s_setprio 1
	v_mfma_scale_f32_16x16x128_f8f6f4 v[160:163], v[8:15], v[32:39], v[160:163], v201, v201 op_sel_hi:[0,0,0]
	v_mfma_scale_f32_16x16x128_f8f6f4 v[156:159], v[0:7], v[32:39], v[156:159], v201, v201 op_sel_hi:[0,0,0]
	v_mfma_scale_f32_16x16x128_f8f6f4 v[152:155], v[8:15], v[40:47], v[152:155], v201, v201 op_sel_hi:[0,0,0]
	v_mfma_scale_f32_16x16x128_f8f6f4 v[148:151], v[0:7], v[40:47], v[148:151], v201, v201 op_sel_hi:[0,0,0]
	v_mfma_scale_f32_16x16x128_f8f6f4 v[144:147], v[8:15], v[48:55], v[144:147], v201, v201 op_sel_hi:[0,0,0]
	v_mfma_scale_f32_16x16x128_f8f6f4 v[140:143], v[0:7], v[48:55], v[140:143], v201, v201 op_sel_hi:[0,0,0]
	v_mfma_scale_f32_16x16x128_f8f6f4 v[136:139], v[8:15], v[56:63], v[136:139], v201, v201 op_sel_hi:[0,0,0]
	v_mfma_scale_f32_16x16x128_f8f6f4 v[132:135], v[0:7], v[56:63], v[132:135], v201, v201 op_sel_hi:[0,0,0]
	s_setprio 0
	s_barrier
	s_mov_b32 m0, s48
	s_mov_b32 s10, s6
	s_mov_b32 s11, s7
	ds_read_b128 v[32:35], v204 offset:0xc000
	ds_read_b128 v[36:39], v204 offset:0xc400
	ds_read_b128 v[40:43], v204 offset:0xc800
	ds_read_b128 v[44:47], v204 offset:0xcc00
	ds_read_b128 v[48:51], v204 offset:0xd000
	ds_read_b128 v[52:55], v204 offset:0xd400
	ds_read_b128 v[56:59], v204 offset:0xd800
	ds_read_b128 v[60:63], v204 offset:0xdc00
	buffer_load_dwordx4 v203, s[8:11], s29 offen lds
	s_add_i32 s29, s60, 0x80180
	s_mov_b32 m0, s49
	s_nop 0
	buffer_load_dwordx4 v203, s[8:11], s29 offen lds
	s_add_i32 s29, s60, 0x8180
	s_mov_b32 m0, s62
	s_nop 0
	buffer_load_dwordx4 v203, s[8:11], s29 offen lds
	s_add_i32 s29, s60, 0x88180
	s_mov_b32 m0, s63
	s_nop 0
	buffer_load_dwordx4 v203, s[8:11], s29 offen lds
	s_mov_b32 m0, s50
	s_nop 0
	buffer_load_dwordx4 v214, s[4:7], s28 offen lds
	s_mov_b32 m0, s51
	s_nop 0
	buffer_load_dwordx4 v217, s[4:7], s28 offen lds
	s_waitcnt vmcnt(8)
	s_waitcnt lgkmcnt(0)
	s_barrier
	s_setprio 1
	v_mfma_scale_f32_16x16x128_f8f6f4 v[128:131], v[24:31], v[32:39], v[128:131], v201, v201 op_sel_hi:[0,0,0]
	v_mfma_scale_f32_16x16x128_f8f6f4 v[124:127], v[16:23], v[32:39], v[124:127], v201, v201 op_sel_hi:[0,0,0]
	v_mfma_scale_f32_16x16x128_f8f6f4 v[120:123], v[24:31], v[40:47], v[120:123], v201, v201 op_sel_hi:[0,0,0]
	v_mfma_scale_f32_16x16x128_f8f6f4 v[116:119], v[16:23], v[40:47], v[116:119], v201, v201 op_sel_hi:[0,0,0]
	v_mfma_scale_f32_16x16x128_f8f6f4 v[112:115], v[24:31], v[48:55], v[112:115], v201, v201 op_sel_hi:[0,0,0]
	v_mfma_scale_f32_16x16x128_f8f6f4 v[108:111], v[16:23], v[48:55], v[108:111], v201, v201 op_sel_hi:[0,0,0]
	v_mfma_scale_f32_16x16x128_f8f6f4 v[104:107], v[24:31], v[56:63], v[104:107], v201, v201 op_sel_hi:[0,0,0]
	v_mfma_scale_f32_16x16x128_f8f6f4 v[100:103], v[16:23], v[56:63], v[100:103], v201, v201 op_sel_hi:[0,0,0]
	s_setprio 0
	s_setprio 1
	v_mfma_scale_f32_16x16x128_f8f6f4 v[96:99], v[8:15], v[32:39], v[96:99], v201, v201 op_sel_hi:[0,0,0]
	v_mfma_scale_f32_16x16x128_f8f6f4 v[92:95], v[0:7], v[32:39], v[92:95], v201, v201 op_sel_hi:[0,0,0]
	v_mfma_scale_f32_16x16x128_f8f6f4 v[88:91], v[8:15], v[40:47], v[88:91], v201, v201 op_sel_hi:[0,0,0]
	v_mfma_scale_f32_16x16x128_f8f6f4 v[84:87], v[0:7], v[40:47], v[84:87], v201, v201 op_sel_hi:[0,0,0]
	v_mfma_scale_f32_16x16x128_f8f6f4 v[80:83], v[8:15], v[48:55], v[80:83], v201, v201 op_sel_hi:[0,0,0]
	v_mfma_scale_f32_16x16x128_f8f6f4 v[76:79], v[0:7], v[48:55], v[76:79], v201, v201 op_sel_hi:[0,0,0]
	v_mfma_scale_f32_16x16x128_f8f6f4 v[72:75], v[8:15], v[56:63], v[72:75], v201, v201 op_sel_hi:[0,0,0]
	v_mfma_scale_f32_16x16x128_f8f6f4 v[68:71], v[0:7], v[56:63], v[68:71], v201, v201 op_sel_hi:[0,0,0]
	s_setprio 0
	s_barrier
	s_waitcnt vmcnt(16)
	v_mbcnt_lo_u32_b32 v0, -1, 0
	v_mbcnt_hi_u32_b32 v0, -1, v0
	s_add_i32 s29, s60, 0x200
	v_lshl_add_u32 v0, v0, 4, s37
	v_ashrrev_i32_e32 v1, 31, v0
	v_lshrrev_b32_e32 v1, 22, v1
	v_add_u32_e32 v1, v0, v1
	v_ashrrev_i32_e32 v1, 10, v1
	v_mul_i32_i24_e32 v2, 0x400, v1
	v_sub_u32_e32 v2, v0, v2
	v_lshrrev_b32_e32 v3, 4, v2
	v_bitop3_b32 v3, v3, v2, 32 bitop3:0x6c
	v_ashrrev_i32_e32 v2, 31, v2
	v_lshrrev_b32_e32 v2, 26, v2
	v_add_u32_e32 v2, v3, v2
	v_and_b32_e32 v2, 0xc0, v2
	v_add_u32_e32 v0, 0x2000, v0
	v_sub_u32_e32 v2, v3, v2
	v_ashrrev_i32_e32 v3, 31, v0
	v_lshrrev_b32_e32 v3, 22, v3
	v_add_u32_e32 v3, v0, v3
	v_ashrrev_i32_e32 v3, 10, v3
	v_mul_i32_i24_e32 v4, 0x400, v3
	v_sub_u32_e32 v0, v0, v4
	v_lshrrev_b32_e32 v4, 4, v0
	v_bitop3_b32 v4, v4, v0, 32 bitop3:0x6c
	v_ashrrev_i32_e32 v0, 31, v0
	v_lshrrev_b32_e32 v0, 26, v0
	v_add_u32_e32 v0, v4, v0
	v_and_b32_e32 v0, 0xffc0, v0
	v_sub_u32_e32 v0, v4, v0
	v_lshrrev_b16_e32 v4, 7, v0
	v_and_b32_e32 v4, 1, v4
	v_add_u16_e32 v0, v0, v4
	v_lshlrev_b32_e32 v1, 5, v1
	v_ashrrev_i16_sdwa v2, v202, sext(v2) dst_sel:DWORD dst_unused:UNUSED_PAD src0_sel:DWORD src1_sel:BYTE_0
	v_lshlrev_b32_e32 v3, 5, v3
	v_ashrrev_i16_sdwa v0, v202, sext(v0) dst_sel:DWORD dst_unused:UNUSED_PAD src0_sel:DWORD src1_sel:BYTE_0
	v_and_b32_e32 v1, 32, v1
	v_bfe_i32 v2, v2, 0, 16
	v_and_b32_e32 v3, 32, v3
	v_bfe_i32 v0, v0, 0, 16
	v_add_lshl_u32 v1, v1, v2, 1
	v_add_lshl_u32 v0, v3, v0, 1
	v_lshl_add_u32 v32, v231, 12, v1
	v_lshl_add_u32 v33, v228, 12, v0
	v_lshl_add_u32 v34, v229, 12, v1
	v_lshl_add_u32 v35, v230, 12, v0
	s_mov_b32 s33, 0
.LBB0_1229:
	s_add_i32 s66, s28, 0x80
	s_cmp_eq_u32 s33, 28
	s_cselect_b64 vcc, -1, 0
	ds_read_b128 v[16:19], v205 offset:0
	ds_read_b128 v[20:23], v205 offset:0x400
	ds_read_b128 v[24:27], v205 offset:0x800
	ds_read_b128 v[28:31], v205 offset:0xc00
	s_and_b64 s[60:61], vcc, exec
	s_cselect_b32 s66, s72, s66
	s_cselect_b32 s61, s73, s29
	s_add_i32 s60, s66, 0x80
	s_mov_b32 m0, s65
	ds_read_b128 v[36:39], v204 offset:0
	ds_read_b128 v[40:43], v204 offset:0x400
	ds_read_b128 v[44:47], v204 offset:0x800
	ds_read_b128 v[48:51], v204 offset:0xc00
	ds_read_b128 v[52:55], v204 offset:0x1000
	ds_read_b128 v[56:59], v204 offset:0x1400
	ds_read_b128 v[228:231], v204 offset:0x1800
	ds_read_b128 v[232:235], v204 offset:0x1c00
	ds_read_b128 v[8:11], v205 offset:0x4000
	ds_read_b128 v[12:15], v205 offset:0x4400
	ds_read_b128 v[0:3], v205 offset:0x4800
	ds_read_b128 v[4:7], v205 offset:0x4c00
	s_nop 0
	buffer_load_dwordx4 v216, s[4:7], s28 offen lds
	s_mov_b32 m0, s68
	s_nop 0
	buffer_load_dwordx4 v215, s[4:7], s28 offen lds
	s_waitcnt vmcnt(8)
	s_waitcnt lgkmcnt(4)
	s_barrier
	s_setprio 1
	v_mfma_scale_f32_16x16x128_f8f6f4 v[192:195], v[16:23], v[36:43], v[192:195], v201, v201 op_sel_hi:[0,0,0]
	v_mfma_scale_f32_16x16x128_f8f6f4 v[188:191], v[24:31], v[36:43], v[188:191], v201, v201 op_sel_hi:[0,0,0]
	v_mfma_scale_f32_16x16x128_f8f6f4 v[184:187], v[16:23], v[44:51], v[184:187], v201, v201 op_sel_hi:[0,0,0]
	v_mfma_scale_f32_16x16x128_f8f6f4 v[180:183], v[24:31], v[44:51], v[180:183], v201, v201 op_sel_hi:[0,0,0]
	v_mfma_scale_f32_16x16x128_f8f6f4 v[176:179], v[16:23], v[52:59], v[176:179], v201, v201 op_sel_hi:[0,0,0]
	v_mfma_scale_f32_16x16x128_f8f6f4 v[172:175], v[24:31], v[52:59], v[172:175], v201, v201 op_sel_hi:[0,0,0]
	v_mfma_scale_f32_16x16x128_f8f6f4 v[168:171], v[16:23], v[228:235], v[168:171], v201, v201 op_sel_hi:[0,0,0]
	v_mfma_scale_f32_16x16x128_f8f6f4 v[164:167], v[24:31], v[228:235], v[164:167], v201, v201 op_sel_hi:[0,0,0]
	s_waitcnt lgkmcnt(0)
	s_setprio 0
	s_setprio 1
	v_mfma_scale_f32_16x16x128_f8f6f4 v[160:163], v[8:15], v[36:43], v[160:163], v201, v201 op_sel_hi:[0,0,0]
	v_mfma_scale_f32_16x16x128_f8f6f4 v[156:159], v[0:7], v[36:43], v[156:159], v201, v201 op_sel_hi:[0,0,0]
	v_mfma_scale_f32_16x16x128_f8f6f4 v[152:155], v[8:15], v[44:51], v[152:155], v201, v201 op_sel_hi:[0,0,0]
	v_mfma_scale_f32_16x16x128_f8f6f4 v[148:151], v[0:7], v[44:51], v[148:151], v201, v201 op_sel_hi:[0,0,0]
	v_mfma_scale_f32_16x16x128_f8f6f4 v[144:147], v[8:15], v[52:59], v[144:147], v201, v201 op_sel_hi:[0,0,0]
	v_mfma_scale_f32_16x16x128_f8f6f4 v[140:143], v[0:7], v[52:59], v[140:143], v201, v201 op_sel_hi:[0,0,0]
	v_mfma_scale_f32_16x16x128_f8f6f4 v[136:139], v[8:15], v[228:235], v[136:139], v201, v201 op_sel_hi:[0,0,0]
	v_mfma_scale_f32_16x16x128_f8f6f4 v[132:135], v[0:7], v[228:235], v[132:135], v201, v201 op_sel_hi:[0,0,0]
	s_setprio 0
	s_barrier
	s_mov_b32 m0, s39
	ds_read_b128 v[36:39], v204 offset:0x4000
	ds_read_b128 v[40:43], v204 offset:0x4400
	ds_read_b128 v[44:47], v204 offset:0x4800
	ds_read_b128 v[48:51], v204 offset:0x4c00
	ds_read_b128 v[52:55], v204 offset:0x5000
	ds_read_b128 v[56:59], v204 offset:0x5400
	ds_read_b128 v[228:231], v204 offset:0x5800
	ds_read_b128 v[232:235], v204 offset:0x5c00
	s_nop 0
	buffer_load_dwordx4 v203, s[8:11], s61 offen lds
	s_add_i32 s67, s61, 0x80000
	s_mov_b32 m0, s40
	v_cndmask_b32_e32 v60, v214, v32, vcc
	buffer_load_dwordx4 v203, s[8:11], s67 offen lds
	s_add_i32 s67, s61, 0x8000
	s_mov_b32 m0, s41
	v_cndmask_b32_e32 v61, v217, v33, vcc
	buffer_load_dwordx4 v203, s[8:11], s67 offen lds
	s_add_i32 s67, s61, 0x88000
	s_mov_b32 m0, s42
	s_nop 0
	buffer_load_dwordx4 v203, s[8:11], s67 offen lds
	s_mov_b32 m0, s38
	s_nop 0
	buffer_load_dwordx4 v60, s[4:7], s66 offen lds
	s_mov_b32 m0, s43
	s_nop 0
	buffer_load_dwordx4 v61, s[4:7], s66 offen lds
	s_waitcnt vmcnt(8)
	s_waitcnt lgkmcnt(0)
	s_barrier
	s_setprio 1
	v_mfma_scale_f32_16x16x128_f8f6f4 v[128:131], v[16:23], v[36:43], v[128:131], v201, v201 op_sel_hi:[0,0,0]
	v_mfma_scale_f32_16x16x128_f8f6f4 v[124:127], v[24:31], v[36:43], v[124:127], v201, v201 op_sel_hi:[0,0,0]
	v_mfma_scale_f32_16x16x128_f8f6f4 v[120:123], v[16:23], v[44:51], v[120:123], v201, v201 op_sel_hi:[0,0,0]
	v_mfma_scale_f32_16x16x128_f8f6f4 v[116:119], v[24:31], v[44:51], v[116:119], v201, v201 op_sel_hi:[0,0,0]
	v_mfma_scale_f32_16x16x128_f8f6f4 v[112:115], v[16:23], v[52:59], v[112:115], v201, v201 op_sel_hi:[0,0,0]
	v_mfma_scale_f32_16x16x128_f8f6f4 v[108:111], v[24:31], v[52:59], v[108:111], v201, v201 op_sel_hi:[0,0,0]
	v_mfma_scale_f32_16x16x128_f8f6f4 v[104:107], v[16:23], v[228:235], v[104:107], v201, v201 op_sel_hi:[0,0,0]
	v_mfma_scale_f32_16x16x128_f8f6f4 v[100:103], v[24:31], v[228:235], v[100:103], v201, v201 op_sel_hi:[0,0,0]
	s_setprio 0
	s_setprio 1
	v_mfma_scale_f32_16x16x128_f8f6f4 v[96:99], v[8:15], v[36:43], v[96:99], v201, v201 op_sel_hi:[0,0,0]
	v_mfma_scale_f32_16x16x128_f8f6f4 v[92:95], v[0:7], v[36:43], v[92:95], v201, v201 op_sel_hi:[0,0,0]
	v_mfma_scale_f32_16x16x128_f8f6f4 v[88:91], v[8:15], v[44:51], v[88:91], v201, v201 op_sel_hi:[0,0,0]
	v_mfma_scale_f32_16x16x128_f8f6f4 v[84:87], v[0:7], v[44:51], v[84:87], v201, v201 op_sel_hi:[0,0,0]
	v_mfma_scale_f32_16x16x128_f8f6f4 v[80:83], v[8:15], v[52:59], v[80:83], v201, v201 op_sel_hi:[0,0,0]
	v_mfma_scale_f32_16x16x128_f8f6f4 v[76:79], v[0:7], v[52:59], v[76:79], v201, v201 op_sel_hi:[0,0,0]
	v_mfma_scale_f32_16x16x128_f8f6f4 v[72:75], v[8:15], v[228:235], v[72:75], v201, v201 op_sel_hi:[0,0,0]
	v_mfma_scale_f32_16x16x128_f8f6f4 v[68:71], v[0:7], v[228:235], v[68:71], v201, v201 op_sel_hi:[0,0,0]
	s_setprio 0
	s_barrier
	ds_read_b128 v[24:27], v205 offset:0x8000
	ds_read_b128 v[28:31], v205 offset:0x8400
	ds_read_b128 v[16:19], v205 offset:0x8800
	ds_read_b128 v[20:23], v205 offset:0x8c00
	s_mov_b32 m0, s44
	v_cndmask_b32_e32 v62, v216, v34, vcc
	ds_read_b128 v[36:39], v204 offset:0x8000
	ds_read_b128 v[40:43], v204 offset:0x8400
	ds_read_b128 v[44:47], v204 offset:0x8800
	ds_read_b128 v[48:51], v204 offset:0x8c00
	ds_read_b128 v[52:55], v204 offset:0x9000
	ds_read_b128 v[56:59], v204 offset:0x9400
	ds_read_b128 v[228:231], v204 offset:0x9800
	ds_read_b128 v[232:235], v204 offset:0x9c00
	ds_read_b128 v[8:11], v205 offset:0xc000
	ds_read_b128 v[12:15], v205 offset:0xc400
	ds_read_b128 v[0:3], v205 offset:0xc800
	ds_read_b128 v[4:7], v205 offset:0xcc00
	buffer_load_dwordx4 v62, s[4:7], s66 offen lds
	v_cndmask_b32_e32 v62, v215, v35, vcc
	s_mov_b32 m0, s45
	s_nop 0
	buffer_load_dwordx4 v62, s[4:7], s66 offen lds
	s_waitcnt vmcnt(8)
	s_waitcnt lgkmcnt(4)
	s_barrier
	s_setprio 1
	v_mfma_scale_f32_16x16x128_f8f6f4 v[192:195], v[24:31], v[36:43], v[192:195], v201, v201 op_sel_hi:[0,0,0]
	v_mfma_scale_f32_16x16x128_f8f6f4 v[188:191], v[16:23], v[36:43], v[188:191], v201, v201 op_sel_hi:[0,0,0]
	v_mfma_scale_f32_16x16x128_f8f6f4 v[184:187], v[24:31], v[44:51], v[184:187], v201, v201 op_sel_hi:[0,0,0]
	v_mfma_scale_f32_16x16x128_f8f6f4 v[180:183], v[16:23], v[44:51], v[180:183], v201, v201 op_sel_hi:[0,0,0]
	v_mfma_scale_f32_16x16x128_f8f6f4 v[176:179], v[24:31], v[52:59], v[176:179], v201, v201 op_sel_hi:[0,0,0]
	v_mfma_scale_f32_16x16x128_f8f6f4 v[172:175], v[16:23], v[52:59], v[172:175], v201, v201 op_sel_hi:[0,0,0]
	v_mfma_scale_f32_16x16x128_f8f6f4 v[168:171], v[24:31], v[228:235], v[168:171], v201, v201 op_sel_hi:[0,0,0]
	v_mfma_scale_f32_16x16x128_f8f6f4 v[164:167], v[16:23], v[228:235], v[164:167], v201, v201 op_sel_hi:[0,0,0]
	s_waitcnt lgkmcnt(0)
	s_setprio 0
	s_setprio 1
	v_mfma_scale_f32_16x16x128_f8f6f4 v[160:163], v[8:15], v[36:43], v[160:163], v201, v201 op_sel_hi:[0,0,0]
	v_mfma_scale_f32_16x16x128_f8f6f4 v[156:159], v[0:7], v[36:43], v[156:159], v201, v201 op_sel_hi:[0,0,0]
	v_mfma_scale_f32_16x16x128_f8f6f4 v[152:155], v[8:15], v[44:51], v[152:155], v201, v201 op_sel_hi:[0,0,0]
	v_mfma_scale_f32_16x16x128_f8f6f4 v[148:151], v[0:7], v[44:51], v[148:151], v201, v201 op_sel_hi:[0,0,0]
	v_mfma_scale_f32_16x16x128_f8f6f4 v[144:147], v[8:15], v[52:59], v[144:147], v201, v201 op_sel_hi:[0,0,0]
	v_mfma_scale_f32_16x16x128_f8f6f4 v[140:143], v[0:7], v[52:59], v[140:143], v201, v201 op_sel_hi:[0,0,0]
	v_mfma_scale_f32_16x16x128_f8f6f4 v[136:139], v[8:15], v[228:235], v[136:139], v201, v201 op_sel_hi:[0,0,0]
	v_mfma_scale_f32_16x16x128_f8f6f4 v[132:135], v[0:7], v[228:235], v[132:135], v201, v201 op_sel_hi:[0,0,0]
	s_setprio 0
	s_barrier
	s_mov_b32 m0, s48
	s_add_i32 s66, s61, 0x80
	ds_read_b128 v[36:39], v204 offset:0xc000
	ds_read_b128 v[40:43], v204 offset:0xc400
	ds_read_b128 v[44:47], v204 offset:0xc800
	ds_read_b128 v[48:51], v204 offset:0xcc00
	ds_read_b128 v[52:55], v204 offset:0xd000
	ds_read_b128 v[56:59], v204 offset:0xd400
	ds_read_b128 v[228:231], v204 offset:0xd800
	ds_read_b128 v[232:235], v204 offset:0xdc00
	buffer_load_dwordx4 v203, s[8:11], s66 offen lds
	s_add_i32 s66, s61, 0x80080
	s_mov_b32 m0, s49
	s_nop 0
	buffer_load_dwordx4 v203, s[8:11], s66 offen lds
	s_add_i32 s66, s61, 0x8080
	s_mov_b32 m0, s62
	s_add_i32 s61, s61, 0x88080
	buffer_load_dwordx4 v203, s[8:11], s66 offen lds
	s_mov_b32 m0, s63
	s_nop 0
	buffer_load_dwordx4 v203, s[8:11], s61 offen lds
	s_mov_b32 m0, s50
	s_nop 0
	buffer_load_dwordx4 v60, s[4:7], s60 offen lds
	s_mov_b32 m0, s51
	s_nop 0
	buffer_load_dwordx4 v61, s[4:7], s60 offen lds
	s_waitcnt vmcnt(8)
	s_waitcnt lgkmcnt(0)
	s_barrier
	s_setprio 1
	v_mfma_scale_f32_16x16x128_f8f6f4 v[128:131], v[24:31], v[36:43], v[128:131], v201, v201 op_sel_hi:[0,0,0]
	v_mfma_scale_f32_16x16x128_f8f6f4 v[124:127], v[16:23], v[36:43], v[124:127], v201, v201 op_sel_hi:[0,0,0]
	v_mfma_scale_f32_16x16x128_f8f6f4 v[120:123], v[24:31], v[44:51], v[120:123], v201, v201 op_sel_hi:[0,0,0]
	v_mfma_scale_f32_16x16x128_f8f6f4 v[116:119], v[16:23], v[44:51], v[116:119], v201, v201 op_sel_hi:[0,0,0]
	v_mfma_scale_f32_16x16x128_f8f6f4 v[112:115], v[24:31], v[52:59], v[112:115], v201, v201 op_sel_hi:[0,0,0]
	v_mfma_scale_f32_16x16x128_f8f6f4 v[108:111], v[16:23], v[52:59], v[108:111], v201, v201 op_sel_hi:[0,0,0]
	v_mfma_scale_f32_16x16x128_f8f6f4 v[104:107], v[24:31], v[228:235], v[104:107], v201, v201 op_sel_hi:[0,0,0]
	v_mfma_scale_f32_16x16x128_f8f6f4 v[100:103], v[16:23], v[228:235], v[100:103], v201, v201 op_sel_hi:[0,0,0]
	s_setprio 0
	s_setprio 1
	v_mfma_scale_f32_16x16x128_f8f6f4 v[96:99], v[8:15], v[36:43], v[96:99], v201, v201 op_sel_hi:[0,0,0]
	v_mfma_scale_f32_16x16x128_f8f6f4 v[92:95], v[0:7], v[36:43], v[92:95], v201, v201 op_sel_hi:[0,0,0]
	v_mfma_scale_f32_16x16x128_f8f6f4 v[88:91], v[8:15], v[44:51], v[88:91], v201, v201 op_sel_hi:[0,0,0]
	v_mfma_scale_f32_16x16x128_f8f6f4 v[84:87], v[0:7], v[44:51], v[84:87], v201, v201 op_sel_hi:[0,0,0]
	v_mfma_scale_f32_16x16x128_f8f6f4 v[80:83], v[8:15], v[52:59], v[80:83], v201, v201 op_sel_hi:[0,0,0]
	v_mfma_scale_f32_16x16x128_f8f6f4 v[76:79], v[0:7], v[52:59], v[76:79], v201, v201 op_sel_hi:[0,0,0]
	v_mfma_scale_f32_16x16x128_f8f6f4 v[72:75], v[8:15], v[228:235], v[72:75], v201, v201 op_sel_hi:[0,0,0]
	v_mfma_scale_f32_16x16x128_f8f6f4 v[68:71], v[0:7], v[228:235], v[68:71], v201, v201 op_sel_hi:[0,0,0]
	s_setprio 0
	s_barrier
	s_add_i32 s33, s33, 2
	s_addk_i32 s28, 0x100
	s_addk_i32 s29, 0x100
	s_cmp_gt_u32 s33, 29
	s_cbranch_scc0 .LBB0_1229
	s_and_b64 vcc, exec, s[18:19]
	s_cbranch_vccz .LBB0_1232
	s_barrier

.LBB0_1329:
	s_add_i32 s36, s89, 0x180
	s_add_i32 s37, s61, 0x180
	s_waitcnt lgkmcnt(0)
	s_barrier
	s_setprio 1
	v_mfma_scale_f32_16x16x128_f8f6f4 v[128:131], v[24:31], v[56:63], 0, v198, v198 op_sel_hi:[0,0,0]
	v_mfma_scale_f32_16x16x128_f8f6f4 v[124:127], v[16:23], v[56:63], 0, v198, v198 op_sel_hi:[0,0,0]
	v_mfma_scale_f32_16x16x128_f8f6f4 v[120:123], v[24:31], v[48:55], 0, v198, v198 op_sel_hi:[0,0,0]
	v_mfma_scale_f32_16x16x128_f8f6f4 v[116:119], v[16:23], v[48:55], 0, v198, v198 op_sel_hi:[0,0,0]
	v_mfma_scale_f32_16x16x128_f8f6f4 v[112:115], v[24:31], v[40:47], 0, v198, v198 op_sel_hi:[0,0,0]
	v_mfma_scale_f32_16x16x128_f8f6f4 v[108:111], v[16:23], v[40:47], 0, v198, v198 op_sel_hi:[0,0,0]
	v_mfma_scale_f32_16x16x128_f8f6f4 v[104:107], v[24:31], v[32:39], 0, v198, v198 op_sel_hi:[0,0,0]
	v_mfma_scale_f32_16x16x128_f8f6f4 v[100:103], v[16:23], v[32:39], 0, v198, v198 op_sel_hi:[0,0,0]
	s_setprio 0
	s_setprio 1
	v_mfma_scale_f32_16x16x128_f8f6f4 v[96:99], v[8:15], v[56:63], 0, v198, v198 op_sel_hi:[0,0,0]
	v_mfma_scale_f32_16x16x128_f8f6f4 v[92:95], v[0:7], v[56:63], 0, v198, v198 op_sel_hi:[0,0,0]
	v_mfma_scale_f32_16x16x128_f8f6f4 v[88:91], v[8:15], v[48:55], 0, v198, v198 op_sel_hi:[0,0,0]
	v_mfma_scale_f32_16x16x128_f8f6f4 v[84:87], v[0:7], v[48:55], 0, v198, v198 op_sel_hi:[0,0,0]
	v_mfma_scale_f32_16x16x128_f8f6f4 v[80:83], v[8:15], v[40:47], 0, v198, v198 op_sel_hi:[0,0,0]
	v_mfma_scale_f32_16x16x128_f8f6f4 v[76:79], v[0:7], v[40:47], 0, v198, v198 op_sel_hi:[0,0,0]
	v_mfma_scale_f32_16x16x128_f8f6f4 v[72:75], v[8:15], v[32:39], 0, v198, v198 op_sel_hi:[0,0,0]
	v_mfma_scale_f32_16x16x128_f8f6f4 v[68:71], v[0:7], v[32:39], 0, v198, v198 op_sel_hi:[0,0,0]
	s_setprio 0
	s_barrier
	ds_read_b128 v[24:27], v202 offset:0x8000
	ds_read_b128 v[28:31], v202 offset:0x8400
	ds_read_b128 v[16:19], v202 offset:0x8800
	ds_read_b128 v[20:23], v202 offset:0x8c00
	s_mov_b32 m0, s50
	ds_read_b128 v[32:35], v201 offset:0x8000
	ds_read_b128 v[36:39], v201 offset:0x8400
	ds_read_b128 v[40:43], v201 offset:0x8800
	ds_read_b128 v[44:47], v201 offset:0x8c00
	ds_read_b128 v[48:51], v201 offset:0x9000
	ds_read_b128 v[52:55], v201 offset:0x9400
	ds_read_b128 v[56:59], v201 offset:0x9800
	ds_read_b128 v[60:63], v201 offset:0x9c00
	ds_read_b128 v[8:11], v202 offset:0xc000
	ds_read_b128 v[12:15], v202 offset:0xc400
	ds_read_b128 v[0:3], v202 offset:0xc800
	ds_read_b128 v[4:7], v202 offset:0xcc00
	s_nop 0
	buffer_load_dwordx4 v207, s[4:7], s33 offen lds
	s_mov_b32 m0, s51
	s_nop 0
	buffer_load_dwordx4 v206, s[4:7], s33 offen lds
	s_waitcnt vmcnt(8)
	s_waitcnt lgkmcnt(4)
	s_barrier
	s_setprio 1
	v_mfma_scale_f32_16x16x128_f8f6f4 v[192:195], v[24:31], v[32:39], v[192:195], v198, v198 op_sel_hi:[0,0,0]
	v_mfma_scale_f32_16x16x128_f8f6f4 v[188:191], v[16:23], v[32:39], v[188:191], v198, v198 op_sel_hi:[0,0,0]
	v_mfma_scale_f32_16x16x128_f8f6f4 v[184:187], v[24:31], v[40:47], v[184:187], v198, v198 op_sel_hi:[0,0,0]
	v_mfma_scale_f32_16x16x128_f8f6f4 v[180:183], v[16:23], v[40:47], v[180:183], v198, v198 op_sel_hi:[0,0,0]
	v_mfma_scale_f32_16x16x128_f8f6f4 v[176:179], v[24:31], v[48:55], v[176:179], v198, v198 op_sel_hi:[0,0,0]
	v_mfma_scale_f32_16x16x128_f8f6f4 v[172:175], v[16:23], v[48:55], v[172:175], v198, v198 op_sel_hi:[0,0,0]
	v_mfma_scale_f32_16x16x128_f8f6f4 v[168:171], v[24:31], v[56:63], v[168:171], v198, v198 op_sel_hi:[0,0,0]
	v_mfma_scale_f32_16x16x128_f8f6f4 v[164:167], v[16:23], v[56:63], v[164:167], v198, v198 op_sel_hi:[0,0,0]
	s_waitcnt lgkmcnt(0)
	s_setprio 0
	s_setprio 1
	v_mfma_scale_f32_16x16x128_f8f6f4 v[160:163], v[8:15], v[32:39], v[160:163], v198, v198 op_sel_hi:[0,0,0]
	v_mfma_scale_f32_16x16x128_f8f6f4 v[156:159], v[0:7], v[32:39], v[156:159], v198, v198 op_sel_hi:[0,0,0]
	v_mfma_scale_f32_16x16x128_f8f6f4 v[152:155], v[8:15], v[40:47], v[152:155], v198, v198 op_sel_hi:[0,0,0]
	v_mfma_scale_f32_16x16x128_f8f6f4 v[148:151], v[0:7], v[40:47], v[148:151], v198, v198 op_sel_hi:[0,0,0]
	v_mfma_scale_f32_16x16x128_f8f6f4 v[144:147], v[8:15], v[48:55], v[144:147], v198, v198 op_sel_hi:[0,0,0]
	v_mfma_scale_f32_16x16x128_f8f6f4 v[140:143], v[0:7], v[48:55], v[140:143], v198, v198 op_sel_hi:[0,0,0]
	v_mfma_scale_f32_16x16x128_f8f6f4 v[136:139], v[8:15], v[56:63], v[136:139], v198, v198 op_sel_hi:[0,0,0]
	v_mfma_scale_f32_16x16x128_f8f6f4 v[132:135], v[0:7], v[56:63], v[132:135], v198, v198 op_sel_hi:[0,0,0]
	s_setprio 0
	s_barrier
	s_mov_b32 m0, s64
	s_mov_b32 s10, s6
	s_mov_b32 s11, s7
	ds_read_b128 v[32:35], v201 offset:0xc000
	ds_read_b128 v[36:39], v201 offset:0xc400
	ds_read_b128 v[40:43], v201 offset:0xc800
	ds_read_b128 v[44:47], v201 offset:0xcc00
	ds_read_b128 v[48:51], v201 offset:0xd000
	ds_read_b128 v[52:55], v201 offset:0xd400
	ds_read_b128 v[56:59], v201 offset:0xd800
	ds_read_b128 v[60:63], v201 offset:0xdc00
	buffer_load_dwordx4 v200, s[8:11], s37 offen lds
	s_add_i32 s33, s61, 0x80180
	s_mov_b32 m0, s65
	s_nop 0
	buffer_load_dwordx4 v200, s[8:11], s33 offen lds
	s_add_i32 s33, s61, 0x8180
	s_mov_b32 m0, s70
	s_nop 0
	buffer_load_dwordx4 v200, s[8:11], s33 offen lds
	s_add_i32 s33, s61, 0x88180
	s_mov_b32 m0, s71
	s_nop 0
	buffer_load_dwordx4 v200, s[8:11], s33 offen lds
	s_mov_b32 m0, s68
	s_nop 0
	buffer_load_dwordx4 v205, s[4:7], s36 offen lds
	s_mov_b32 m0, s69
	s_nop 0
	buffer_load_dwordx4 v208, s[4:7], s36 offen lds
	s_waitcnt vmcnt(8)
	s_waitcnt lgkmcnt(0)
	s_barrier
	s_setprio 1
	v_mfma_scale_f32_16x16x128_f8f6f4 v[128:131], v[24:31], v[32:39], v[128:131], v198, v198 op_sel_hi:[0,0,0]
	v_mfma_scale_f32_16x16x128_f8f6f4 v[124:127], v[16:23], v[32:39], v[124:127], v198, v198 op_sel_hi:[0,0,0]
	v_mfma_scale_f32_16x16x128_f8f6f4 v[120:123], v[24:31], v[40:47], v[120:123], v198, v198 op_sel_hi:[0,0,0]
	v_mfma_scale_f32_16x16x128_f8f6f4 v[116:119], v[16:23], v[40:47], v[116:119], v198, v198 op_sel_hi:[0,0,0]
	v_mfma_scale_f32_16x16x128_f8f6f4 v[112:115], v[24:31], v[48:55], v[112:115], v198, v198 op_sel_hi:[0,0,0]
	v_mfma_scale_f32_16x16x128_f8f6f4 v[108:111], v[16:23], v[48:55], v[108:111], v198, v198 op_sel_hi:[0,0,0]
	v_mfma_scale_f32_16x16x128_f8f6f4 v[104:107], v[24:31], v[56:63], v[104:107], v198, v198 op_sel_hi:[0,0,0]
	v_mfma_scale_f32_16x16x128_f8f6f4 v[100:103], v[16:23], v[56:63], v[100:103], v198, v198 op_sel_hi:[0,0,0]
	s_setprio 0
	s_setprio 1
	v_mfma_scale_f32_16x16x128_f8f6f4 v[96:99], v[8:15], v[32:39], v[96:99], v198, v198 op_sel_hi:[0,0,0]
	v_mfma_scale_f32_16x16x128_f8f6f4 v[92:95], v[0:7], v[32:39], v[92:95], v198, v198 op_sel_hi:[0,0,0]
	v_mfma_scale_f32_16x16x128_f8f6f4 v[88:91], v[8:15], v[40:47], v[88:91], v198, v198 op_sel_hi:[0,0,0]
	v_mfma_scale_f32_16x16x128_f8f6f4 v[84:87], v[0:7], v[40:47], v[84:87], v198, v198 op_sel_hi:[0,0,0]
	v_mfma_scale_f32_16x16x128_f8f6f4 v[80:83], v[8:15], v[48:55], v[80:83], v198, v198 op_sel_hi:[0,0,0]
	v_mfma_scale_f32_16x16x128_f8f6f4 v[76:79], v[0:7], v[48:55], v[76:79], v198, v198 op_sel_hi:[0,0,0]
	v_mfma_scale_f32_16x16x128_f8f6f4 v[72:75], v[8:15], v[56:63], v[72:75], v198, v198 op_sel_hi:[0,0,0]
	v_mfma_scale_f32_16x16x128_f8f6f4 v[68:71], v[0:7], v[56:63], v[68:71], v198, v198 op_sel_hi:[0,0,0]
	s_setprio 0
	s_barrier
	s_waitcnt vmcnt(16)
	v_mbcnt_lo_u32_b32 v0, -1, 0
	v_mbcnt_hi_u32_b32 v0, -1, v0
	s_add_i32 s33, s61, 0x200
	v_lshl_add_u32 v0, v0, 4, s40
	v_ashrrev_i32_e32 v1, 31, v0
	v_lshrrev_b32_e32 v1, 22, v1
	v_add_u32_e32 v1, v0, v1
	v_ashrrev_i32_e32 v1, 10, v1
	v_mul_i32_i24_e32 v2, 0x400, v1
	v_sub_u32_e32 v2, v0, v2
	v_lshrrev_b32_e32 v3, 4, v2
	v_bitop3_b32 v3, v3, v2, 32 bitop3:0x6c
	v_ashrrev_i32_e32 v2, 31, v2
	v_lshrrev_b32_e32 v2, 26, v2
	v_add_u32_e32 v2, v3, v2
	v_and_b32_e32 v2, 0xc0, v2
	v_add_u32_e32 v0, 0x2000, v0
	v_sub_u32_e32 v2, v3, v2
	v_ashrrev_i32_e32 v3, 31, v0
	v_lshrrev_b32_e32 v3, 22, v3
	v_add_u32_e32 v3, v0, v3
	v_ashrrev_i32_e32 v3, 10, v3
	v_mul_i32_i24_e32 v4, 0x400, v3
	v_sub_u32_e32 v0, v0, v4
	v_lshrrev_b32_e32 v4, 4, v0
	v_bitop3_b32 v4, v4, v0, 32 bitop3:0x6c
	v_ashrrev_i32_e32 v0, 31, v0
	v_lshrrev_b32_e32 v0, 26, v0
	v_add_u32_e32 v0, v4, v0
	v_and_b32_e32 v0, 0xffc0, v0
	v_sub_u32_e32 v0, v4, v0
	v_lshrrev_b16_e32 v4, 7, v0
	v_and_b32_e32 v4, 1, v4
	v_add_u16_e32 v0, v0, v4
	v_lshlrev_b32_e32 v1, 5, v1
	v_ashrrev_i16_sdwa v2, v199, sext(v2) dst_sel:DWORD dst_unused:UNUSED_PAD src0_sel:DWORD src1_sel:BYTE_0
	v_lshlrev_b32_e32 v3, 5, v3
	v_ashrrev_i16_sdwa v0, v199, sext(v0) dst_sel:DWORD dst_unused:UNUSED_PAD src0_sel:DWORD src1_sel:BYTE_0
	v_and_b32_e32 v1, 32, v1
	v_bfe_i32 v2, v2, 0, 16
	v_and_b32_e32 v3, 32, v3
	v_bfe_i32 v0, v0, 0, 16
	v_add_lshl_u32 v1, v1, v2, 1
	v_add_lshl_u32 v0, v3, v0, 1
	v_lshl_add_u32 v32, v220, 12, v1
	v_lshl_add_u32 v33, v217, 12, v0
	v_lshl_add_u32 v34, v218, 12, v1
	v_lshl_add_u32 v35, v219, 12, v0
	s_mov_b32 s37, 0
.LBB0_1330:
	s_add_i32 s61, s36, 0x80
	s_cmp_eq_u32 s37, 28
	s_cselect_b64 vcc, -1, 0
	ds_read_b128 v[16:19], v202 offset:0
	ds_read_b128 v[20:23], v202 offset:0x400
	ds_read_b128 v[24:27], v202 offset:0x800
	ds_read_b128 v[28:31], v202 offset:0xc00
	s_and_b64 s[66:67], vcc, exec
	s_cselect_b32 s67, s85, s61
	s_cselect_b32 s66, s86, s33
	s_add_i32 s61, s67, 0x80
	s_mov_b32 m0, s73
	ds_read_b128 v[36:39], v201 offset:0
	ds_read_b128 v[40:43], v201 offset:0x400
	ds_read_b128 v[44:47], v201 offset:0x800
	ds_read_b128 v[48:51], v201 offset:0xc00
	ds_read_b128 v[52:55], v201 offset:0x1000
	ds_read_b128 v[56:59], v201 offset:0x1400
	ds_read_b128 v[218:221], v201 offset:0x1800
	ds_read_b128 v[222:225], v201 offset:0x1c00
	ds_read_b128 v[8:11], v202 offset:0x4000
	ds_read_b128 v[12:15], v202 offset:0x4400
	ds_read_b128 v[0:3], v202 offset:0x4800
	ds_read_b128 v[4:7], v202 offset:0x4c00
	s_nop 0
	buffer_load_dwordx4 v207, s[4:7], s36 offen lds
	s_mov_b32 m0, s74
	s_nop 0
	buffer_load_dwordx4 v206, s[4:7], s36 offen lds
	s_waitcnt vmcnt(8)
	s_waitcnt lgkmcnt(4)
	s_barrier
	s_setprio 1
	v_mfma_scale_f32_16x16x128_f8f6f4 v[192:195], v[16:23], v[36:43], v[192:195], v198, v198 op_sel_hi:[0,0,0]
	v_mfma_scale_f32_16x16x128_f8f6f4 v[188:191], v[24:31], v[36:43], v[188:191], v198, v198 op_sel_hi:[0,0,0]
	v_mfma_scale_f32_16x16x128_f8f6f4 v[184:187], v[16:23], v[44:51], v[184:187], v198, v198 op_sel_hi:[0,0,0]
	v_mfma_scale_f32_16x16x128_f8f6f4 v[180:183], v[24:31], v[44:51], v[180:183], v198, v198 op_sel_hi:[0,0,0]
	v_mfma_scale_f32_16x16x128_f8f6f4 v[176:179], v[16:23], v[52:59], v[176:179], v198, v198 op_sel_hi:[0,0,0]
	v_mfma_scale_f32_16x16x128_f8f6f4 v[172:175], v[24:31], v[52:59], v[172:175], v198, v198 op_sel_hi:[0,0,0]
	v_mfma_scale_f32_16x16x128_f8f6f4 v[168:171], v[16:23], v[218:225], v[168:171], v198, v198 op_sel_hi:[0,0,0]
	v_mfma_scale_f32_16x16x128_f8f6f4 v[164:167], v[24:31], v[218:225], v[164:167], v198, v198 op_sel_hi:[0,0,0]
	s_waitcnt lgkmcnt(0)
	s_setprio 0
	s_setprio 1
	v_mfma_scale_f32_16x16x128_f8f6f4 v[160:163], v[8:15], v[36:43], v[160:163], v198, v198 op_sel_hi:[0,0,0]
	v_mfma_scale_f32_16x16x128_f8f6f4 v[156:159], v[0:7], v[36:43], v[156:159], v198, v198 op_sel_hi:[0,0,0]
	v_mfma_scale_f32_16x16x128_f8f6f4 v[152:155], v[8:15], v[44:51], v[152:155], v198, v198 op_sel_hi:[0,0,0]
	v_mfma_scale_f32_16x16x128_f8f6f4 v[148:151], v[0:7], v[44:51], v[148:151], v198, v198 op_sel_hi:[0,0,0]
	v_mfma_scale_f32_16x16x128_f8f6f4 v[144:147], v[8:15], v[52:59], v[144:147], v198, v198 op_sel_hi:[0,0,0]
	v_mfma_scale_f32_16x16x128_f8f6f4 v[140:143], v[0:7], v[52:59], v[140:143], v198, v198 op_sel_hi:[0,0,0]
	v_mfma_scale_f32_16x16x128_f8f6f4 v[136:139], v[8:15], v[218:225], v[136:139], v198, v198 op_sel_hi:[0,0,0]
	v_mfma_scale_f32_16x16x128_f8f6f4 v[132:135], v[0:7], v[218:225], v[132:135], v198, v198 op_sel_hi:[0,0,0]
	s_setprio 0
	s_barrier
	s_mov_b32 m0, s45
	ds_read_b128 v[36:39], v201 offset:0x4000
	ds_read_b128 v[40:43], v201 offset:0x4400
	ds_read_b128 v[44:47], v201 offset:0x4800
	ds_read_b128 v[48:51], v201 offset:0x4c00
	ds_read_b128 v[52:55], v201 offset:0x5000
	ds_read_b128 v[56:59], v201 offset:0x5400
	ds_read_b128 v[218:221], v201 offset:0x5800
	ds_read_b128 v[222:225], v201 offset:0x5c00
	s_nop 0
	buffer_load_dwordx4 v200, s[8:11], s66 offen lds
	s_add_i32 s89, s66, 0x80000
	s_mov_b32 m0, s46
	v_cndmask_b32_e32 v60, v205, v32, vcc
	buffer_load_dwordx4 v200, s[8:11], s89 offen lds
	s_add_i32 s89, s66, 0x8000
	s_mov_b32 m0, s47
	v_cndmask_b32_e32 v61, v208, v33, vcc
	buffer_load_dwordx4 v200, s[8:11], s89 offen lds
	s_add_i32 s89, s66, 0x88000
	s_mov_b32 m0, s48
	s_nop 0
	buffer_load_dwordx4 v200, s[8:11], s89 offen lds
	s_mov_b32 m0, s44
	s_nop 0
	buffer_load_dwordx4 v60, s[4:7], s67 offen lds
	s_mov_b32 m0, s49
	s_nop 0
	buffer_load_dwordx4 v61, s[4:7], s67 offen lds
	s_waitcnt vmcnt(8)
	s_waitcnt lgkmcnt(0)
	s_barrier
	s_setprio 1
	v_mfma_scale_f32_16x16x128_f8f6f4 v[128:131], v[16:23], v[36:43], v[128:131], v198, v198 op_sel_hi:[0,0,0]
	v_mfma_scale_f32_16x16x128_f8f6f4 v[124:127], v[24:31], v[36:43], v[124:127], v198, v198 op_sel_hi:[0,0,0]
	v_mfma_scale_f32_16x16x128_f8f6f4 v[120:123], v[16:23], v[44:51], v[120:123], v198, v198 op_sel_hi:[0,0,0]
	v_mfma_scale_f32_16x16x128_f8f6f4 v[116:119], v[24:31], v[44:51], v[116:119], v198, v198 op_sel_hi:[0,0,0]
	v_mfma_scale_f32_16x16x128_f8f6f4 v[112:115], v[16:23], v[52:59], v[112:115], v198, v198 op_sel_hi:[0,0,0]
	v_mfma_scale_f32_16x16x128_f8f6f4 v[108:111], v[24:31], v[52:59], v[108:111], v198, v198 op_sel_hi:[0,0,0]
	v_mfma_scale_f32_16x16x128_f8f6f4 v[104:107], v[16:23], v[218:225], v[104:107], v198, v198 op_sel_hi:[0,0,0]
	v_mfma_scale_f32_16x16x128_f8f6f4 v[100:103], v[24:31], v[218:225], v[100:103], v198, v198 op_sel_hi:[0,0,0]
	s_setprio 0
	s_setprio 1
	v_mfma_scale_f32_16x16x128_f8f6f4 v[96:99], v[8:15], v[36:43], v[96:99], v198, v198 op_sel_hi:[0,0,0]
	v_mfma_scale_f32_16x16x128_f8f6f4 v[92:95], v[0:7], v[36:43], v[92:95], v198, v198 op_sel_hi:[0,0,0]
	v_mfma_scale_f32_16x16x128_f8f6f4 v[88:91], v[8:15], v[44:51], v[88:91], v198, v198 op_sel_hi:[0,0,0]
	v_mfma_scale_f32_16x16x128_f8f6f4 v[84:87], v[0:7], v[44:51], v[84:87], v198, v198 op_sel_hi:[0,0,0]
	v_mfma_scale_f32_16x16x128_f8f6f4 v[80:83], v[8:15], v[52:59], v[80:83], v198, v198 op_sel_hi:[0,0,0]
	v_mfma_scale_f32_16x16x128_f8f6f4 v[76:79], v[0:7], v[52:59], v[76:79], v198, v198 op_sel_hi:[0,0,0]
	v_mfma_scale_f32_16x16x128_f8f6f4 v[72:75], v[8:15], v[218:225], v[72:75], v198, v198 op_sel_hi:[0,0,0]
	v_mfma_scale_f32_16x16x128_f8f6f4 v[68:71], v[0:7], v[218:225], v[68:71], v198, v198 op_sel_hi:[0,0,0]
	s_setprio 0
	s_barrier
	ds_read_b128 v[24:27], v202 offset:0x8000
	ds_read_b128 v[28:31], v202 offset:0x8400
	ds_read_b128 v[16:19], v202 offset:0x8800
	ds_read_b128 v[20:23], v202 offset:0x8c00
	s_mov_b32 m0, s50
	v_cndmask_b32_e32 v62, v207, v34, vcc
	ds_read_b128 v[36:39], v201 offset:0x8000
	ds_read_b128 v[40:43], v201 offset:0x8400
	ds_read_b128 v[44:47], v201 offset:0x8800
	ds_read_b128 v[48:51], v201 offset:0x8c00
	ds_read_b128 v[52:55], v201 offset:0x9000
	ds_read_b128 v[56:59], v201 offset:0x9400
	ds_read_b128 v[218:221], v201 offset:0x9800
	ds_read_b128 v[222:225], v201 offset:0x9c00
	ds_read_b128 v[8:11], v202 offset:0xc000
	ds_read_b128 v[12:15], v202 offset:0xc400
	ds_read_b128 v[0:3], v202 offset:0xc800
	ds_read_b128 v[4:7], v202 offset:0xcc00
	buffer_load_dwordx4 v62, s[4:7], s67 offen lds
	v_cndmask_b32_e32 v62, v206, v35, vcc
	s_mov_b32 m0, s51
	s_nop 0
	buffer_load_dwordx4 v62, s[4:7], s67 offen lds
	s_waitcnt vmcnt(8)
	s_waitcnt lgkmcnt(4)
	s_barrier
	s_setprio 1
	v_mfma_scale_f32_16x16x128_f8f6f4 v[192:195], v[24:31], v[36:43], v[192:195], v198, v198 op_sel_hi:[0,0,0]
	v_mfma_scale_f32_16x16x128_f8f6f4 v[188:191], v[16:23], v[36:43], v[188:191], v198, v198 op_sel_hi:[0,0,0]
	v_mfma_scale_f32_16x16x128_f8f6f4 v[184:187], v[24:31], v[44:51], v[184:187], v198, v198 op_sel_hi:[0,0,0]
	v_mfma_scale_f32_16x16x128_f8f6f4 v[180:183], v[16:23], v[44:51], v[180:183], v198, v198 op_sel_hi:[0,0,0]
	v_mfma_scale_f32_16x16x128_f8f6f4 v[176:179], v[24:31], v[52:59], v[176:179], v198, v198 op_sel_hi:[0,0,0]
	v_mfma_scale_f32_16x16x128_f8f6f4 v[172:175], v[16:23], v[52:59], v[172:175], v198, v198 op_sel_hi:[0,0,0]
	v_mfma_scale_f32_16x16x128_f8f6f4 v[168:171], v[24:31], v[218:225], v[168:171], v198, v198 op_sel_hi:[0,0,0]
	v_mfma_scale_f32_16x16x128_f8f6f4 v[164:167], v[16:23], v[218:225], v[164:167], v198, v198 op_sel_hi:[0,0,0]
	s_waitcnt lgkmcnt(0)
	s_setprio 0
	s_setprio 1
	v_mfma_scale_f32_16x16x128_f8f6f4 v[160:163], v[8:15], v[36:43], v[160:163], v198, v198 op_sel_hi:[0,0,0]
	v_mfma_scale_f32_16x16x128_f8f6f4 v[156:159], v[0:7], v[36:43], v[156:159], v198, v198 op_sel_hi:[0,0,0]
	v_mfma_scale_f32_16x16x128_f8f6f4 v[152:155], v[8:15], v[44:51], v[152:155], v198, v198 op_sel_hi:[0,0,0]
	v_mfma_scale_f32_16x16x128_f8f6f4 v[148:151], v[0:7], v[44:51], v[148:151], v198, v198 op_sel_hi:[0,0,0]
	v_mfma_scale_f32_16x16x128_f8f6f4 v[144:147], v[8:15], v[52:59], v[144:147], v198, v198 op_sel_hi:[0,0,0]
	v_mfma_scale_f32_16x16x128_f8f6f4 v[140:143], v[0:7], v[52:59], v[140:143], v198, v198 op_sel_hi:[0,0,0]
	v_mfma_scale_f32_16x16x128_f8f6f4 v[136:139], v[8:15], v[218:225], v[136:139], v198, v198 op_sel_hi:[0,0,0]
	v_mfma_scale_f32_16x16x128_f8f6f4 v[132:135], v[0:7], v[218:225], v[132:135], v198, v198 op_sel_hi:[0,0,0]
	s_setprio 0
	s_barrier
	s_mov_b32 m0, s64
	s_add_i32 s67, s66, 0x80
	ds_read_b128 v[36:39], v201 offset:0xc000
	ds_read_b128 v[40:43], v201 offset:0xc400
	ds_read_b128 v[44:47], v201 offset:0xc800
	ds_read_b128 v[48:51], v201 offset:0xcc00
	ds_read_b128 v[52:55], v201 offset:0xd000
	ds_read_b128 v[56:59], v201 offset:0xd400
	ds_read_b128 v[218:221], v201 offset:0xd800
	ds_read_b128 v[222:225], v201 offset:0xdc00
	buffer_load_dwordx4 v200, s[8:11], s67 offen lds
	s_add_i32 s67, s66, 0x80080
	s_mov_b32 m0, s65
	s_nop 0
	buffer_load_dwordx4 v200, s[8:11], s67 offen lds
	s_add_i32 s67, s66, 0x8080
	s_mov_b32 m0, s70
	s_add_i32 s66, s66, 0x88080
	buffer_load_dwordx4 v200, s[8:11], s67 offen lds
	s_mov_b32 m0, s71
	s_nop 0
	buffer_load_dwordx4 v200, s[8:11], s66 offen lds
	s_mov_b32 m0, s68
	s_nop 0
	buffer_load_dwordx4 v60, s[4:7], s61 offen lds
	s_mov_b32 m0, s69
	s_nop 0
	buffer_load_dwordx4 v61, s[4:7], s61 offen lds
	s_waitcnt vmcnt(8)
	s_waitcnt lgkmcnt(0)
	s_barrier
	s_setprio 1
	v_mfma_scale_f32_16x16x128_f8f6f4 v[128:131], v[24:31], v[36:43], v[128:131], v198, v198 op_sel_hi:[0,0,0]
	v_mfma_scale_f32_16x16x128_f8f6f4 v[124:127], v[16:23], v[36:43], v[124:127], v198, v198 op_sel_hi:[0,0,0]
	v_mfma_scale_f32_16x16x128_f8f6f4 v[120:123], v[24:31], v[44:51], v[120:123], v198, v198 op_sel_hi:[0,0,0]
	v_mfma_scale_f32_16x16x128_f8f6f4 v[116:119], v[16:23], v[44:51], v[116:119], v198, v198 op_sel_hi:[0,0,0]
	v_mfma_scale_f32_16x16x128_f8f6f4 v[112:115], v[24:31], v[52:59], v[112:115], v198, v198 op_sel_hi:[0,0,0]
	v_mfma_scale_f32_16x16x128_f8f6f4 v[108:111], v[16:23], v[52:59], v[108:111], v198, v198 op_sel_hi:[0,0,0]
	v_mfma_scale_f32_16x16x128_f8f6f4 v[104:107], v[24:31], v[218:225], v[104:107], v198, v198 op_sel_hi:[0,0,0]
	v_mfma_scale_f32_16x16x128_f8f6f4 v[100:103], v[16:23], v[218:225], v[100:103], v198, v198 op_sel_hi:[0,0,0]
	s_setprio 0
	s_setprio 1
	v_mfma_scale_f32_16x16x128_f8f6f4 v[96:99], v[8:15], v[36:43], v[96:99], v198, v198 op_sel_hi:[0,0,0]
	v_mfma_scale_f32_16x16x128_f8f6f4 v[92:95], v[0:7], v[36:43], v[92:95], v198, v198 op_sel_hi:[0,0,0]
	v_mfma_scale_f32_16x16x128_f8f6f4 v[88:91], v[8:15], v[44:51], v[88:91], v198, v198 op_sel_hi:[0,0,0]
	v_mfma_scale_f32_16x16x128_f8f6f4 v[84:87], v[0:7], v[44:51], v[84:87], v198, v198 op_sel_hi:[0,0,0]
	v_mfma_scale_f32_16x16x128_f8f6f4 v[80:83], v[8:15], v[52:59], v[80:83], v198, v198 op_sel_hi:[0,0,0]
	v_mfma_scale_f32_16x16x128_f8f6f4 v[76:79], v[0:7], v[52:59], v[76:79], v198, v198 op_sel_hi:[0,0,0]
	v_mfma_scale_f32_16x16x128_f8f6f4 v[72:75], v[8:15], v[218:225], v[72:75], v198, v198 op_sel_hi:[0,0,0]
	v_mfma_scale_f32_16x16x128_f8f6f4 v[68:71], v[0:7], v[218:225], v[68:71], v198, v198 op_sel_hi:[0,0,0]
	s_setprio 0
	s_barrier
	s_add_i32 s37, s37, 2
	s_addk_i32 s36, 0x100
	s_addk_i32 s33, 0x100
	s_cmp_gt_u32 s37, 29
	s_cbranch_scc0 .LBB0_1330
	s_and_b64 vcc, exec, s[28:29]
	s_cbranch_vccz .LBB0_1333
	s_barrier

.LBB0_1369:
	s_add_i32 s33, s88, 0x180
	s_add_i32 s40, s89, 0x180
	s_waitcnt lgkmcnt(0)
	s_barrier
	s_setprio 1
	v_mfma_scale_f32_16x16x128_f8f6f4 v[128:131], v[24:31], v[56:63], 0, v235, v235 op_sel_hi:[0,0,0]
	v_mfma_scale_f32_16x16x128_f8f6f4 v[124:127], v[16:23], v[56:63], 0, v235, v235 op_sel_hi:[0,0,0]
	v_mfma_scale_f32_16x16x128_f8f6f4 v[120:123], v[24:31], v[48:55], 0, v235, v235 op_sel_hi:[0,0,0]
	v_mfma_scale_f32_16x16x128_f8f6f4 v[116:119], v[16:23], v[48:55], 0, v235, v235 op_sel_hi:[0,0,0]
	v_mfma_scale_f32_16x16x128_f8f6f4 v[112:115], v[24:31], v[40:47], 0, v235, v235 op_sel_hi:[0,0,0]
	v_mfma_scale_f32_16x16x128_f8f6f4 v[108:111], v[16:23], v[40:47], 0, v235, v235 op_sel_hi:[0,0,0]
	v_mfma_scale_f32_16x16x128_f8f6f4 v[104:107], v[24:31], v[32:39], 0, v235, v235 op_sel_hi:[0,0,0]
	v_mfma_scale_f32_16x16x128_f8f6f4 v[100:103], v[16:23], v[32:39], 0, v235, v235 op_sel_hi:[0,0,0]
	s_setprio 0
	s_setprio 1
	v_mfma_scale_f32_16x16x128_f8f6f4 v[96:99], v[8:15], v[56:63], 0, v235, v235 op_sel_hi:[0,0,0]
	v_mfma_scale_f32_16x16x128_f8f6f4 v[92:95], v[0:7], v[56:63], 0, v235, v235 op_sel_hi:[0,0,0]
	v_mfma_scale_f32_16x16x128_f8f6f4 v[88:91], v[8:15], v[48:55], 0, v235, v235 op_sel_hi:[0,0,0]
	v_mfma_scale_f32_16x16x128_f8f6f4 v[84:87], v[0:7], v[48:55], 0, v235, v235 op_sel_hi:[0,0,0]
	v_mfma_scale_f32_16x16x128_f8f6f4 v[80:83], v[8:15], v[40:47], 0, v235, v235 op_sel_hi:[0,0,0]
	v_mfma_scale_f32_16x16x128_f8f6f4 v[76:79], v[0:7], v[40:47], 0, v235, v235 op_sel_hi:[0,0,0]
	v_mfma_scale_f32_16x16x128_f8f6f4 v[72:75], v[8:15], v[32:39], 0, v235, v235 op_sel_hi:[0,0,0]
	v_mfma_scale_f32_16x16x128_f8f6f4 v[68:71], v[0:7], v[32:39], 0, v235, v235 op_sel_hi:[0,0,0]
	s_setprio 0
	s_barrier
	ds_read_b128 v[16:19], v233 offset:0x8000
	ds_read_b128 v[20:23], v233 offset:0x8400
	ds_read_b128 v[24:27], v233 offset:0x8800
	ds_read_b128 v[28:31], v233 offset:0x8c00
	s_mov_b32 m0, s62
	s_add_i32 s10, s88, 0x10100
	ds_read_b128 v[32:35], v232 offset:0x8000
	ds_read_b128 v[36:39], v232 offset:0x8400
	ds_read_b128 v[40:43], v232 offset:0x8800
	ds_read_b128 v[44:47], v232 offset:0x8c00
	ds_read_b128 v[48:51], v232 offset:0x9000
	ds_read_b128 v[52:55], v232 offset:0x9400
	ds_read_b128 v[56:59], v232 offset:0x9800
	ds_read_b128 v[60:63], v232 offset:0x9c00
	ds_read_b128 v[8:11], v233 offset:0xc000
	ds_read_b128 v[12:15], v233 offset:0xc400
	ds_read_b128 v[0:3], v233 offset:0xc800
	ds_read_b128 v[4:7], v233 offset:0xcc00
	buffer_load_dwordx4 v230, s[4:7], s10 offen lds
	s_add_i32 s10, s88, 0x18100
	s_mov_b32 m0, s63
	s_nop 0
	buffer_load_dwordx4 v230, s[4:7], s10 offen lds
	s_waitcnt vmcnt(8)
	s_waitcnt lgkmcnt(4)
	s_barrier
	s_setprio 1
	v_mfma_scale_f32_16x16x128_f8f6f4 v[192:195], v[16:23], v[32:39], v[192:195], v235, v235 op_sel_hi:[0,0,0]
	v_mfma_scale_f32_16x16x128_f8f6f4 v[188:191], v[24:31], v[32:39], v[188:191], v235, v235 op_sel_hi:[0,0,0]
	v_mfma_scale_f32_16x16x128_f8f6f4 v[184:187], v[16:23], v[40:47], v[184:187], v235, v235 op_sel_hi:[0,0,0]
	v_mfma_scale_f32_16x16x128_f8f6f4 v[180:183], v[24:31], v[40:47], v[180:183], v235, v235 op_sel_hi:[0,0,0]
	v_mfma_scale_f32_16x16x128_f8f6f4 v[176:179], v[16:23], v[48:55], v[176:179], v235, v235 op_sel_hi:[0,0,0]
	v_mfma_scale_f32_16x16x128_f8f6f4 v[172:175], v[24:31], v[48:55], v[172:175], v235, v235 op_sel_hi:[0,0,0]
	v_mfma_scale_f32_16x16x128_f8f6f4 v[168:171], v[16:23], v[56:63], v[168:171], v235, v235 op_sel_hi:[0,0,0]
	v_mfma_scale_f32_16x16x128_f8f6f4 v[164:167], v[24:31], v[56:63], v[164:167], v235, v235 op_sel_hi:[0,0,0]
	s_waitcnt lgkmcnt(0)
	s_setprio 0
	s_setprio 1
	v_mfma_scale_f32_16x16x128_f8f6f4 v[160:163], v[8:15], v[32:39], v[160:163], v235, v235 op_sel_hi:[0,0,0]
	v_mfma_scale_f32_16x16x128_f8f6f4 v[156:159], v[0:7], v[32:39], v[156:159], v235, v235 op_sel_hi:[0,0,0]
	v_mfma_scale_f32_16x16x128_f8f6f4 v[152:155], v[8:15], v[40:47], v[152:155], v235, v235 op_sel_hi:[0,0,0]
	v_mfma_scale_f32_16x16x128_f8f6f4 v[148:151], v[0:7], v[40:47], v[148:151], v235, v235 op_sel_hi:[0,0,0]
	v_mfma_scale_f32_16x16x128_f8f6f4 v[144:147], v[8:15], v[48:55], v[144:147], v235, v235 op_sel_hi:[0,0,0]
	v_mfma_scale_f32_16x16x128_f8f6f4 v[140:143], v[0:7], v[48:55], v[140:143], v235, v235 op_sel_hi:[0,0,0]
	v_mfma_scale_f32_16x16x128_f8f6f4 v[136:139], v[8:15], v[56:63], v[136:139], v235, v235 op_sel_hi:[0,0,0]
	v_mfma_scale_f32_16x16x128_f8f6f4 v[132:135], v[0:7], v[56:63], v[132:135], v235, v235 op_sel_hi:[0,0,0]
	s_setprio 0
	s_barrier
	s_mov_b32 m0, s64
	s_mov_b32 s10, s6
	s_mov_b32 s11, s7
	ds_read_b128 v[32:35], v232 offset:0xc000
	ds_read_b128 v[36:39], v232 offset:0xc400
	ds_read_b128 v[40:43], v232 offset:0xc800
	ds_read_b128 v[44:47], v232 offset:0xcc00
	ds_read_b128 v[48:51], v232 offset:0xd000
	ds_read_b128 v[52:55], v232 offset:0xd400
	ds_read_b128 v[56:59], v232 offset:0xd800
	ds_read_b128 v[60:63], v232 offset:0xdc00
	buffer_load_dwordx4 v231, s[8:11], s40 offen lds
	s_add_i32 s40, s89, 0x10180
	s_mov_b32 m0, s65
	s_nop 0
	buffer_load_dwordx4 v231, s[8:11], s40 offen lds
	s_add_i32 s40, s89, 0x1180
	s_mov_b32 m0, s70
	s_nop 0
	buffer_load_dwordx4 v231, s[8:11], s40 offen lds
	s_add_i32 s40, s89, 0x11180
	s_mov_b32 m0, s71
	s_nop 0
	buffer_load_dwordx4 v231, s[8:11], s40 offen lds
	s_mov_b32 m0, s68
	s_nop 0
	buffer_load_dwordx4 v230, s[4:7], s33 offen lds
	s_add_i32 s33, s88, 0x8180
	s_mov_b32 m0, s69
	s_nop 0
	buffer_load_dwordx4 v230, s[4:7], s33 offen lds
	s_waitcnt vmcnt(8)
	s_waitcnt lgkmcnt(0)
	s_barrier
	s_setprio 1
	v_mfma_scale_f32_16x16x128_f8f6f4 v[128:131], v[16:23], v[32:39], v[128:131], v235, v235 op_sel_hi:[0,0,0]
	v_mfma_scale_f32_16x16x128_f8f6f4 v[124:127], v[24:31], v[32:39], v[124:127], v235, v235 op_sel_hi:[0,0,0]
	v_mfma_scale_f32_16x16x128_f8f6f4 v[120:123], v[16:23], v[40:47], v[120:123], v235, v235 op_sel_hi:[0,0,0]
	v_mfma_scale_f32_16x16x128_f8f6f4 v[116:119], v[24:31], v[40:47], v[116:119], v235, v235 op_sel_hi:[0,0,0]
	v_mfma_scale_f32_16x16x128_f8f6f4 v[112:115], v[16:23], v[48:55], v[112:115], v235, v235 op_sel_hi:[0,0,0]
	v_mfma_scale_f32_16x16x128_f8f6f4 v[108:111], v[24:31], v[48:55], v[108:111], v235, v235 op_sel_hi:[0,0,0]
	v_mfma_scale_f32_16x16x128_f8f6f4 v[104:107], v[16:23], v[56:63], v[104:107], v235, v235 op_sel_hi:[0,0,0]
	v_mfma_scale_f32_16x16x128_f8f6f4 v[100:103], v[24:31], v[56:63], v[100:103], v235, v235 op_sel_hi:[0,0,0]
	s_setprio 0
	s_setprio 1
	v_mfma_scale_f32_16x16x128_f8f6f4 v[96:99], v[8:15], v[32:39], v[96:99], v235, v235 op_sel_hi:[0,0,0]
	v_mfma_scale_f32_16x16x128_f8f6f4 v[92:95], v[0:7], v[32:39], v[92:95], v235, v235 op_sel_hi:[0,0,0]
	v_mfma_scale_f32_16x16x128_f8f6f4 v[88:91], v[8:15], v[40:47], v[88:91], v235, v235 op_sel_hi:[0,0,0]
	v_mfma_scale_f32_16x16x128_f8f6f4 v[84:87], v[0:7], v[40:47], v[84:87], v235, v235 op_sel_hi:[0,0,0]
	v_mfma_scale_f32_16x16x128_f8f6f4 v[80:83], v[8:15], v[48:55], v[80:83], v235, v235 op_sel_hi:[0,0,0]
	v_mfma_scale_f32_16x16x128_f8f6f4 v[76:79], v[0:7], v[48:55], v[76:79], v235, v235 op_sel_hi:[0,0,0]
	v_mfma_scale_f32_16x16x128_f8f6f4 v[72:75], v[8:15], v[56:63], v[72:75], v235, v235 op_sel_hi:[0,0,0]
	v_mfma_scale_f32_16x16x128_f8f6f4 v[68:71], v[0:7], v[56:63], v[68:71], v235, v235 op_sel_hi:[0,0,0]
	s_setprio 0
	s_barrier
	ds_read_b128 v[16:19], v233 offset:0
	ds_read_b128 v[20:23], v233 offset:0x400
	ds_read_b128 v[24:27], v233 offset:0x800
	ds_read_b128 v[28:31], v233 offset:0xc00
	s_add_i32 s33, s85, 0x80
	s_mov_b32 m0, s74
	s_add_i32 s40, s88, 0x10180
	ds_read_b128 v[32:35], v232 offset:0
	ds_read_b128 v[36:39], v232 offset:0x400
	ds_read_b128 v[40:43], v232 offset:0x800
	ds_read_b128 v[44:47], v232 offset:0xc00
	ds_read_b128 v[48:51], v232 offset:0x1000
	ds_read_b128 v[52:55], v232 offset:0x1400
	ds_read_b128 v[56:59], v232 offset:0x1800
	ds_read_b128 v[60:63], v232 offset:0x1c00
	ds_read_b128 v[8:11], v233 offset:0x4000
	ds_read_b128 v[12:15], v233 offset:0x4400
	ds_read_b128 v[0:3], v233 offset:0x4800
	ds_read_b128 v[4:7], v233 offset:0x4c00
	buffer_load_dwordx4 v230, s[4:7], s40 offen lds
	s_add_i32 s40, s88, 0x18180
	s_mov_b32 m0, s76
	s_nop 0
	buffer_load_dwordx4 v230, s[4:7], s40 offen lds
	s_waitcnt vmcnt(8)
	s_waitcnt lgkmcnt(4)
	s_barrier
	s_setprio 1
	v_mfma_scale_f32_16x16x128_f8f6f4 v[192:195], v[16:23], v[32:39], v[192:195], v235, v235 op_sel_hi:[0,0,0]
	v_mfma_scale_f32_16x16x128_f8f6f4 v[188:191], v[24:31], v[32:39], v[188:191], v235, v235 op_sel_hi:[0,0,0]
	v_mfma_scale_f32_16x16x128_f8f6f4 v[184:187], v[16:23], v[40:47], v[184:187], v235, v235 op_sel_hi:[0,0,0]
	v_mfma_scale_f32_16x16x128_f8f6f4 v[180:183], v[24:31], v[40:47], v[180:183], v235, v235 op_sel_hi:[0,0,0]
	v_mfma_scale_f32_16x16x128_f8f6f4 v[176:179], v[16:23], v[48:55], v[176:179], v235, v235 op_sel_hi:[0,0,0]
	v_mfma_scale_f32_16x16x128_f8f6f4 v[172:175], v[24:31], v[48:55], v[172:175], v235, v235 op_sel_hi:[0,0,0]
	v_mfma_scale_f32_16x16x128_f8f6f4 v[168:171], v[16:23], v[56:63], v[168:171], v235, v235 op_sel_hi:[0,0,0]
	v_mfma_scale_f32_16x16x128_f8f6f4 v[164:167], v[24:31], v[56:63], v[164:167], v235, v235 op_sel_hi:[0,0,0]
	s_waitcnt lgkmcnt(0)
	s_setprio 0
	s_setprio 1
	v_mfma_scale_f32_16x16x128_f8f6f4 v[160:163], v[8:15], v[32:39], v[160:163], v235, v235 op_sel_hi:[0,0,0]
	v_mfma_scale_f32_16x16x128_f8f6f4 v[156:159], v[0:7], v[32:39], v[156:159], v235, v235 op_sel_hi:[0,0,0]
	v_mfma_scale_f32_16x16x128_f8f6f4 v[152:155], v[8:15], v[40:47], v[152:155], v235, v235 op_sel_hi:[0,0,0]
	v_mfma_scale_f32_16x16x128_f8f6f4 v[148:151], v[0:7], v[40:47], v[148:151], v235, v235 op_sel_hi:[0,0,0]
	v_mfma_scale_f32_16x16x128_f8f6f4 v[144:147], v[8:15], v[48:55], v[144:147], v235, v235 op_sel_hi:[0,0,0]
	v_mfma_scale_f32_16x16x128_f8f6f4 v[140:143], v[0:7], v[48:55], v[140:143], v235, v235 op_sel_hi:[0,0,0]
	v_mfma_scale_f32_16x16x128_f8f6f4 v[136:139], v[8:15], v[56:63], v[136:139], v235, v235 op_sel_hi:[0,0,0]
	v_mfma_scale_f32_16x16x128_f8f6f4 v[132:135], v[0:7], v[56:63], v[132:135], v235, v235 op_sel_hi:[0,0,0]
	s_setprio 0
	s_barrier
	s_mov_b32 m0, s46
	ds_read_b128 v[32:35], v232 offset:0x4000
	ds_read_b128 v[36:39], v232 offset:0x4400
	ds_read_b128 v[40:43], v232 offset:0x4800
	ds_read_b128 v[44:47], v232 offset:0x4c00
	ds_read_b128 v[48:51], v232 offset:0x5000
	ds_read_b128 v[52:55], v232 offset:0x5400
	ds_read_b128 v[56:59], v232 offset:0x5800
	ds_read_b128 v[60:63], v232 offset:0x5c00
	s_nop 0
	buffer_load_dwordx4 v231, s[8:11], s86 offen lds
	s_add_i32 s40, s86, 0x10000
	s_mov_b32 m0, s47
	s_nop 0
	buffer_load_dwordx4 v231, s[8:11], s40 offen lds
	s_add_i32 s40, s86, 0x1000
	s_mov_b32 m0, s49
	s_nop 0
	buffer_load_dwordx4 v231, s[8:11], s40 offen lds
	s_add_i32 s40, s86, 0x11000
	s_mov_b32 m0, s50
	s_nop 0
	buffer_load_dwordx4 v231, s[8:11], s40 offen lds
	s_mov_b32 m0, s48
	s_add_i32 s40, s85, 0x8000
	buffer_load_dwordx4 v230, s[4:7], s85 offen lds
	s_mov_b32 m0, s51
	s_nop 0
	buffer_load_dwordx4 v230, s[4:7], s40 offen lds
	s_waitcnt vmcnt(8)
	s_waitcnt lgkmcnt(0)
	s_barrier
	s_setprio 1
	v_mfma_scale_f32_16x16x128_f8f6f4 v[128:131], v[16:23], v[32:39], v[128:131], v235, v235 op_sel_hi:[0,0,0]
	v_mfma_scale_f32_16x16x128_f8f6f4 v[124:127], v[24:31], v[32:39], v[124:127], v235, v235 op_sel_hi:[0,0,0]
	v_mfma_scale_f32_16x16x128_f8f6f4 v[120:123], v[16:23], v[40:47], v[120:123], v235, v235 op_sel_hi:[0,0,0]
	v_mfma_scale_f32_16x16x128_f8f6f4 v[116:119], v[24:31], v[40:47], v[116:119], v235, v235 op_sel_hi:[0,0,0]
	v_mfma_scale_f32_16x16x128_f8f6f4 v[112:115], v[16:23], v[48:55], v[112:115], v235, v235 op_sel_hi:[0,0,0]
	v_mfma_scale_f32_16x16x128_f8f6f4 v[108:111], v[24:31], v[48:55], v[108:111], v235, v235 op_sel_hi:[0,0,0]
	v_mfma_scale_f32_16x16x128_f8f6f4 v[104:107], v[16:23], v[56:63], v[104:107], v235, v235 op_sel_hi:[0,0,0]
	v_mfma_scale_f32_16x16x128_f8f6f4 v[100:103], v[24:31], v[56:63], v[100:103], v235, v235 op_sel_hi:[0,0,0]
	s_setprio 0
	s_setprio 1
	v_mfma_scale_f32_16x16x128_f8f6f4 v[96:99], v[8:15], v[32:39], v[96:99], v235, v235 op_sel_hi:[0,0,0]
	v_mfma_scale_f32_16x16x128_f8f6f4 v[92:95], v[0:7], v[32:39], v[92:95], v235, v235 op_sel_hi:[0,0,0]
	v_mfma_scale_f32_16x16x128_f8f6f4 v[88:91], v[8:15], v[40:47], v[88:91], v235, v235 op_sel_hi:[0,0,0]
	v_mfma_scale_f32_16x16x128_f8f6f4 v[84:87], v[0:7], v[40:47], v[84:87], v235, v235 op_sel_hi:[0,0,0]
	v_mfma_scale_f32_16x16x128_f8f6f4 v[80:83], v[8:15], v[48:55], v[80:83], v235, v235 op_sel_hi:[0,0,0]
	v_mfma_scale_f32_16x16x128_f8f6f4 v[76:79], v[0:7], v[48:55], v[76:79], v235, v235 op_sel_hi:[0,0,0]
	v_mfma_scale_f32_16x16x128_f8f6f4 v[72:75], v[8:15], v[56:63], v[72:75], v235, v235 op_sel_hi:[0,0,0]
	v_mfma_scale_f32_16x16x128_f8f6f4 v[68:71], v[0:7], v[56:63], v[68:71], v235, v235 op_sel_hi:[0,0,0]
	s_setprio 0
	s_barrier
	ds_read_b128 v[16:19], v233 offset:0x8000
	ds_read_b128 v[20:23], v233 offset:0x8400
	ds_read_b128 v[24:27], v233 offset:0x8800
	ds_read_b128 v[28:31], v233 offset:0x8c00
	s_mov_b32 m0, s62
	s_add_i32 s40, s85, 0x10000
	ds_read_b128 v[32:35], v232 offset:0x8000
	ds_read_b128 v[36:39], v232 offset:0x8400
	ds_read_b128 v[40:43], v232 offset:0x8800
	ds_read_b128 v[44:47], v232 offset:0x8c00
	ds_read_b128 v[48:51], v232 offset:0x9000
	ds_read_b128 v[52:55], v232 offset:0x9400
	ds_read_b128 v[56:59], v232 offset:0x9800
	ds_read_b128 v[60:63], v232 offset:0x9c00
	ds_read_b128 v[8:11], v233 offset:0xc000
	ds_read_b128 v[12:15], v233 offset:0xc400
	ds_read_b128 v[0:3], v233 offset:0xc800
	ds_read_b128 v[4:7], v233 offset:0xcc00
	buffer_load_dwordx4 v230, s[4:7], s40 offen lds
	s_add_i32 s40, s85, 0x18000
	s_mov_b32 m0, s63
	s_nop 0
	buffer_load_dwordx4 v230, s[4:7], s40 offen lds
	s_waitcnt vmcnt(8)
	s_waitcnt lgkmcnt(4)
	s_barrier
	s_setprio 1
	v_mfma_scale_f32_16x16x128_f8f6f4 v[192:195], v[16:23], v[32:39], v[192:195], v235, v235 op_sel_hi:[0,0,0]
	v_mfma_scale_f32_16x16x128_f8f6f4 v[188:191], v[24:31], v[32:39], v[188:191], v235, v235 op_sel_hi:[0,0,0]
	v_mfma_scale_f32_16x16x128_f8f6f4 v[184:187], v[16:23], v[40:47], v[184:187], v235, v235 op_sel_hi:[0,0,0]
	v_mfma_scale_f32_16x16x128_f8f6f4 v[180:183], v[24:31], v[40:47], v[180:183], v235, v235 op_sel_hi:[0,0,0]
	v_mfma_scale_f32_16x16x128_f8f6f4 v[176:179], v[16:23], v[48:55], v[176:179], v235, v235 op_sel_hi:[0,0,0]
	v_mfma_scale_f32_16x16x128_f8f6f4 v[172:175], v[24:31], v[48:55], v[172:175], v235, v235 op_sel_hi:[0,0,0]
	v_mfma_scale_f32_16x16x128_f8f6f4 v[168:171], v[16:23], v[56:63], v[168:171], v235, v235 op_sel_hi:[0,0,0]
	v_mfma_scale_f32_16x16x128_f8f6f4 v[164:167], v[24:31], v[56:63], v[164:167], v235, v235 op_sel_hi:[0,0,0]
	s_waitcnt lgkmcnt(0)
	s_setprio 0
	s_setprio 1
	v_mfma_scale_f32_16x16x128_f8f6f4 v[160:163], v[8:15], v[32:39], v[160:163], v235, v235 op_sel_hi:[0,0,0]
	v_mfma_scale_f32_16x16x128_f8f6f4 v[156:159], v[0:7], v[32:39], v[156:159], v235, v235 op_sel_hi:[0,0,0]
	v_mfma_scale_f32_16x16x128_f8f6f4 v[152:155], v[8:15], v[40:47], v[152:155], v235, v235 op_sel_hi:[0,0,0]
	v_mfma_scale_f32_16x16x128_f8f6f4 v[148:151], v[0:7], v[40:47], v[148:151], v235, v235 op_sel_hi:[0,0,0]
	v_mfma_scale_f32_16x16x128_f8f6f4 v[144:147], v[8:15], v[48:55], v[144:147], v235, v235 op_sel_hi:[0,0,0]
	v_mfma_scale_f32_16x16x128_f8f6f4 v[140:143], v[0:7], v[48:55], v[140:143], v235, v235 op_sel_hi:[0,0,0]
	v_mfma_scale_f32_16x16x128_f8f6f4 v[136:139], v[8:15], v[56:63], v[136:139], v235, v235 op_sel_hi:[0,0,0]
	v_mfma_scale_f32_16x16x128_f8f6f4 v[132:135], v[0:7], v[56:63], v[132:135], v235, v235 op_sel_hi:[0,0,0]
	s_setprio 0
	s_barrier
	s_mov_b32 m0, s64
	s_add_i32 s40, s86, 0x80
	ds_read_b128 v[32:35], v232 offset:0xc000
	ds_read_b128 v[36:39], v232 offset:0xc400
	ds_read_b128 v[40:43], v232 offset:0xc800
	ds_read_b128 v[44:47], v232 offset:0xcc00
	ds_read_b128 v[48:51], v232 offset:0xd000
	ds_read_b128 v[52:55], v232 offset:0xd400
	ds_read_b128 v[56:59], v232 offset:0xd800
	ds_read_b128 v[60:63], v232 offset:0xdc00
	buffer_load_dwordx4 v231, s[8:11], s40 offen lds
	s_add_i32 s40, s86, 0x10080
	s_mov_b32 m0, s65
	s_nop 0
	buffer_load_dwordx4 v231, s[8:11], s40 offen lds
	s_add_i32 s40, s86, 0x1080
	s_mov_b32 m0, s70
	s_nop 0
	buffer_load_dwordx4 v231, s[8:11], s40 offen lds
	s_add_i32 s40, s86, 0x11080
	s_mov_b32 m0, s71
	s_nop 0
	buffer_load_dwordx4 v231, s[8:11], s40 offen lds
	s_mov_b32 m0, s68
	s_add_i32 s10, s85, 0x8080
	buffer_load_dwordx4 v230, s[4:7], s33 offen lds
	s_mov_b32 m0, s69
	s_nop 0
	buffer_load_dwordx4 v230, s[4:7], s10 offen lds
	s_waitcnt vmcnt(8)
	s_waitcnt lgkmcnt(0)
	s_barrier
	s_setprio 1
	v_mfma_scale_f32_16x16x128_f8f6f4 v[128:131], v[16:23], v[32:39], v[128:131], v235, v235 op_sel_hi:[0,0,0]
	v_mfma_scale_f32_16x16x128_f8f6f4 v[124:127], v[24:31], v[32:39], v[124:127], v235, v235 op_sel_hi:[0,0,0]
	v_mfma_scale_f32_16x16x128_f8f6f4 v[120:123], v[16:23], v[40:47], v[120:123], v235, v235 op_sel_hi:[0,0,0]
	v_mfma_scale_f32_16x16x128_f8f6f4 v[116:119], v[24:31], v[40:47], v[116:119], v235, v235 op_sel_hi:[0,0,0]
	v_mfma_scale_f32_16x16x128_f8f6f4 v[112:115], v[16:23], v[48:55], v[112:115], v235, v235 op_sel_hi:[0,0,0]
	v_mfma_scale_f32_16x16x128_f8f6f4 v[108:111], v[24:31], v[48:55], v[108:111], v235, v235 op_sel_hi:[0,0,0]
	v_mfma_scale_f32_16x16x128_f8f6f4 v[104:107], v[16:23], v[56:63], v[104:107], v235, v235 op_sel_hi:[0,0,0]
	v_mfma_scale_f32_16x16x128_f8f6f4 v[100:103], v[24:31], v[56:63], v[100:103], v235, v235 op_sel_hi:[0,0,0]
	s_setprio 0
	s_setprio 1
	v_mfma_scale_f32_16x16x128_f8f6f4 v[96:99], v[8:15], v[32:39], v[96:99], v235, v235 op_sel_hi:[0,0,0]
	v_mfma_scale_f32_16x16x128_f8f6f4 v[92:95], v[0:7], v[32:39], v[92:95], v235, v235 op_sel_hi:[0,0,0]
	v_mfma_scale_f32_16x16x128_f8f6f4 v[88:91], v[8:15], v[40:47], v[88:91], v235, v235 op_sel_hi:[0,0,0]
	v_mfma_scale_f32_16x16x128_f8f6f4 v[84:87], v[0:7], v[40:47], v[84:87], v235, v235 op_sel_hi:[0,0,0]
	v_mfma_scale_f32_16x16x128_f8f6f4 v[80:83], v[8:15], v[48:55], v[80:83], v235, v235 op_sel_hi:[0,0,0]
	v_mfma_scale_f32_16x16x128_f8f6f4 v[76:79], v[0:7], v[48:55], v[76:79], v235, v235 op_sel_hi:[0,0,0]
	v_mfma_scale_f32_16x16x128_f8f6f4 v[72:75], v[8:15], v[56:63], v[72:75], v235, v235 op_sel_hi:[0,0,0]
	v_mfma_scale_f32_16x16x128_f8f6f4 v[68:71], v[0:7], v[56:63], v[68:71], v235, v235 op_sel_hi:[0,0,0]
	s_setprio 0
	s_barrier
	s_andn2_b64 vcc, exec, s[20:21]
	s_cbranch_vccnz .LBB0_1371
	s_barrier

.LBB0_1452:
	s_add_i32 s33, s80, 0x180
	s_add_i32 s36, s81, 0x180
	s_waitcnt lgkmcnt(0)
	s_barrier
	s_setprio 1
	v_mfma_scale_f32_16x16x128_f8f6f4 v[128:131], v[24:31], v[56:63], 0, v235, v235 op_sel_hi:[0,0,0]
	v_mfma_scale_f32_16x16x128_f8f6f4 v[124:127], v[16:23], v[56:63], 0, v235, v235 op_sel_hi:[0,0,0]
	v_mfma_scale_f32_16x16x128_f8f6f4 v[120:123], v[24:31], v[48:55], 0, v235, v235 op_sel_hi:[0,0,0]
	v_mfma_scale_f32_16x16x128_f8f6f4 v[116:119], v[16:23], v[48:55], 0, v235, v235 op_sel_hi:[0,0,0]
	v_mfma_scale_f32_16x16x128_f8f6f4 v[112:115], v[24:31], v[40:47], 0, v235, v235 op_sel_hi:[0,0,0]
	v_mfma_scale_f32_16x16x128_f8f6f4 v[108:111], v[16:23], v[40:47], 0, v235, v235 op_sel_hi:[0,0,0]
	v_mfma_scale_f32_16x16x128_f8f6f4 v[104:107], v[24:31], v[32:39], 0, v235, v235 op_sel_hi:[0,0,0]
	v_mfma_scale_f32_16x16x128_f8f6f4 v[100:103], v[16:23], v[32:39], 0, v235, v235 op_sel_hi:[0,0,0]
	s_setprio 0
	s_setprio 1
	v_mfma_scale_f32_16x16x128_f8f6f4 v[96:99], v[8:15], v[56:63], 0, v235, v235 op_sel_hi:[0,0,0]
	v_mfma_scale_f32_16x16x128_f8f6f4 v[92:95], v[0:7], v[56:63], 0, v235, v235 op_sel_hi:[0,0,0]
	v_mfma_scale_f32_16x16x128_f8f6f4 v[88:91], v[8:15], v[48:55], 0, v235, v235 op_sel_hi:[0,0,0]
	v_mfma_scale_f32_16x16x128_f8f6f4 v[84:87], v[0:7], v[48:55], 0, v235, v235 op_sel_hi:[0,0,0]
	v_mfma_scale_f32_16x16x128_f8f6f4 v[80:83], v[8:15], v[40:47], 0, v235, v235 op_sel_hi:[0,0,0]
	v_mfma_scale_f32_16x16x128_f8f6f4 v[76:79], v[0:7], v[40:47], 0, v235, v235 op_sel_hi:[0,0,0]
	v_mfma_scale_f32_16x16x128_f8f6f4 v[72:75], v[8:15], v[32:39], 0, v235, v235 op_sel_hi:[0,0,0]
	v_mfma_scale_f32_16x16x128_f8f6f4 v[68:71], v[0:7], v[32:39], 0, v235, v235 op_sel_hi:[0,0,0]
	s_setprio 0
	s_barrier
	ds_read_b128 v[16:19], v233 offset:0x8000
	ds_read_b128 v[20:23], v233 offset:0x8400
	ds_read_b128 v[24:27], v233 offset:0x8800
	ds_read_b128 v[28:31], v233 offset:0x8c00
	s_mov_b32 m0, s62
	s_add_i32 s10, s80, 0x10100
	ds_read_b128 v[32:35], v232 offset:0x8000
	ds_read_b128 v[36:39], v232 offset:0x8400
	ds_read_b128 v[40:43], v232 offset:0x8800
	ds_read_b128 v[44:47], v232 offset:0x8c00
	ds_read_b128 v[48:51], v232 offset:0x9000
	ds_read_b128 v[52:55], v232 offset:0x9400
	ds_read_b128 v[56:59], v232 offset:0x9800
	ds_read_b128 v[60:63], v232 offset:0x9c00
	ds_read_b128 v[8:11], v233 offset:0xc000
	ds_read_b128 v[12:15], v233 offset:0xc400
	ds_read_b128 v[0:3], v233 offset:0xc800
	ds_read_b128 v[4:7], v233 offset:0xcc00
	buffer_load_dwordx4 v230, s[4:7], s10 offen lds
	s_add_i32 s10, s80, 0x18100
	s_mov_b32 m0, s63
	s_nop 0
	buffer_load_dwordx4 v230, s[4:7], s10 offen lds
	s_waitcnt vmcnt(8)
	s_waitcnt lgkmcnt(4)
	s_barrier
	s_setprio 1
	v_mfma_scale_f32_16x16x128_f8f6f4 v[192:195], v[16:23], v[32:39], v[192:195], v235, v235 op_sel_hi:[0,0,0]
	v_mfma_scale_f32_16x16x128_f8f6f4 v[188:191], v[24:31], v[32:39], v[188:191], v235, v235 op_sel_hi:[0,0,0]
	v_mfma_scale_f32_16x16x128_f8f6f4 v[184:187], v[16:23], v[40:47], v[184:187], v235, v235 op_sel_hi:[0,0,0]
	v_mfma_scale_f32_16x16x128_f8f6f4 v[180:183], v[24:31], v[40:47], v[180:183], v235, v235 op_sel_hi:[0,0,0]
	v_mfma_scale_f32_16x16x128_f8f6f4 v[176:179], v[16:23], v[48:55], v[176:179], v235, v235 op_sel_hi:[0,0,0]
	v_mfma_scale_f32_16x16x128_f8f6f4 v[172:175], v[24:31], v[48:55], v[172:175], v235, v235 op_sel_hi:[0,0,0]
	v_mfma_scale_f32_16x16x128_f8f6f4 v[168:171], v[16:23], v[56:63], v[168:171], v235, v235 op_sel_hi:[0,0,0]
	v_mfma_scale_f32_16x16x128_f8f6f4 v[164:167], v[24:31], v[56:63], v[164:167], v235, v235 op_sel_hi:[0,0,0]
	s_waitcnt lgkmcnt(0)
	s_setprio 0
	s_setprio 1
	v_mfma_scale_f32_16x16x128_f8f6f4 v[160:163], v[8:15], v[32:39], v[160:163], v235, v235 op_sel_hi:[0,0,0]
	v_mfma_scale_f32_16x16x128_f8f6f4 v[156:159], v[0:7], v[32:39], v[156:159], v235, v235 op_sel_hi:[0,0,0]
	v_mfma_scale_f32_16x16x128_f8f6f4 v[152:155], v[8:15], v[40:47], v[152:155], v235, v235 op_sel_hi:[0,0,0]
	v_mfma_scale_f32_16x16x128_f8f6f4 v[148:151], v[0:7], v[40:47], v[148:151], v235, v235 op_sel_hi:[0,0,0]
	v_mfma_scale_f32_16x16x128_f8f6f4 v[144:147], v[8:15], v[48:55], v[144:147], v235, v235 op_sel_hi:[0,0,0]
	v_mfma_scale_f32_16x16x128_f8f6f4 v[140:143], v[0:7], v[48:55], v[140:143], v235, v235 op_sel_hi:[0,0,0]
	v_mfma_scale_f32_16x16x128_f8f6f4 v[136:139], v[8:15], v[56:63], v[136:139], v235, v235 op_sel_hi:[0,0,0]
	v_mfma_scale_f32_16x16x128_f8f6f4 v[132:135], v[0:7], v[56:63], v[132:135], v235, v235 op_sel_hi:[0,0,0]
	s_setprio 0
	s_barrier
	s_mov_b32 m0, s64
	s_mov_b32 s10, s6
	s_mov_b32 s11, s7
	ds_read_b128 v[32:35], v232 offset:0xc000
	ds_read_b128 v[36:39], v232 offset:0xc400
	ds_read_b128 v[40:43], v232 offset:0xc800
	ds_read_b128 v[44:47], v232 offset:0xcc00
	ds_read_b128 v[48:51], v232 offset:0xd000
	ds_read_b128 v[52:55], v232 offset:0xd400
	ds_read_b128 v[56:59], v232 offset:0xd800
	ds_read_b128 v[60:63], v232 offset:0xdc00
	buffer_load_dwordx4 v231, s[8:11], s36 offen lds
	s_add_i32 s36, s81, 0x10180
	s_mov_b32 m0, s65
	s_nop 0
	buffer_load_dwordx4 v231, s[8:11], s36 offen lds
	s_add_i32 s36, s81, 0x1180
	s_mov_b32 m0, s70
	s_nop 0
	buffer_load_dwordx4 v231, s[8:11], s36 offen lds
	s_add_i32 s36, s81, 0x11180
	s_mov_b32 m0, s71
	s_nop 0
	buffer_load_dwordx4 v231, s[8:11], s36 offen lds
	s_mov_b32 m0, s68
	s_nop 0
	buffer_load_dwordx4 v230, s[4:7], s33 offen lds
	s_add_i32 s33, s80, 0x8180
	s_mov_b32 m0, s69
	s_nop 0
	buffer_load_dwordx4 v230, s[4:7], s33 offen lds
	s_waitcnt vmcnt(8)
	s_waitcnt lgkmcnt(0)
	s_barrier
	s_setprio 1
	v_mfma_scale_f32_16x16x128_f8f6f4 v[128:131], v[16:23], v[32:39], v[128:131], v235, v235 op_sel_hi:[0,0,0]
	v_mfma_scale_f32_16x16x128_f8f6f4 v[124:127], v[24:31], v[32:39], v[124:127], v235, v235 op_sel_hi:[0,0,0]
	v_mfma_scale_f32_16x16x128_f8f6f4 v[120:123], v[16:23], v[40:47], v[120:123], v235, v235 op_sel_hi:[0,0,0]
	v_mfma_scale_f32_16x16x128_f8f6f4 v[116:119], v[24:31], v[40:47], v[116:119], v235, v235 op_sel_hi:[0,0,0]
	v_mfma_scale_f32_16x16x128_f8f6f4 v[112:115], v[16:23], v[48:55], v[112:115], v235, v235 op_sel_hi:[0,0,0]
	v_mfma_scale_f32_16x16x128_f8f6f4 v[108:111], v[24:31], v[48:55], v[108:111], v235, v235 op_sel_hi:[0,0,0]
	v_mfma_scale_f32_16x16x128_f8f6f4 v[104:107], v[16:23], v[56:63], v[104:107], v235, v235 op_sel_hi:[0,0,0]
	v_mfma_scale_f32_16x16x128_f8f6f4 v[100:103], v[24:31], v[56:63], v[100:103], v235, v235 op_sel_hi:[0,0,0]
	s_setprio 0
	s_setprio 1
	v_mfma_scale_f32_16x16x128_f8f6f4 v[96:99], v[8:15], v[32:39], v[96:99], v235, v235 op_sel_hi:[0,0,0]
	v_mfma_scale_f32_16x16x128_f8f6f4 v[92:95], v[0:7], v[32:39], v[92:95], v235, v235 op_sel_hi:[0,0,0]
	v_mfma_scale_f32_16x16x128_f8f6f4 v[88:91], v[8:15], v[40:47], v[88:91], v235, v235 op_sel_hi:[0,0,0]
	v_mfma_scale_f32_16x16x128_f8f6f4 v[84:87], v[0:7], v[40:47], v[84:87], v235, v235 op_sel_hi:[0,0,0]
	v_mfma_scale_f32_16x16x128_f8f6f4 v[80:83], v[8:15], v[48:55], v[80:83], v235, v235 op_sel_hi:[0,0,0]
	v_mfma_scale_f32_16x16x128_f8f6f4 v[76:79], v[0:7], v[48:55], v[76:79], v235, v235 op_sel_hi:[0,0,0]
	v_mfma_scale_f32_16x16x128_f8f6f4 v[72:75], v[8:15], v[56:63], v[72:75], v235, v235 op_sel_hi:[0,0,0]
	v_mfma_scale_f32_16x16x128_f8f6f4 v[68:71], v[0:7], v[56:63], v[68:71], v235, v235 op_sel_hi:[0,0,0]
	s_setprio 0
	s_barrier
	ds_read_b128 v[16:19], v233 offset:0
	ds_read_b128 v[20:23], v233 offset:0x400
	ds_read_b128 v[24:27], v233 offset:0x800
	ds_read_b128 v[28:31], v233 offset:0xc00
	s_add_i32 s33, s43, 0x80
	s_mov_b32 m0, s74
	s_add_i32 s36, s80, 0x10180
	ds_read_b128 v[32:35], v232 offset:0
	ds_read_b128 v[36:39], v232 offset:0x400
	ds_read_b128 v[40:43], v232 offset:0x800
	ds_read_b128 v[44:47], v232 offset:0xc00
	ds_read_b128 v[48:51], v232 offset:0x1000
	ds_read_b128 v[52:55], v232 offset:0x1400
	ds_read_b128 v[56:59], v232 offset:0x1800
	ds_read_b128 v[60:63], v232 offset:0x1c00
	ds_read_b128 v[8:11], v233 offset:0x4000
	ds_read_b128 v[12:15], v233 offset:0x4400
	ds_read_b128 v[0:3], v233 offset:0x4800
	ds_read_b128 v[4:7], v233 offset:0x4c00
	buffer_load_dwordx4 v230, s[4:7], s36 offen lds
	s_add_i32 s36, s80, 0x18180
	s_mov_b32 m0, s76
	s_nop 0
	buffer_load_dwordx4 v230, s[4:7], s36 offen lds
	s_waitcnt vmcnt(8)
	s_waitcnt lgkmcnt(4)
	s_barrier
	s_setprio 1
	v_mfma_scale_f32_16x16x128_f8f6f4 v[192:195], v[16:23], v[32:39], v[192:195], v235, v235 op_sel_hi:[0,0,0]
	v_mfma_scale_f32_16x16x128_f8f6f4 v[188:191], v[24:31], v[32:39], v[188:191], v235, v235 op_sel_hi:[0,0,0]
	v_mfma_scale_f32_16x16x128_f8f6f4 v[184:187], v[16:23], v[40:47], v[184:187], v235, v235 op_sel_hi:[0,0,0]
	v_mfma_scale_f32_16x16x128_f8f6f4 v[180:183], v[24:31], v[40:47], v[180:183], v235, v235 op_sel_hi:[0,0,0]
	v_mfma_scale_f32_16x16x128_f8f6f4 v[176:179], v[16:23], v[48:55], v[176:179], v235, v235 op_sel_hi:[0,0,0]
	v_mfma_scale_f32_16x16x128_f8f6f4 v[172:175], v[24:31], v[48:55], v[172:175], v235, v235 op_sel_hi:[0,0,0]
	v_mfma_scale_f32_16x16x128_f8f6f4 v[168:171], v[16:23], v[56:63], v[168:171], v235, v235 op_sel_hi:[0,0,0]
	v_mfma_scale_f32_16x16x128_f8f6f4 v[164:167], v[24:31], v[56:63], v[164:167], v235, v235 op_sel_hi:[0,0,0]
	s_waitcnt lgkmcnt(0)
	s_setprio 0
	s_setprio 1
	v_mfma_scale_f32_16x16x128_f8f6f4 v[160:163], v[8:15], v[32:39], v[160:163], v235, v235 op_sel_hi:[0,0,0]
	v_mfma_scale_f32_16x16x128_f8f6f4 v[156:159], v[0:7], v[32:39], v[156:159], v235, v235 op_sel_hi:[0,0,0]
	v_mfma_scale_f32_16x16x128_f8f6f4 v[152:155], v[8:15], v[40:47], v[152:155], v235, v235 op_sel_hi:[0,0,0]
	v_mfma_scale_f32_16x16x128_f8f6f4 v[148:151], v[0:7], v[40:47], v[148:151], v235, v235 op_sel_hi:[0,0,0]
	v_mfma_scale_f32_16x16x128_f8f6f4 v[144:147], v[8:15], v[48:55], v[144:147], v235, v235 op_sel_hi:[0,0,0]
	v_mfma_scale_f32_16x16x128_f8f6f4 v[140:143], v[0:7], v[48:55], v[140:143], v235, v235 op_sel_hi:[0,0,0]
	v_mfma_scale_f32_16x16x128_f8f6f4 v[136:139], v[8:15], v[56:63], v[136:139], v235, v235 op_sel_hi:[0,0,0]
	v_mfma_scale_f32_16x16x128_f8f6f4 v[132:135], v[0:7], v[56:63], v[132:135], v235, v235 op_sel_hi:[0,0,0]
	s_setprio 0
	s_barrier
	s_mov_b32 m0, s46
	ds_read_b128 v[32:35], v232 offset:0x4000
	ds_read_b128 v[36:39], v232 offset:0x4400
	ds_read_b128 v[40:43], v232 offset:0x4800
	ds_read_b128 v[44:47], v232 offset:0x4c00
	ds_read_b128 v[48:51], v232 offset:0x5000
	ds_read_b128 v[52:55], v232 offset:0x5400
	ds_read_b128 v[56:59], v232 offset:0x5800
	ds_read_b128 v[60:63], v232 offset:0x5c00
	s_nop 0
	buffer_load_dwordx4 v231, s[8:11], s78 offen lds
	s_add_i32 s36, s78, 0x10000
	s_mov_b32 m0, s47
	s_nop 0
	buffer_load_dwordx4 v231, s[8:11], s36 offen lds
	s_add_i32 s36, s78, 0x1000
	s_mov_b32 m0, s49
	s_nop 0
	buffer_load_dwordx4 v231, s[8:11], s36 offen lds
	s_add_i32 s36, s78, 0x11000
	s_mov_b32 m0, s50
	s_nop 0
	buffer_load_dwordx4 v231, s[8:11], s36 offen lds
	s_mov_b32 m0, s48
	s_add_i32 s36, s43, 0x8000
	buffer_load_dwordx4 v230, s[4:7], s43 offen lds
	s_mov_b32 m0, s51
	s_nop 0
	buffer_load_dwordx4 v230, s[4:7], s36 offen lds
	s_waitcnt vmcnt(8)
	s_waitcnt lgkmcnt(0)
	s_barrier
	s_setprio 1
	v_mfma_scale_f32_16x16x128_f8f6f4 v[128:131], v[16:23], v[32:39], v[128:131], v235, v235 op_sel_hi:[0,0,0]
	v_mfma_scale_f32_16x16x128_f8f6f4 v[124:127], v[24:31], v[32:39], v[124:127], v235, v235 op_sel_hi:[0,0,0]
	v_mfma_scale_f32_16x16x128_f8f6f4 v[120:123], v[16:23], v[40:47], v[120:123], v235, v235 op_sel_hi:[0,0,0]
	v_mfma_scale_f32_16x16x128_f8f6f4 v[116:119], v[24:31], v[40:47], v[116:119], v235, v235 op_sel_hi:[0,0,0]
	v_mfma_scale_f32_16x16x128_f8f6f4 v[112:115], v[16:23], v[48:55], v[112:115], v235, v235 op_sel_hi:[0,0,0]
	v_mfma_scale_f32_16x16x128_f8f6f4 v[108:111], v[24:31], v[48:55], v[108:111], v235, v235 op_sel_hi:[0,0,0]
	v_mfma_scale_f32_16x16x128_f8f6f4 v[104:107], v[16:23], v[56:63], v[104:107], v235, v235 op_sel_hi:[0,0,0]
	v_mfma_scale_f32_16x16x128_f8f6f4 v[100:103], v[24:31], v[56:63], v[100:103], v235, v235 op_sel_hi:[0,0,0]
	s_setprio 0
	s_setprio 1
	v_mfma_scale_f32_16x16x128_f8f6f4 v[96:99], v[8:15], v[32:39], v[96:99], v235, v235 op_sel_hi:[0,0,0]
	v_mfma_scale_f32_16x16x128_f8f6f4 v[92:95], v[0:7], v[32:39], v[92:95], v235, v235 op_sel_hi:[0,0,0]
	v_mfma_scale_f32_16x16x128_f8f6f4 v[88:91], v[8:15], v[40:47], v[88:91], v235, v235 op_sel_hi:[0,0,0]
	v_mfma_scale_f32_16x16x128_f8f6f4 v[84:87], v[0:7], v[40:47], v[84:87], v235, v235 op_sel_hi:[0,0,0]
	v_mfma_scale_f32_16x16x128_f8f6f4 v[80:83], v[8:15], v[48:55], v[80:83], v235, v235 op_sel_hi:[0,0,0]
	v_mfma_scale_f32_16x16x128_f8f6f4 v[76:79], v[0:7], v[48:55], v[76:79], v235, v235 op_sel_hi:[0,0,0]
	v_mfma_scale_f32_16x16x128_f8f6f4 v[72:75], v[8:15], v[56:63], v[72:75], v235, v235 op_sel_hi:[0,0,0]
	v_mfma_scale_f32_16x16x128_f8f6f4 v[68:71], v[0:7], v[56:63], v[68:71], v235, v235 op_sel_hi:[0,0,0]
	s_setprio 0
	s_barrier
	ds_read_b128 v[16:19], v233 offset:0x8000
	ds_read_b128 v[20:23], v233 offset:0x8400
	ds_read_b128 v[24:27], v233 offset:0x8800
	ds_read_b128 v[28:31], v233 offset:0x8c00
	s_mov_b32 m0, s62
	s_add_i32 s36, s43, 0x10000
	ds_read_b128 v[32:35], v232 offset:0x8000
	ds_read_b128 v[36:39], v232 offset:0x8400
	ds_read_b128 v[40:43], v232 offset:0x8800
	ds_read_b128 v[44:47], v232 offset:0x8c00
	ds_read_b128 v[48:51], v232 offset:0x9000
	ds_read_b128 v[52:55], v232 offset:0x9400
	ds_read_b128 v[56:59], v232 offset:0x9800
	ds_read_b128 v[60:63], v232 offset:0x9c00
	ds_read_b128 v[8:11], v233 offset:0xc000
	ds_read_b128 v[12:15], v233 offset:0xc400
	ds_read_b128 v[0:3], v233 offset:0xc800
	ds_read_b128 v[4:7], v233 offset:0xcc00
	buffer_load_dwordx4 v230, s[4:7], s36 offen lds
	s_add_i32 s36, s43, 0x18000
	s_mov_b32 m0, s63
	s_nop 0
	buffer_load_dwordx4 v230, s[4:7], s36 offen lds
	s_waitcnt vmcnt(8)
	s_waitcnt lgkmcnt(4)
	s_barrier
	s_setprio 1
	v_mfma_scale_f32_16x16x128_f8f6f4 v[192:195], v[16:23], v[32:39], v[192:195], v235, v235 op_sel_hi:[0,0,0]
	v_mfma_scale_f32_16x16x128_f8f6f4 v[188:191], v[24:31], v[32:39], v[188:191], v235, v235 op_sel_hi:[0,0,0]
	v_mfma_scale_f32_16x16x128_f8f6f4 v[184:187], v[16:23], v[40:47], v[184:187], v235, v235 op_sel_hi:[0,0,0]
	v_mfma_scale_f32_16x16x128_f8f6f4 v[180:183], v[24:31], v[40:47], v[180:183], v235, v235 op_sel_hi:[0,0,0]
	v_mfma_scale_f32_16x16x128_f8f6f4 v[176:179], v[16:23], v[48:55], v[176:179], v235, v235 op_sel_hi:[0,0,0]
	v_mfma_scale_f32_16x16x128_f8f6f4 v[172:175], v[24:31], v[48:55], v[172:175], v235, v235 op_sel_hi:[0,0,0]
	v_mfma_scale_f32_16x16x128_f8f6f4 v[168:171], v[16:23], v[56:63], v[168:171], v235, v235 op_sel_hi:[0,0,0]
	v_mfma_scale_f32_16x16x128_f8f6f4 v[164:167], v[24:31], v[56:63], v[164:167], v235, v235 op_sel_hi:[0,0,0]
	s_waitcnt lgkmcnt(0)
	s_setprio 0
	s_setprio 1
	v_mfma_scale_f32_16x16x128_f8f6f4 v[160:163], v[8:15], v[32:39], v[160:163], v235, v235 op_sel_hi:[0,0,0]
	v_mfma_scale_f32_16x16x128_f8f6f4 v[156:159], v[0:7], v[32:39], v[156:159], v235, v235 op_sel_hi:[0,0,0]
	v_mfma_scale_f32_16x16x128_f8f6f4 v[152:155], v[8:15], v[40:47], v[152:155], v235, v235 op_sel_hi:[0,0,0]
	v_mfma_scale_f32_16x16x128_f8f6f4 v[148:151], v[0:7], v[40:47], v[148:151], v235, v235 op_sel_hi:[0,0,0]
	v_mfma_scale_f32_16x16x128_f8f6f4 v[144:147], v[8:15], v[48:55], v[144:147], v235, v235 op_sel_hi:[0,0,0]
	v_mfma_scale_f32_16x16x128_f8f6f4 v[140:143], v[0:7], v[48:55], v[140:143], v235, v235 op_sel_hi:[0,0,0]
	v_mfma_scale_f32_16x16x128_f8f6f4 v[136:139], v[8:15], v[56:63], v[136:139], v235, v235 op_sel_hi:[0,0,0]
	v_mfma_scale_f32_16x16x128_f8f6f4 v[132:135], v[0:7], v[56:63], v[132:135], v235, v235 op_sel_hi:[0,0,0]
	s_setprio 0
	s_barrier
	s_mov_b32 m0, s64
	s_add_i32 s36, s78, 0x80
	ds_read_b128 v[32:35], v232 offset:0xc000
	ds_read_b128 v[36:39], v232 offset:0xc400
	ds_read_b128 v[40:43], v232 offset:0xc800
	ds_read_b128 v[44:47], v232 offset:0xcc00
	ds_read_b128 v[48:51], v232 offset:0xd000
	ds_read_b128 v[52:55], v232 offset:0xd400
	ds_read_b128 v[56:59], v232 offset:0xd800
	ds_read_b128 v[60:63], v232 offset:0xdc00
	buffer_load_dwordx4 v231, s[8:11], s36 offen lds
	s_add_i32 s36, s78, 0x10080
	s_mov_b32 m0, s65
	s_nop 0
	buffer_load_dwordx4 v231, s[8:11], s36 offen lds
	s_add_i32 s36, s78, 0x1080
	s_mov_b32 m0, s70
	s_nop 0
	buffer_load_dwordx4 v231, s[8:11], s36 offen lds
	s_add_i32 s36, s78, 0x11080
	s_mov_b32 m0, s71
	s_nop 0
	buffer_load_dwordx4 v231, s[8:11], s36 offen lds
	s_mov_b32 m0, s68
	s_add_i32 s10, s43, 0x8080
	buffer_load_dwordx4 v230, s[4:7], s33 offen lds
	s_mov_b32 m0, s69
	s_nop 0
	buffer_load_dwordx4 v230, s[4:7], s10 offen lds
	s_waitcnt vmcnt(8)
	s_waitcnt lgkmcnt(0)
	s_barrier
	s_setprio 1
	v_mfma_scale_f32_16x16x128_f8f6f4 v[128:131], v[16:23], v[32:39], v[128:131], v235, v235 op_sel_hi:[0,0,0]
	v_mfma_scale_f32_16x16x128_f8f6f4 v[124:127], v[24:31], v[32:39], v[124:127], v235, v235 op_sel_hi:[0,0,0]
	v_mfma_scale_f32_16x16x128_f8f6f4 v[120:123], v[16:23], v[40:47], v[120:123], v235, v235 op_sel_hi:[0,0,0]
	v_mfma_scale_f32_16x16x128_f8f6f4 v[116:119], v[24:31], v[40:47], v[116:119], v235, v235 op_sel_hi:[0,0,0]
	v_mfma_scale_f32_16x16x128_f8f6f4 v[112:115], v[16:23], v[48:55], v[112:115], v235, v235 op_sel_hi:[0,0,0]
	v_mfma_scale_f32_16x16x128_f8f6f4 v[108:111], v[24:31], v[48:55], v[108:111], v235, v235 op_sel_hi:[0,0,0]
	v_mfma_scale_f32_16x16x128_f8f6f4 v[104:107], v[16:23], v[56:63], v[104:107], v235, v235 op_sel_hi:[0,0,0]
	v_mfma_scale_f32_16x16x128_f8f6f4 v[100:103], v[24:31], v[56:63], v[100:103], v235, v235 op_sel_hi:[0,0,0]
	s_setprio 0
	s_setprio 1
	v_mfma_scale_f32_16x16x128_f8f6f4 v[96:99], v[8:15], v[32:39], v[96:99], v235, v235 op_sel_hi:[0,0,0]
	v_mfma_scale_f32_16x16x128_f8f6f4 v[92:95], v[0:7], v[32:39], v[92:95], v235, v235 op_sel_hi:[0,0,0]
	v_mfma_scale_f32_16x16x128_f8f6f4 v[88:91], v[8:15], v[40:47], v[88:91], v235, v235 op_sel_hi:[0,0,0]
	v_mfma_scale_f32_16x16x128_f8f6f4 v[84:87], v[0:7], v[40:47], v[84:87], v235, v235 op_sel_hi:[0,0,0]
	v_mfma_scale_f32_16x16x128_f8f6f4 v[80:83], v[8:15], v[48:55], v[80:83], v235, v235 op_sel_hi:[0,0,0]
	v_mfma_scale_f32_16x16x128_f8f6f4 v[76:79], v[0:7], v[48:55], v[76:79], v235, v235 op_sel_hi:[0,0,0]
	v_mfma_scale_f32_16x16x128_f8f6f4 v[72:75], v[8:15], v[56:63], v[72:75], v235, v235 op_sel_hi:[0,0,0]
	v_mfma_scale_f32_16x16x128_f8f6f4 v[68:71], v[0:7], v[56:63], v[68:71], v235, v235 op_sel_hi:[0,0,0]
	s_setprio 0
	s_barrier
	s_andn2_b64 vcc, exec, s[20:21]
	s_cbranch_vccnz .LBB0_1454
	s_barrier
